# ring GEMM + write-through (sc1) hs/csr-segment stores + sc1 on W-image loads
# speedup vs baseline: 1.0060x; 1.0060x over previous
.LBB1_226:
	ds_read_b128 v[6:9], v2
	v_add_u32_e32 v0, 0x100, v0
	v_cmp_le_i32_e32 vcc, s4, v0
	v_add_u32_e32 v2, 0x1000, v2
	s_or_b64 s[0:1], vcc, s[0:1]
	s_waitcnt lgkmcnt(0)
	global_store_dwordx4 v[4:5], v[6:9], off sc1
	v_lshl_add_u64 v[4:5], v[4:5], 0, s[2:3]
	s_andn2_b64 exec, exec, s[0:1]
	s_cbranch_execnz .LBB1_226

_Z6k_gemmPKfPKDv8_DF16_S0_S0_PDF16_:
	s_load_dwordx2 s[8:9], s[0:1], 0x0
	s_load_dwordx2 s[10:11], s[0:1], 0x10
	s_load_dwordx2 s[12:13], s[0:1], 0x8
	s_load_dwordx4 s[4:7], s[0:1], 0x18
	s_mul_i32 s14, s2, 0xc4
	v_lshrrev_b32_e32 v1, 5, v0
	v_and_b32_e32 v89, 31, v0
	v_add_u32_e32 v2, s14, v1
	v_lshlrev_b32_e32 v154, 4, v89
	s_movk_i32 s15, 0x1664
	v_mad_u64_u32 v[150:151], s[0:1], v2, s15, v[154:155]
	s_lshl_b32 s16, s2, 2
	v_mul_u32_u24_e32 v245, 25, v1
	v_add_u32_e32 v245, s16, v245
	v_and_b32_e32 v245, 31, v245
	v_xor_b32_e32 v246, 16, v245
	v_lshlrev_b32_e32 v247, 2, v246
	v_sub_u32_e32 v244, v150, v247
	v_lshlrev_b32_e32 v247, 2, v245
	v_sub_u32_e32 v150, v150, v247
	s_movk_i32 s17, 0x1ee0
	v_mul_u32_u24_e32 v242, s17, v1
	v_add_u32_e32 v243, 0xffffff00, v242
	v_lshl_add_u32 v247, v89, 3, v242
	v_lshlrev_b32_e32 v248, 1, v245
	v_sub_u32_e32 v248, v247, v248
	v_add_u32_e32 v234, 64, v248
	v_add_u32_e32 v235, 0x42, v248
	v_add_u32_e32 v236, 0x44, v248
	v_add_u32_e32 v237, 0x46, v248
	v_lshlrev_b32_e32 v248, 1, v246
	v_sub_u32_e32 v248, v247, v248
	v_add_u32_e32 v238, 64, v248
	v_add_u32_e32 v239, 0x42, v248
	v_add_u32_e32 v240, 0x44, v248
	v_add_u32_e32 v241, 0x46, v248
	v_and_b32_e32 v247, 7, v89
	v_lshl_add_u32 v247, v247, 3, v242
	v_mov_b32_e32 v248, 0
	v_mov_b32_e32 v249, 0
	ds_write_b64 v247, v[248:249] offset:0
	ds_write_b64 v247, v[248:249] offset:608
	ds_write_b64 v247, v[248:249] offset:1216
	ds_write_b64 v247, v[248:249] offset:1824
	ds_write_b64 v247, v[248:249] offset:2432
	ds_write_b64 v247, v[248:249] offset:3040
	ds_write_b64 v247, v[248:249] offset:3648
	ds_write_b64 v247, v[248:249] offset:4256
	ds_write_b64 v247, v[248:249] offset:4864
	ds_write_b64 v247, v[248:249] offset:5472
	ds_write_b64 v247, v[248:249] offset:6080
	ds_write_b64 v247, v[248:249] offset:6688
	ds_write_b64 v247, v[248:249] offset:7296
	v_mov_b32_e32 v2, 2
	v_lshlrev_b32_sdwa v2, v2, v0 dst_sel:DWORD dst_unused:UNUSED_PAD src0_sel:DWORD src1_sel:BYTE_0
	v_mov_b32_e32 v3, 0
	s_waitcnt lgkmcnt(0)
	v_lshl_add_u64 v[4:5], s[4:5], 0, v[2:3]
	s_mov_b32 s0, 0x166000
	v_add_co_u32_e32 v4, vcc, s0, v4
	v_add_u32_e32 v6, 0x111514dc, v154
	s_nop 0
	v_addc_co_u32_e32 v5, vcc, 0, v5, vcc
	global_load_dword v90, v[4:5], off
	v_add_u32_e32 v4, 0x16640, v244
	v_min_u32_e32 v2, v150, v6
	v_min_u32_e32 v4, v4, v6
	global_load_dwordx4 v[82:85], v2, s[8:9] nt
	global_load_dwordx4 v[78:81], v4, s[8:9] nt
	v_add_u32_e32 v2, 0x2cc80, v150
	v_min_u32_e32 v2, v2, v6
	v_add_u32_e32 v4, 0x432c0, v244
	v_min_u32_e32 v4, v4, v6
	global_load_dwordx4 v[74:77], v2, s[8:9] nt
	global_load_dwordx4 v[70:73], v4, s[8:9] nt
	v_add_u32_e32 v2, 0x59900, v150
	v_min_u32_e32 v2, v2, v6
	v_add_u32_e32 v4, 0x6ff40, v244
	v_min_u32_e32 v4, v4, v6
	global_load_dwordx4 v[66:69], v2, s[8:9] nt
	global_load_dwordx4 v[54:57], v4, s[8:9] nt
	v_add_u32_e32 v2, 0x86580, v150
	v_min_u32_e32 v2, v2, v6
	v_add_u32_e32 v4, 0x9cbc0, v244
	v_min_u32_e32 v4, v4, v6
	global_load_dwordx4 v[62:65], v2, s[8:9] nt
	global_load_dwordx4 v[58:61], v4, s[8:9] nt
	v_add_u32_e32 v2, 0xb3200, v150
	v_min_u32_e32 v2, v2, v6
	v_add_u32_e32 v4, 0xc9840, v244
	v_min_u32_e32 v4, v4, v6
	global_load_dwordx4 v[46:49], v2, s[8:9] nt
	global_load_dwordx4 v[38:41], v4, s[8:9] nt
	v_add_u32_e32 v2, 0xdfe80, v150
	v_min_u32_e32 v2, v2, v6
	v_add_u32_e32 v4, 0xf64c0, v244
	s_movk_i32 s3, 0xc4
	v_or_b32_e32 v7, 0xc0, v1
	v_min_u32_e32 v4, v4, v6
	global_load_dwordx4 v[34:37], v2, s[8:9] nt
	global_load_dwordx4 v[14:17], v4, s[8:9] nt
	v_add_u32_e32 v2, 0x10cb00, v150
	v_min_u32_e32 v2, v2, v6
	v_cmp_gt_u32_e64 s[0:1], s3, v7
	v_bfe_u32 v87, v0, 4, 2
	v_and_b32_e32 v86, 15, v0
	v_cndmask_b32_e64 v2, 0, v2, s[0:1]
	global_load_dwordx4 v[10:13], v2, s[8:9] nt
	v_lshlrev_b32_e32 v2, 12, v87
	v_lshl_add_u64 v[4:5], s[12:13], 0, v[2:3]
	v_lshlrev_b32_e32 v2, 3, v0
	v_and_b32_e32 v2, 0xe00, v2
	v_lshl_add_u64 v[4:5], v[4:5], 0, v[2:3]
	v_lshlrev_b32_e32 v2, 4, v86
	v_lshl_add_u64 v[152:153], v[4:5], 0, v[2:3]
	s_movk_i32 s2, 0x4000
	v_add_co_u32_e32 v2, vcc, s2, v152
	s_mov_b32 s2, 0x8000
	s_nop 0
	v_addc_co_u32_e32 v3, vcc, 0, v153, vcc
	global_load_dwordx4 v[26:29], v[152:153], off sc1
	global_load_dwordx4 v[50:53], v[152:153], off offset:256 sc1
	global_load_dwordx4 v[18:21], v[2:3], off sc1
	global_load_dwordx4 v[42:45], v[2:3], off offset:256 sc1
	v_add_co_u32_e32 v2, vcc, s2, v152
	s_movk_i32 s2, 0xd0
	s_nop 0
	v_addc_co_u32_e32 v3, vcc, 0, v153, vcc
	v_add_co_u32_e32 v92, vcc, 0xc000, v152
	global_load_dwordx4 v[22:25], v[2:3], off sc1
	global_load_dwordx4 v[30:33], v[2:3], off offset:256 sc1
	v_addc_co_u32_e32 v93, vcc, 0, v153, vcc
	global_load_dwordx4 v[6:9], v[92:93], off sc1
	global_load_dwordx4 v[2:5], v[92:93], off offset:256 sc1
	v_cmp_gt_u32_e32 vcc, s2, v0
	v_add_u32_e32 v88, 0x111516dc, v154
	s_and_saveexec_b64 s[4:5], vcc
	s_cbranch_execz .LBB2_5
	v_cndmask_b32_e32 v91, 0, v0, vcc
	v_cmp_gt_u32_e32 vcc, s3, v91
	v_add_u32_e32 v91, s14, v91
	s_mov_b32 s2, 0xc350
	v_cmp_gt_i32_e64 s[2:3], s2, v91
	v_ashrrev_i32_e32 v92, 31, v91
	s_and_b64 s[2:3], vcc, s[2:3]
	v_cndmask_b32_e64 v93, 0, v92, s[2:3]
	v_mov_b32_e32 v92, 0xc34f
	v_cndmask_b32_e64 v92, v92, v91, s[2:3]
	v_mov_b64_e32 v[94:95], s[8:9]
	v_mad_i64_i32 v[94:95], s[12:13], v92, s15, v[94:95]
	v_add_co_u32_e32 v94, vcc, 0x1000, v94
	v_lshl_add_u64 v[92:93], v[92:93], 2, s[10:11]
	s_nop 0
	v_addc_co_u32_e32 v95, vcc, 0, v95, vcc
	global_load_dword v91, v[92:93], off
	global_load_dword v96, v[94:95], off offset:1632
	v_mov_b32_e32 v94, 0x1ee00
	s_waitcnt vmcnt(1)
	v_cndmask_b32_e64 v93, 0, v91, s[2:3]
	s_waitcnt vmcnt(0)
	v_cndmask_b32_e64 v92, 0, v96, s[2:3]
	v_lshl_add_u32 v91, v0, 3, v94
	ds_write_b64 v91, v[92:93]

.LBB2_7:
	s_or_b64 exec, exec, s[2:3]
	s_waitcnt vmcnt(21)
	v_add_u32_e32 v90, 0x200, v150
	v_min_u32_e32 v90, v90, v88
	global_load_dwordx4 v[110:113], v90, s[8:9] nt
	v_mul_u32_u24_e32 v1, 0x120, v1
	s_waitcnt vmcnt(21)
	v_cvt_pk_f16_f32 v85, v84, v85
	v_cvt_pk_f16_f32 v84, v82, v83
	v_lshl_add_u32 v1, v89, 3, v1
	s_movk_i32 s2, 0x120
	ds_write_b16 v234, v84 offset:0
	ds_write_b16_d16_hi v235, v84 offset:0
	ds_write_b16 v236, v85 offset:0
	ds_write_b16_d16_hi v237, v85 offset:0
	v_add_u32_e32 v82, 0x16840, v244
	v_min_u32_e32 v82, v82, v88
	global_load_dwordx4 v[114:117], v82, s[8:9] nt
	s_waitcnt vmcnt(21)
	v_cvt_pk_f16_f32 v81, v80, v81
	v_cvt_pk_f16_f32 v80, v78, v79
	ds_write_b16 v238, v80 offset:608
	ds_write_b16_d16_hi v239, v80 offset:608
	ds_write_b16 v240, v81 offset:608
	ds_write_b16_d16_hi v241, v81 offset:608
	v_add_u32_e32 v78, 0x2ce80, v150
	v_min_u32_e32 v78, v78, v88
	global_load_dwordx4 v[118:121], v78, s[8:9] nt
	s_waitcnt vmcnt(21)
	v_cvt_pk_f16_f32 v77, v76, v77
	v_cvt_pk_f16_f32 v76, v74, v75
	ds_write_b16 v234, v76 offset:1216
	ds_write_b16_d16_hi v235, v76 offset:1216
	ds_write_b16 v236, v77 offset:1216
	ds_write_b16_d16_hi v237, v77 offset:1216
	v_add_u32_e32 v74, 0x434c0, v244
	v_min_u32_e32 v74, v74, v88
	global_load_dwordx4 v[74:77], v74, s[8:9] nt
	s_waitcnt vmcnt(21)
	v_cvt_pk_f16_f32 v73, v72, v73
	v_cvt_pk_f16_f32 v72, v70, v71
	ds_write_b16 v238, v72 offset:1824
	ds_write_b16_d16_hi v239, v72 offset:1824
	ds_write_b16 v240, v73 offset:1824
	ds_write_b16_d16_hi v241, v73 offset:1824
	v_add_u32_e32 v70, 0x59b00, v150
	v_min_u32_e32 v70, v70, v88
	global_load_dwordx4 v[78:81], v70, s[8:9] nt
	s_waitcnt vmcnt(21)
	v_cvt_pk_f16_f32 v69, v68, v69
	v_cvt_pk_f16_f32 v68, v66, v67
	ds_write_b16 v234, v68 offset:2432
	ds_write_b16_d16_hi v235, v68 offset:2432
	ds_write_b16 v236, v69 offset:2432
	ds_write_b16_d16_hi v237, v69 offset:2432
	v_add_u32_e32 v66, 0x70140, v244
	v_min_u32_e32 v66, v66, v88
	global_load_dwordx4 v[82:85], v66, s[8:9] nt
	s_waitcnt vmcnt(21)
	v_cvt_pk_f16_f32 v57, v56, v57
	v_cvt_pk_f16_f32 v56, v54, v55
	ds_write_b16 v238, v56 offset:3040
	ds_write_b16_d16_hi v239, v56 offset:3040
	ds_write_b16 v240, v57 offset:3040
	ds_write_b16_d16_hi v241, v57 offset:3040
	v_add_u32_e32 v54, 0x86780, v150
	v_min_u32_e32 v54, v54, v88
	global_load_dwordx4 v[54:57], v54, s[8:9] nt
	s_waitcnt vmcnt(21)
	v_cvt_pk_f16_f32 v65, v64, v65
	v_cvt_pk_f16_f32 v64, v62, v63
	ds_write_b16 v234, v64 offset:3648
	ds_write_b16_d16_hi v235, v64 offset:3648
	ds_write_b16 v236, v65 offset:3648
	ds_write_b16_d16_hi v237, v65 offset:3648
	v_add_u32_e32 v62, 0x9cdc0, v244
	v_min_u32_e32 v62, v62, v88
	global_load_dwordx4 v[90:93], v62, s[8:9] nt
	s_waitcnt vmcnt(21)
	v_cvt_pk_f16_f32 v61, v60, v61
	v_cvt_pk_f16_f32 v60, v58, v59
	ds_write_b16 v238, v60 offset:4256
	ds_write_b16_d16_hi v239, v60 offset:4256
	ds_write_b16 v240, v61 offset:4256
	ds_write_b16_d16_hi v241, v61 offset:4256
	v_add_u32_e32 v58, 0xb3400, v150
	v_min_u32_e32 v58, v58, v88
	global_load_dwordx4 v[94:97], v58, s[8:9] nt
	s_waitcnt vmcnt(21)
	v_cvt_pk_f16_f32 v49, v48, v49
	v_cvt_pk_f16_f32 v48, v46, v47
	ds_write_b16 v234, v48 offset:4864
	ds_write_b16_d16_hi v235, v48 offset:4864
	ds_write_b16 v236, v49 offset:4864
	ds_write_b16_d16_hi v237, v49 offset:4864
	v_add_u32_e32 v46, 0xc9a40, v244
	v_min_u32_e32 v46, v46, v88
	global_load_dwordx4 v[98:101], v46, s[8:9] nt
	s_waitcnt vmcnt(21)
	v_cvt_pk_f16_f32 v41, v40, v41
	v_cvt_pk_f16_f32 v40, v38, v39
	ds_write_b16 v238, v40 offset:5472
	ds_write_b16_d16_hi v239, v40 offset:5472
	ds_write_b16 v240, v41 offset:5472
	ds_write_b16_d16_hi v241, v41 offset:5472
	v_add_u32_e32 v38, 0xe0080, v150
	v_min_u32_e32 v38, v38, v88
	global_load_dwordx4 v[102:105], v38, s[8:9] nt
	s_waitcnt vmcnt(21)
	v_cvt_pk_f16_f32 v37, v36, v37
	v_cvt_pk_f16_f32 v36, v34, v35
	ds_write_b16 v234, v36 offset:6080
	ds_write_b16_d16_hi v235, v36 offset:6080
	ds_write_b16 v236, v37 offset:6080
	ds_write_b16_d16_hi v237, v37 offset:6080
	v_add_u32_e32 v34, 0xf66c0, v244
	v_min_u32_e32 v34, v34, v88
	global_load_dwordx4 v[106:109], v34, s[8:9] nt
	s_waitcnt vmcnt(21)
	v_cvt_pk_f16_f32 v17, v16, v17
	v_cvt_pk_f16_f32 v16, v14, v15
	ds_write_b16 v238, v16 offset:6688
	ds_write_b16_d16_hi v239, v16 offset:6688
	ds_write_b16 v240, v17 offset:6688
	ds_write_b16_d16_hi v241, v17 offset:6688
	v_add_u32_e32 v14, 0x10cd00, v150
	v_min_u32_e32 v14, v14, v88
	v_cndmask_b32_e64 v14, 0, v14, s[0:1]
	global_load_dwordx4 v[46:49], v14, s[8:9] nt
	s_waitcnt vmcnt(21)
	v_cvt_pk_f16_f32 v13, v12, v13
	v_cvt_pk_f16_f32 v12, v10, v11
	ds_write_b16 v234, v12 offset:7296
	ds_write_b16_d16_hi v235, v12 offset:7296
	ds_write_b16 v236, v13 offset:7296
	ds_write_b16_d16_hi v237, v13 offset:7296
	s_waitcnt lgkmcnt(0)
	s_barrier
	v_sub_u32_e32 v245, v234, v243
	v_add_u32_e32 v246, 0xfffffdc0, v245
	v_min_u32_e32 v245, v245, v246
	v_add_u32_e32 v234, v242, v245
	v_sub_u32_e32 v245, v235, v243
	v_add_u32_e32 v246, 0xfffffdc0, v245
	v_min_u32_e32 v245, v245, v246
	v_add_u32_e32 v235, v242, v245
	v_sub_u32_e32 v245, v236, v243
	v_add_u32_e32 v246, 0xfffffdc0, v245
	v_min_u32_e32 v245, v245, v246
	v_add_u32_e32 v236, v242, v245
	v_sub_u32_e32 v245, v237, v243
	v_add_u32_e32 v246, 0xfffffdc0, v245
	v_min_u32_e32 v245, v245, v246
	v_add_u32_e32 v237, v242, v245
	v_sub_u32_e32 v245, v238, v243
	v_add_u32_e32 v246, 0xfffffdc0, v245
	v_min_u32_e32 v245, v245, v246
	v_add_u32_e32 v238, v242, v245
	v_sub_u32_e32 v245, v239, v243
	v_add_u32_e32 v246, 0xfffffdc0, v245
	v_min_u32_e32 v245, v245, v246
	v_add_u32_e32 v239, v242, v245
	v_sub_u32_e32 v245, v240, v243
	v_add_u32_e32 v246, 0xfffffdc0, v245
	v_min_u32_e32 v245, v245, v246
	v_add_u32_e32 v240, v242, v245
	v_sub_u32_e32 v245, v241, v243
	v_add_u32_e32 v246, 0xfffffdc0, v245
	v_min_u32_e32 v245, v245, v246
	v_add_u32_e32 v241, v242, v245
	s_mov_b32 s3, 0x10000
	v_add_co_u32_e32 v10, vcc, s3, v152
	s_mov_b32 s3, 0x14000
	s_nop 0
	v_addc_co_u32_e32 v11, vcc, 0, v153, vcc
	v_add_co_u32_e32 v58, vcc, s3, v152
	global_load_dwordx4 v[34:37], v[10:11], off sc1
	global_load_dwordx4 v[38:41], v[10:11], off offset:256 sc1
	v_addc_co_u32_e32 v59, vcc, 0, v153, vcc
	global_load_dwordx4 v[14:17], v[58:59], off sc1
	global_load_dwordx4 v[10:13], v[58:59], off offset:256 sc1
	v_lshlrev_b32_e32 v58, 4, v87
	v_add_u32_e32 v224, 0x111518dc, v154
	v_mad_u32_u24 v151, v86, s17, v58
	ds_read_b128 v[58:61], v151 offset:0
	v_add_u32_e32 v62, 0x400, v150
	s_waitcnt vmcnt(24) lgkmcnt(0)
	v_mfma_f32_16x16x32_f16 v[86:89], v[26:29], v[58:61], 0
	s_waitcnt vmcnt(23)
	v_mfma_f32_16x16x32_f16 v[122:125], v[50:53], v[58:61], 0
	v_min_u32_e32 v58, v62, v224
	global_load_dwordx4 v[58:61], v58, s[8:9] nt
	s_waitcnt vmcnt(17)
	v_cvt_pk_f16_f32 v63, v112, v113
	v_cvt_pk_f16_f32 v62, v110, v111
	v_add_u32_e32 v155, 0xea00, v1
	ds_write_b16 v234, v62 offset:0
	ds_write_b16_d16_hi v235, v62 offset:0
	ds_write_b16 v236, v63 offset:0
	ds_write_b16_d16_hi v237, v63 offset:0
	ds_read_b128 v[62:65], v151 offset:608
	ds_read_b128 v[66:69], v151 offset:1216
	s_waitcnt lgkmcnt(1)
	v_mfma_f32_16x16x32_f16 v[110:113], v[26:29], v[62:65], 0
	v_mfma_f32_16x16x32_f16 v[126:129], v[50:53], v[62:65], 0
	s_waitcnt lgkmcnt(0)
	v_mfma_f32_16x16x32_f16 v[130:133], v[26:29], v[66:69], 0
	v_mfma_f32_16x16x32_f16 v[134:137], v[50:53], v[66:69], 0
	ds_read_b128 v[62:65], v151 offset:1824
	ds_read_b128 v[66:69], v151 offset:2432
	s_waitcnt lgkmcnt(1)
	v_mfma_f32_16x16x32_f16 v[138:141], v[26:29], v[62:65], 0
	v_mfma_f32_16x16x32_f16 v[142:145], v[50:53], v[62:65], 0
	s_waitcnt lgkmcnt(0)
	v_mfma_f32_16x16x32_f16 v[146:149], v[26:29], v[66:69], 0
	v_mfma_f32_16x16x32_f16 v[156:159], v[50:53], v[66:69], 0
	v_add_u32_e32 v62, 0x16a40, v244
	v_min_u32_e32 v62, v62, v224
	global_load_dwordx4 v[62:65], v62, s[8:9] nt
	s_waitcnt vmcnt(17)
	v_cvt_pk_f16_f32 v67, v116, v117
	v_cvt_pk_f16_f32 v66, v114, v115
	ds_write_b16 v238, v66 offset:608
	ds_write_b16_d16_hi v239, v66 offset:608
	ds_write_b16 v240, v67 offset:608
	ds_write_b16_d16_hi v241, v67 offset:608
	ds_read_b128 v[66:69], v151 offset:3040
	ds_read_b128 v[70:73], v151 offset:4864
	s_waitcnt lgkmcnt(1)
	v_mfma_f32_16x16x32_f16 v[114:117], v[26:29], v[66:69], 0
	v_mfma_f32_16x16x32_f16 v[160:163], v[50:53], v[66:69], 0
	ds_read_b128 v[66:69], v151 offset:3648
	ds_read_b128 v[164:167], v151 offset:4256
	s_waitcnt lgkmcnt(1)
	v_mfma_f32_16x16x32_f16 v[168:171], v[26:29], v[66:69], 0
	v_mfma_f32_16x16x32_f16 v[172:175], v[50:53], v[66:69], 0
	s_waitcnt lgkmcnt(0)
	v_mfma_f32_16x16x32_f16 v[176:179], v[26:29], v[164:167], 0
	v_mfma_f32_16x16x32_f16 v[164:167], v[50:53], v[164:167], 0
	v_mfma_f32_16x16x32_f16 v[180:183], v[26:29], v[70:73], 0
	v_mfma_f32_16x16x32_f16 v[184:187], v[50:53], v[70:73], 0
	v_add_u32_e32 v66, 0x2d080, v150
	v_min_u32_e32 v66, v66, v224
	global_load_dwordx4 v[66:69], v66, s[8:9] nt
	s_waitcnt vmcnt(17)
	v_cvt_pk_f16_f32 v71, v120, v121
	v_cvt_pk_f16_f32 v70, v118, v119
	ds_write_b16 v234, v70 offset:1216
	ds_write_b16_d16_hi v235, v70 offset:1216
	ds_write_b16 v236, v71 offset:1216
	ds_write_b16_d16_hi v237, v71 offset:1216
	ds_read_b128 v[70:73], v151 offset:5472
	ds_read_b128 v[118:121], v151 offset:6080
	s_waitcnt lgkmcnt(1)
	v_mfma_f32_16x16x32_f16 v[188:191], v[26:29], v[70:73], 0
	v_mfma_f32_16x16x32_f16 v[192:195], v[50:53], v[70:73], 0
	ds_read_b128 v[70:73], v151 offset:6688
	ds_read_b128 v[200:203], v151 offset:7296
	s_waitcnt lgkmcnt(2)
	v_mfma_f32_16x16x32_f16 v[196:199], v[26:29], v[118:121], 0
	v_mfma_f32_16x16x32_f16 v[118:121], v[50:53], v[118:121], 0
	s_waitcnt lgkmcnt(1)
	v_mfma_f32_16x16x32_f16 v[204:207], v[26:29], v[70:73], 0
	v_mfma_f32_16x16x32_f16 v[208:211], v[50:53], v[70:73], 0
	s_waitcnt lgkmcnt(0)
	v_mfma_f32_16x16x32_f16 v[26:29], v[26:29], v[200:203], 0
	v_mfma_f32_16x16x32_f16 v[200:203], v[50:53], v[200:203], 0
	v_add_u32_e32 v50, 0x436c0, v244
	v_min_u32_e32 v50, v50, v224
	global_load_dwordx4 v[70:73], v50, s[8:9] nt
	s_waitcnt vmcnt(17)
	v_cvt_pk_f16_f32 v51, v76, v77
	v_cvt_pk_f16_f32 v50, v74, v75
	ds_write_b16 v238, v50 offset:1824
	ds_write_b16_d16_hi v239, v50 offset:1824
	ds_write_b16 v240, v51 offset:1824
	ds_write_b16_d16_hi v241, v51 offset:1824
	ds_read_b128 v[50:53], v151 offset:64
	ds_read_b128 v[74:77], v151 offset:672
	s_waitcnt lgkmcnt(1)
	v_mfma_f32_16x16x32_f16 v[86:89], v[18:21], v[50:53], v[86:89]
	v_mfma_f32_16x16x32_f16 v[122:125], v[42:45], v[50:53], v[122:125]
	s_waitcnt lgkmcnt(0)
	v_mfma_f32_16x16x32_f16 v[110:113], v[18:21], v[74:77], v[110:113]
	v_mfma_f32_16x16x32_f16 v[126:129], v[42:45], v[74:77], v[126:129]
	ds_read_b128 v[50:53], v151 offset:1280
	ds_read_b128 v[74:77], v151 offset:1888
	s_waitcnt lgkmcnt(1)
	v_mfma_f32_16x16x32_f16 v[130:133], v[18:21], v[50:53], v[130:133]
	v_mfma_f32_16x16x32_f16 v[134:137], v[42:45], v[50:53], v[134:137]
	s_waitcnt lgkmcnt(0)
	v_mfma_f32_16x16x32_f16 v[138:141], v[18:21], v[74:77], v[138:141]
	v_mfma_f32_16x16x32_f16 v[142:145], v[42:45], v[74:77], v[142:145]
	v_add_u32_e32 v50, 0x59d00, v150
	v_min_u32_e32 v50, v50, v224
	global_load_dwordx4 v[74:77], v50, s[8:9] nt
	s_waitcnt vmcnt(17)
	v_cvt_pk_f16_f32 v51, v80, v81
	v_cvt_pk_f16_f32 v50, v78, v79
	ds_write_b16 v234, v50 offset:2432
	ds_write_b16_d16_hi v235, v50 offset:2432
	ds_write_b16 v236, v51 offset:2432
	ds_write_b16_d16_hi v237, v51 offset:2432
	ds_read_b128 v[50:53], v151 offset:2496
	ds_read_b128 v[78:81], v151 offset:3104
	s_waitcnt lgkmcnt(1)
	v_mfma_f32_16x16x32_f16 v[146:149], v[18:21], v[50:53], v[146:149]
	v_mfma_f32_16x16x32_f16 v[156:159], v[42:45], v[50:53], v[156:159]
	s_waitcnt lgkmcnt(0)
	v_mfma_f32_16x16x32_f16 v[114:117], v[18:21], v[78:81], v[114:117]
	v_mfma_f32_16x16x32_f16 v[160:163], v[42:45], v[78:81], v[160:163]
	ds_read_b128 v[50:53], v151 offset:3712
	ds_read_b128 v[78:81], v151 offset:4320
	s_waitcnt lgkmcnt(1)
	v_mfma_f32_16x16x32_f16 v[168:171], v[18:21], v[50:53], v[168:171]
	v_mfma_f32_16x16x32_f16 v[172:175], v[42:45], v[50:53], v[172:175]
	s_waitcnt lgkmcnt(0)
	v_mfma_f32_16x16x32_f16 v[176:179], v[18:21], v[78:81], v[176:179]
	v_mfma_f32_16x16x32_f16 v[164:167], v[42:45], v[78:81], v[164:167]
	v_add_u32_e32 v50, 0x70340, v244
	v_min_u32_e32 v50, v50, v224
	global_load_dwordx4 v[78:81], v50, s[8:9] nt
	s_waitcnt vmcnt(17)
	v_cvt_pk_f16_f32 v51, v84, v85
	v_cvt_pk_f16_f32 v50, v82, v83
	ds_write_b16 v238, v50 offset:3040
	ds_write_b16_d16_hi v239, v50 offset:3040
	ds_write_b16 v240, v51 offset:3040
	ds_write_b16_d16_hi v241, v51 offset:3040
	ds_read_b128 v[50:53], v151 offset:4928
	ds_read_b128 v[82:85], v151 offset:5536
	s_waitcnt lgkmcnt(1)
	v_mfma_f32_16x16x32_f16 v[180:183], v[18:21], v[50:53], v[180:183]
	v_mfma_f32_16x16x32_f16 v[184:187], v[42:45], v[50:53], v[184:187]
	s_waitcnt lgkmcnt(0)
	v_mfma_f32_16x16x32_f16 v[188:191], v[18:21], v[82:85], v[188:191]
	v_mfma_f32_16x16x32_f16 v[192:195], v[42:45], v[82:85], v[192:195]
	ds_read_b128 v[50:53], v151 offset:6144
	ds_read_b128 v[82:85], v151 offset:6752
	s_waitcnt lgkmcnt(1)
	v_mfma_f32_16x16x32_f16 v[196:199], v[18:21], v[50:53], v[196:199]
	v_mfma_f32_16x16x32_f16 v[118:121], v[42:45], v[50:53], v[118:121]
	s_waitcnt lgkmcnt(0)
	v_mfma_f32_16x16x32_f16 v[204:207], v[18:21], v[82:85], v[204:207]
	v_mfma_f32_16x16x32_f16 v[208:211], v[42:45], v[82:85], v[208:211]
	v_add_u32_e32 v50, 0x86980, v150
	v_min_u32_e32 v50, v50, v224
	global_load_dwordx4 v[82:85], v50, s[8:9] nt
	s_waitcnt vmcnt(17)
	v_cvt_pk_f16_f32 v51, v56, v57
	v_cvt_pk_f16_f32 v50, v54, v55
	ds_write_b16 v234, v50 offset:3648
	ds_write_b16_d16_hi v235, v50 offset:3648
	ds_write_b16 v236, v51 offset:3648
	ds_write_b16_d16_hi v237, v51 offset:3648
	ds_read_b128 v[212:215], v151 offset:7360
	s_mov_b32 s2, 0x18000
	s_waitcnt lgkmcnt(0)
	v_mfma_f32_16x16x32_f16 v[216:219], v[18:21], v[212:215], v[26:29]
	v_add_co_u32_e32 v18, vcc, s2, v152
	s_mov_b32 s2, 0x1c000
	s_nop 0
	v_addc_co_u32_e32 v19, vcc, 0, v153, vcc
	global_load_dwordx4 v[50:53], v[18:19], off sc1
	global_load_dwordx4 v[54:57], v[18:19], off offset:256 sc1
	v_add_co_u32_e32 v18, vcc, s2, v152
	v_mfma_f32_16x16x32_f16 v[42:45], v[42:45], v[212:215], v[200:203]
	s_nop 0
	v_addc_co_u32_e32 v19, vcc, 0, v153, vcc
	global_load_dwordx4 v[26:29], v[18:19], off sc1
	s_nop 0
	global_load_dwordx4 v[18:21], v[18:19], off offset:256 sc1
	ds_read_b128 v[200:203], v151 offset:128
	ds_read_b128 v[212:215], v151 offset:736
	s_waitcnt lgkmcnt(1)
	v_mfma_f32_16x16x32_f16 v[220:223], v[22:25], v[200:203], v[86:89]
	s_nop 2
	ds_read_b128 v[86:89], v151 offset:1344
	v_mfma_f32_16x16x32_f16 v[122:125], v[30:33], v[200:203], v[122:125]
	s_waitcnt lgkmcnt(1)
	v_mfma_f32_16x16x32_f16 v[110:113], v[22:25], v[212:215], v[110:113]
	v_mfma_f32_16x16x32_f16 v[126:129], v[30:33], v[212:215], v[126:129]
	s_waitcnt lgkmcnt(0)
	v_mfma_f32_16x16x32_f16 v[130:133], v[22:25], v[86:89], v[130:133]
	v_mfma_f32_16x16x32_f16 v[134:137], v[30:33], v[86:89], v[134:137]
	v_add_u32_e32 v86, 0x9cfc0, v244
	v_min_u32_e32 v86, v86, v224
	global_load_dwordx4 v[86:89], v86, s[8:9] nt
	s_waitcnt vmcnt(21)
	v_cvt_pk_f16_f32 v93, v92, v93
	v_cvt_pk_f16_f32 v92, v90, v91
	ds_write_b16 v238, v92 offset:4256
	ds_write_b16_d16_hi v239, v92 offset:4256
	ds_write_b16 v240, v93 offset:4256
	ds_write_b16_d16_hi v241, v93 offset:4256
	ds_read_b128 v[90:93], v151 offset:1952
	ds_read_b128 v[200:203], v151 offset:2560
	s_waitcnt lgkmcnt(1)
	v_mfma_f32_16x16x32_f16 v[138:141], v[22:25], v[90:93], v[138:141]
	v_mfma_f32_16x16x32_f16 v[142:145], v[30:33], v[90:93], v[142:145]
	s_waitcnt lgkmcnt(0)
	v_mfma_f32_16x16x32_f16 v[146:149], v[22:25], v[200:203], v[146:149]
	v_mfma_f32_16x16x32_f16 v[156:159], v[30:33], v[200:203], v[156:159]
	ds_read_b128 v[90:93], v151 offset:3168
	ds_read_b128 v[200:203], v151 offset:3776
	s_waitcnt lgkmcnt(1)
	v_mfma_f32_16x16x32_f16 v[114:117], v[22:25], v[90:93], v[114:117]
	v_mfma_f32_16x16x32_f16 v[160:163], v[30:33], v[90:93], v[160:163]
	s_waitcnt lgkmcnt(0)
	v_mfma_f32_16x16x32_f16 v[168:171], v[22:25], v[200:203], v[168:171]
	v_mfma_f32_16x16x32_f16 v[172:175], v[30:33], v[200:203], v[172:175]
	v_add_u32_e32 v90, 0xb3600, v150
	v_min_u32_e32 v90, v90, v224
	global_load_dwordx4 v[90:93], v90, s[8:9] nt
	s_waitcnt vmcnt(21)
	v_cvt_pk_f16_f32 v97, v96, v97
	v_cvt_pk_f16_f32 v96, v94, v95
	ds_write_b16 v234, v96 offset:4864
	ds_write_b16_d16_hi v235, v96 offset:4864
	ds_write_b16 v236, v97 offset:4864
	ds_write_b16_d16_hi v237, v97 offset:4864
	ds_read_b128 v[94:97], v151 offset:4384
	ds_read_b128 v[200:203], v151 offset:6208
	s_waitcnt lgkmcnt(1)
	v_mfma_f32_16x16x32_f16 v[176:179], v[22:25], v[94:97], v[176:179]
	v_mfma_f32_16x16x32_f16 v[164:167], v[30:33], v[94:97], v[164:167]
	ds_read_b128 v[94:97], v151 offset:4992
	ds_read_b128 v[212:215], v151 offset:5600
	s_waitcnt lgkmcnt(1)
	v_mfma_f32_16x16x32_f16 v[180:183], v[22:25], v[94:97], v[180:183]
	v_mfma_f32_16x16x32_f16 v[184:187], v[30:33], v[94:97], v[184:187]
	s_waitcnt lgkmcnt(0)
	v_mfma_f32_16x16x32_f16 v[188:191], v[22:25], v[212:215], v[188:191]
	v_mfma_f32_16x16x32_f16 v[192:195], v[30:33], v[212:215], v[192:195]
	v_mfma_f32_16x16x32_f16 v[196:199], v[22:25], v[200:203], v[196:199]
	v_mfma_f32_16x16x32_f16 v[118:121], v[30:33], v[200:203], v[118:121]
	v_add_u32_e32 v94, 0xc9c40, v244
	v_min_u32_e32 v94, v94, v224
	global_load_dwordx4 v[94:97], v94, s[8:9] nt
	s_waitcnt vmcnt(21)
	v_cvt_pk_f16_f32 v101, v100, v101
	v_cvt_pk_f16_f32 v100, v98, v99
	ds_write_b16 v238, v100 offset:5472
	ds_write_b16_d16_hi v239, v100 offset:5472
	ds_write_b16 v240, v101 offset:5472
	ds_write_b16_d16_hi v241, v101 offset:5472
	ds_read_b128 v[98:101], v151 offset:6816
	ds_read_b128 v[200:203], v151 offset:7424
	s_waitcnt lgkmcnt(1)
	v_mfma_f32_16x16x32_f16 v[204:207], v[22:25], v[98:101], v[204:207]
	v_mfma_f32_16x16x32_f16 v[208:211], v[30:33], v[98:101], v[208:211]
	s_waitcnt lgkmcnt(0)
	v_mfma_f32_16x16x32_f16 v[30:33], v[30:33], v[200:203], v[42:45]
	s_nop 2
	ds_read_b128 v[42:45], v151 offset:192
	ds_read_b128 v[98:101], v151 offset:800
	v_mfma_f32_16x16x32_f16 v[22:25], v[22:25], v[200:203], v[216:219]
	s_waitcnt lgkmcnt(1)
	v_mfma_f32_16x16x32_f16 v[200:203], v[6:9], v[42:45], v[220:223]
	v_mfma_f32_16x16x32_f16 v[122:125], v[2:5], v[42:45], v[122:125]
	s_waitcnt lgkmcnt(0)
	v_mfma_f32_16x16x32_f16 v[212:215], v[6:9], v[98:101], v[110:113]
	v_mfma_f32_16x16x32_f16 v[126:129], v[2:5], v[98:101], v[126:129]
	v_add_u32_e32 v42, 0xe0280, v150
	v_min_u32_e32 v42, v42, v224
	global_load_dwordx4 v[98:101], v42, s[8:9] nt
	s_waitcnt vmcnt(21)
	v_cvt_pk_f16_f32 v43, v104, v105
	v_cvt_pk_f16_f32 v42, v102, v103
	ds_write_b16 v234, v42 offset:6080
	ds_write_b16_d16_hi v235, v42 offset:6080
	ds_write_b16 v236, v43 offset:6080
	ds_write_b16_d16_hi v237, v43 offset:6080
	ds_read_b128 v[42:45], v151 offset:1408
	ds_read_b128 v[102:105], v151 offset:2016
	s_waitcnt lgkmcnt(1)
	v_mfma_f32_16x16x32_f16 v[130:133], v[6:9], v[42:45], v[130:133]
	v_mfma_f32_16x16x32_f16 v[134:137], v[2:5], v[42:45], v[134:137]
	s_waitcnt lgkmcnt(0)
	v_mfma_f32_16x16x32_f16 v[138:141], v[6:9], v[102:105], v[138:141]
	v_mfma_f32_16x16x32_f16 v[142:145], v[2:5], v[102:105], v[142:145]
	ds_read_b128 v[42:45], v151 offset:2624
	ds_read_b128 v[102:105], v151 offset:3232
	s_waitcnt lgkmcnt(1)
	v_mfma_f32_16x16x32_f16 v[146:149], v[6:9], v[42:45], v[146:149]
	v_mfma_f32_16x16x32_f16 v[216:219], v[2:5], v[42:45], v[156:159]
	s_waitcnt lgkmcnt(0)
	v_mfma_f32_16x16x32_f16 v[220:223], v[6:9], v[102:105], v[114:117]
	v_mfma_f32_16x16x32_f16 v[158:161], v[2:5], v[102:105], v[160:163]
	v_add_u32_e32 v42, 0xf68c0, v244
	v_min_u32_e32 v42, v42, v224
	global_load_dwordx4 v[102:105], v42, s[8:9] nt
	s_waitcnt vmcnt(21)
	v_cvt_pk_f16_f32 v43, v108, v109
	v_cvt_pk_f16_f32 v42, v106, v107
	ds_write_b16 v238, v42 offset:6688
	ds_write_b16_d16_hi v239, v42 offset:6688
	ds_write_b16 v240, v43 offset:6688
	ds_write_b16_d16_hi v241, v43 offset:6688
	ds_read_b128 v[42:45], v151 offset:3840
	ds_read_b128 v[106:109], v151 offset:4448
	s_waitcnt lgkmcnt(1)
	v_mfma_f32_16x16x32_f16 v[168:171], v[6:9], v[42:45], v[168:171]
	v_mfma_f32_16x16x32_f16 v[172:175], v[2:5], v[42:45], v[172:175]
	s_waitcnt lgkmcnt(0)
	v_mfma_f32_16x16x32_f16 v[176:179], v[6:9], v[106:109], v[176:179]
	v_mfma_f32_16x16x32_f16 v[162:165], v[2:5], v[106:109], v[164:167]
	ds_read_b128 v[42:45], v151 offset:5056
	ds_read_b128 v[106:109], v151 offset:5664
	s_waitcnt lgkmcnt(1)
	v_mfma_f32_16x16x32_f16 v[180:183], v[6:9], v[42:45], v[180:183]
	v_mfma_f32_16x16x32_f16 v[184:187], v[2:5], v[42:45], v[184:187]
	s_waitcnt lgkmcnt(0)
	v_mfma_f32_16x16x32_f16 v[188:191], v[6:9], v[106:109], v[188:191]
	v_mfma_f32_16x16x32_f16 v[192:195], v[2:5], v[106:109], v[192:195]
	v_add_u32_e32 v42, 0x10cf00, v150
	v_min_u32_e32 v42, v42, v224
	v_cndmask_b32_e64 v42, 0, v42, s[0:1]
	global_load_dwordx4 v[106:109], v42, s[8:9] nt
	s_waitcnt vmcnt(21)
	v_cvt_pk_f16_f32 v43, v48, v49
	v_cvt_pk_f16_f32 v42, v46, v47
	ds_write_b16 v234, v42 offset:7296
	ds_write_b16_d16_hi v235, v42 offset:7296
	ds_write_b16 v236, v43 offset:7296
	ds_write_b16_d16_hi v237, v43 offset:7296
	ds_read_b128 v[42:45], v151 offset:6272
	ds_read_b128 v[46:49], v151 offset:6880
	ds_read_b128 v[110:113], v151 offset:7488
	s_mov_b32 s2, 0x20000
	v_add_co_u32_e32 v114, vcc, s2, v152
	s_mov_b32 s2, 0x24000
	s_nop 0
	v_addc_co_u32_e32 v115, vcc, 0, v153, vcc
	s_waitcnt lgkmcnt(2)
	v_mfma_f32_16x16x32_f16 v[196:199], v[6:9], v[42:45], v[196:199]
	s_waitcnt lgkmcnt(0)
	s_barrier
	v_sub_u32_e32 v245, v234, v243
	v_add_u32_e32 v246, 0xfffffdc0, v245
	v_min_u32_e32 v245, v245, v246
	v_add_u32_e32 v234, v242, v245
	v_sub_u32_e32 v245, v235, v243
	v_add_u32_e32 v246, 0xfffffdc0, v245
	v_min_u32_e32 v245, v245, v246
	v_add_u32_e32 v235, v242, v245
	v_sub_u32_e32 v245, v236, v243
	v_add_u32_e32 v246, 0xfffffdc0, v245
	v_min_u32_e32 v245, v245, v246
	v_add_u32_e32 v236, v242, v245
	v_sub_u32_e32 v245, v237, v243
	v_add_u32_e32 v246, 0xfffffdc0, v245
	v_min_u32_e32 v245, v245, v246
	v_add_u32_e32 v237, v242, v245
	v_sub_u32_e32 v245, v238, v243
	v_add_u32_e32 v246, 0xfffffdc0, v245
	v_min_u32_e32 v245, v245, v246
	v_add_u32_e32 v238, v242, v245
	v_sub_u32_e32 v245, v239, v243
	v_add_u32_e32 v246, 0xfffffdc0, v245
	v_min_u32_e32 v245, v245, v246
	v_add_u32_e32 v239, v242, v245
	v_sub_u32_e32 v245, v240, v243
	v_add_u32_e32 v246, 0xfffffdc0, v245
	v_min_u32_e32 v245, v245, v246
	v_add_u32_e32 v240, v242, v245
	v_sub_u32_e32 v245, v241, v243
	v_add_u32_e32 v246, 0xfffffdc0, v245
	v_min_u32_e32 v245, v245, v246
	v_add_u32_e32 v241, v242, v245
	v_mfma_f32_16x16x32_f16 v[204:207], v[6:9], v[46:49], v[204:207]
	v_mfma_f32_16x16x32_f16 v[228:231], v[6:9], v[110:113], v[22:25]
	v_add_co_u32_e32 v6, vcc, s2, v152
	s_nop 1
	v_addc_co_u32_e32 v7, vcc, 0, v153, vcc
	v_mfma_f32_16x16x32_f16 v[224:227], v[2:5], v[42:45], v[118:121]
	v_mfma_f32_16x16x32_f16 v[208:211], v[2:5], v[46:49], v[208:211]
	global_load_dwordx4 v[42:45], v[114:115], off sc1
	global_load_dwordx4 v[46:49], v[114:115], off offset:256 sc1
	global_load_dwordx4 v[22:25], v[6:7], off sc1
	s_nop 0
	global_load_dwordx4 v[6:9], v[6:7], off offset:256 sc1
	v_mfma_f32_16x16x32_f16 v[2:5], v[2:5], v[110:113], v[30:33]
	v_add_u32_e32 v157, 0x11151adc, v154
	s_nop 1
	ds_read_b128 v[30:33], v151 offset:256
	v_add_u32_e32 v156, 0xea00, v151
	v_add_u32_e32 v110, 0x600, v150
	s_waitcnt vmcnt(24) lgkmcnt(0)
	v_mfma_f32_16x16x32_f16 v[200:203], v[34:37], v[30:33], v[200:203]
	s_waitcnt vmcnt(23)
	v_mfma_f32_16x16x32_f16 v[30:33], v[38:41], v[30:33], v[122:125]
	v_min_u32_e32 v110, v110, v157
	global_load_dwordx4 v[110:113], v110, s[8:9] nt
	s_waitcnt vmcnt(21)
	v_cvt_pk_f16_f32 v61, v60, v61
	v_cvt_pk_f16_f32 v60, v58, v59
	ds_write_b16 v234, v60 offset:0
	ds_write_b16_d16_hi v235, v60 offset:0
	ds_write_b16 v236, v61 offset:0
	ds_write_b16_d16_hi v237, v61 offset:0
	ds_read_b128 v[58:61], v151 offset:864
	ds_read_b128 v[114:117], v151 offset:1472
	s_waitcnt lgkmcnt(1)
	v_mfma_f32_16x16x32_f16 v[122:125], v[34:37], v[58:61], v[212:215]
	v_mfma_f32_16x16x32_f16 v[58:61], v[38:41], v[58:61], v[126:129]
	s_waitcnt lgkmcnt(0)
	v_mfma_f32_16x16x32_f16 v[126:129], v[34:37], v[114:117], v[130:133]
	v_mfma_f32_16x16x32_f16 v[130:133], v[38:41], v[114:117], v[134:137]
	ds_read_b128 v[114:117], v151 offset:2080
	ds_read_b128 v[118:121], v151 offset:2688
	s_waitcnt lgkmcnt(1)
	v_mfma_f32_16x16x32_f16 v[134:137], v[34:37], v[114:117], v[138:141]
	v_mfma_f32_16x16x32_f16 v[138:141], v[38:41], v[114:117], v[142:145]
	s_waitcnt lgkmcnt(0)
	v_mfma_f32_16x16x32_f16 v[142:145], v[34:37], v[118:121], v[146:149]
	v_mfma_f32_16x16x32_f16 v[146:149], v[38:41], v[118:121], v[216:219]
	v_add_u32_e32 v114, 0x16c40, v244
	v_min_u32_e32 v114, v114, v157
	global_load_dwordx4 v[114:117], v114, s[8:9] nt
	s_waitcnt vmcnt(21)
	v_cvt_pk_f16_f32 v65, v64, v65
	v_cvt_pk_f16_f32 v64, v62, v63
	ds_write_b16 v238, v64 offset:608
	ds_write_b16_d16_hi v239, v64 offset:608
	ds_write_b16 v240, v65 offset:608
	ds_write_b16_d16_hi v241, v65 offset:608
	ds_read_b128 v[62:65], v151 offset:3296
	ds_read_b128 v[118:121], v151 offset:5120
	s_waitcnt lgkmcnt(1)
	v_mfma_f32_16x16x32_f16 v[212:215], v[34:37], v[62:65], v[220:223]
	v_mfma_f32_16x16x32_f16 v[62:65], v[38:41], v[62:65], v[158:161]
	s_nop 2
	ds_read_b128 v[158:161], v151 offset:3904
	ds_read_b128 v[216:219], v151 offset:4512
	s_waitcnt lgkmcnt(1)
	v_mfma_f32_16x16x32_f16 v[166:169], v[34:37], v[158:161], v[168:171]
	v_mfma_f32_16x16x32_f16 v[158:161], v[38:41], v[158:161], v[172:175]
	s_waitcnt lgkmcnt(0)
	v_mfma_f32_16x16x32_f16 v[170:173], v[34:37], v[216:219], v[176:179]
	v_mfma_f32_16x16x32_f16 v[162:165], v[38:41], v[216:219], v[162:165]
	v_mfma_f32_16x16x32_f16 v[174:177], v[34:37], v[118:121], v[180:183]
	v_mfma_f32_16x16x32_f16 v[178:181], v[38:41], v[118:121], v[184:187]
	v_add_u32_e32 v118, 0x2d280, v150
	v_min_u32_e32 v118, v118, v157
	global_load_dwordx4 v[118:121], v118, s[8:9] nt
	s_waitcnt vmcnt(21)
	v_cvt_pk_f16_f32 v69, v68, v69
	v_cvt_pk_f16_f32 v68, v66, v67
	ds_write_b16 v234, v68 offset:1216
	ds_write_b16_d16_hi v235, v68 offset:1216
	ds_write_b16 v236, v69 offset:1216
	ds_write_b16_d16_hi v237, v69 offset:1216
	ds_read_b128 v[66:69], v151 offset:5728
	ds_read_b128 v[182:185], v151 offset:6336
	s_waitcnt lgkmcnt(1)
	v_mfma_f32_16x16x32_f16 v[186:189], v[34:37], v[66:69], v[188:191]
	v_mfma_f32_16x16x32_f16 v[190:193], v[38:41], v[66:69], v[192:195]
	ds_read_b128 v[66:69], v151 offset:6944
	ds_read_b128 v[216:219], v151 offset:7552
	s_waitcnt lgkmcnt(2)
	v_mfma_f32_16x16x32_f16 v[194:197], v[34:37], v[182:185], v[196:199]
	v_mfma_f32_16x16x32_f16 v[182:185], v[38:41], v[182:185], v[224:227]
	s_waitcnt lgkmcnt(1)
	v_mfma_f32_16x16x32_f16 v[204:207], v[34:37], v[66:69], v[204:207]
	v_mfma_f32_16x16x32_f16 v[208:211], v[38:41], v[66:69], v[208:211]
	s_waitcnt lgkmcnt(0)
	v_mfma_f32_16x16x32_f16 v[220:223], v[34:37], v[216:219], v[228:231]
	v_mfma_f32_16x16x32_f16 v[2:5], v[38:41], v[216:219], v[2:5]
	v_add_u32_e32 v34, 0x438c0, v244
	v_min_u32_e32 v34, v34, v157
	global_load_dwordx4 v[34:37], v34, s[8:9] nt
	s_waitcnt vmcnt(21)
	v_cvt_pk_f16_f32 v39, v72, v73
	v_cvt_pk_f16_f32 v38, v70, v71
	ds_write_b16 v238, v38 offset:1824
	ds_write_b16_d16_hi v239, v38 offset:1824
	ds_write_b16 v240, v39 offset:1824
	ds_write_b16_d16_hi v241, v39 offset:1824
	ds_read_b128 v[38:41], v151 offset:320
	ds_read_b128 v[66:69], v151 offset:928
	s_waitcnt lgkmcnt(1)
	v_mfma_f32_16x16x32_f16 v[198:201], v[14:17], v[38:41], v[200:203]
	v_mfma_f32_16x16x32_f16 v[38:41], v[10:13], v[38:41], v[30:33]
	s_waitcnt lgkmcnt(0)
	v_mfma_f32_16x16x32_f16 v[216:219], v[10:13], v[66:69], v[58:61]
	s_nop 0
	ds_read_b128 v[30:33], v151 offset:1536
	s_nop 0
	ds_read_b128 v[58:61], v151 offset:2144
	v_mfma_f32_16x16x32_f16 v[122:125], v[14:17], v[66:69], v[122:125]
	s_waitcnt lgkmcnt(1)
	v_mfma_f32_16x16x32_f16 v[126:129], v[14:17], v[30:33], v[126:129]
	v_mfma_f32_16x16x32_f16 v[130:133], v[10:13], v[30:33], v[130:133]
	s_waitcnt lgkmcnt(0)
	v_mfma_f32_16x16x32_f16 v[134:137], v[14:17], v[58:61], v[134:137]
	v_mfma_f32_16x16x32_f16 v[138:141], v[10:13], v[58:61], v[138:141]
	v_add_u32_e32 v30, 0x59f00, v150
	v_min_u32_e32 v30, v30, v157
	global_load_dwordx4 v[66:69], v30, s[8:9] nt
	s_waitcnt vmcnt(21)
	v_cvt_pk_f16_f32 v31, v76, v77
	v_cvt_pk_f16_f32 v30, v74, v75
	ds_write_b16 v234, v30 offset:2432
	ds_write_b16_d16_hi v235, v30 offset:2432
	ds_write_b16 v236, v31 offset:2432
	ds_write_b16_d16_hi v237, v31 offset:2432
	ds_read_b128 v[30:33], v151 offset:2752
	ds_read_b128 v[58:61], v151 offset:3360
	s_waitcnt lgkmcnt(1)
	v_mfma_f32_16x16x32_f16 v[142:145], v[14:17], v[30:33], v[142:145]
	v_mfma_f32_16x16x32_f16 v[146:149], v[10:13], v[30:33], v[146:149]
	s_waitcnt lgkmcnt(0)
	v_mfma_f32_16x16x32_f16 v[212:215], v[14:17], v[58:61], v[212:215]
	v_mfma_f32_16x16x32_f16 v[224:227], v[10:13], v[58:61], v[62:65]
	ds_read_b128 v[30:33], v151 offset:3968
	ds_read_b128 v[58:61], v151 offset:4576
	s_waitcnt lgkmcnt(1)
	v_mfma_f32_16x16x32_f16 v[166:169], v[14:17], v[30:33], v[166:169]
	v_mfma_f32_16x16x32_f16 v[158:161], v[10:13], v[30:33], v[158:161]
	s_waitcnt lgkmcnt(0)
	v_mfma_f32_16x16x32_f16 v[170:173], v[14:17], v[58:61], v[170:173]
	v_mfma_f32_16x16x32_f16 v[162:165], v[10:13], v[58:61], v[162:165]
	v_add_u32_e32 v30, 0x70540, v244
	v_min_u32_e32 v30, v30, v157
	global_load_dwordx4 v[70:73], v30, s[8:9] nt
	s_waitcnt vmcnt(21)
	v_cvt_pk_f16_f32 v31, v80, v81
	v_cvt_pk_f16_f32 v30, v78, v79
	ds_write_b16 v238, v30 offset:3040
	ds_write_b16_d16_hi v239, v30 offset:3040
	ds_write_b16 v240, v31 offset:3040
	ds_write_b16_d16_hi v241, v31 offset:3040
	ds_read_b128 v[30:33], v151 offset:5184
	ds_read_b128 v[58:61], v151 offset:5792
	s_waitcnt lgkmcnt(1)
	v_mfma_f32_16x16x32_f16 v[174:177], v[14:17], v[30:33], v[174:177]
	v_mfma_f32_16x16x32_f16 v[178:181], v[10:13], v[30:33], v[178:181]
	s_waitcnt lgkmcnt(0)
	v_mfma_f32_16x16x32_f16 v[186:189], v[14:17], v[58:61], v[186:189]
	v_mfma_f32_16x16x32_f16 v[190:193], v[10:13], v[58:61], v[190:193]
	ds_read_b128 v[30:33], v151 offset:6400
	ds_read_b128 v[58:61], v151 offset:7008
	s_waitcnt lgkmcnt(1)
	v_mfma_f32_16x16x32_f16 v[194:197], v[14:17], v[30:33], v[194:197]
	v_mfma_f32_16x16x32_f16 v[182:185], v[10:13], v[30:33], v[182:185]
	s_waitcnt lgkmcnt(0)
	v_mfma_f32_16x16x32_f16 v[202:205], v[14:17], v[58:61], v[204:207]
	v_mfma_f32_16x16x32_f16 v[206:209], v[10:13], v[58:61], v[208:211]
	v_add_u32_e32 v30, 0x86b80, v150
	v_min_u32_e32 v30, v30, v157
	global_load_dwordx4 v[74:77], v30, s[8:9] nt
	s_waitcnt vmcnt(21)
	v_cvt_pk_f16_f32 v31, v84, v85
	v_cvt_pk_f16_f32 v30, v82, v83
	ds_write_b16 v234, v30 offset:3648
	ds_write_b16_d16_hi v235, v30 offset:3648
	ds_write_b16 v236, v31 offset:3648
	ds_write_b16_d16_hi v237, v31 offset:3648
	ds_read_b128 v[78:81], v151 offset:7616
	s_mov_b32 s2, 0x28000
	s_waitcnt lgkmcnt(0)
	v_mfma_f32_16x16x32_f16 v[220:223], v[14:17], v[78:81], v[220:223]
	v_add_co_u32_e32 v14, vcc, s2, v152
	s_mov_b32 s2, 0x2c000
	s_nop 0
	v_addc_co_u32_e32 v15, vcc, 0, v153, vcc
	global_load_dwordx4 v[58:61], v[14:15], off sc1
	global_load_dwordx4 v[62:65], v[14:15], off offset:256 sc1
	v_add_co_u32_e32 v14, vcc, s2, v152
	v_mfma_f32_16x16x32_f16 v[2:5], v[10:13], v[78:81], v[2:5]
	s_nop 0
	v_addc_co_u32_e32 v15, vcc, 0, v153, vcc
	global_load_dwordx4 v[30:33], v[14:15], off sc1
	s_nop 0
	global_load_dwordx4 v[14:17], v[14:15], off offset:256 sc1
	ds_read_b128 v[10:13], v151 offset:384
	ds_read_b128 v[78:81], v151 offset:992
	s_waitcnt vmcnt(24) lgkmcnt(1)
	v_mfma_f32_16x16x32_f16 v[198:201], v[50:53], v[10:13], v[198:201]
	s_waitcnt vmcnt(23)
	v_mfma_f32_16x16x32_f16 v[10:13], v[54:57], v[10:13], v[38:41]
	s_waitcnt lgkmcnt(0)
	v_mfma_f32_16x16x32_f16 v[38:41], v[50:53], v[78:81], v[122:125]
	v_mfma_f32_16x16x32_f16 v[122:125], v[54:57], v[78:81], v[216:219]
	ds_read_b128 v[78:81], v151 offset:1600
	s_waitcnt lgkmcnt(0)
	v_mfma_f32_16x16x32_f16 v[126:129], v[50:53], v[78:81], v[126:129]
	v_mfma_f32_16x16x32_f16 v[130:133], v[54:57], v[78:81], v[130:133]
	v_add_u32_e32 v78, 0x9d1c0, v244
	v_min_u32_e32 v78, v78, v157
	global_load_dwordx4 v[78:81], v78, s[8:9] nt
	s_waitcnt vmcnt(21)
	v_cvt_pk_f16_f32 v83, v88, v89
	v_cvt_pk_f16_f32 v82, v86, v87
	ds_write_b16 v238, v82 offset:4256
	ds_write_b16_d16_hi v239, v82 offset:4256
	ds_write_b16 v240, v83 offset:4256
	ds_write_b16_d16_hi v241, v83 offset:4256
	ds_read_b128 v[82:85], v151 offset:2208
	ds_read_b128 v[86:89], v151 offset:2816
	s_waitcnt lgkmcnt(1)
	v_mfma_f32_16x16x32_f16 v[134:137], v[50:53], v[82:85], v[134:137]
	v_mfma_f32_16x16x32_f16 v[138:141], v[54:57], v[82:85], v[138:141]
	s_waitcnt lgkmcnt(0)
	v_mfma_f32_16x16x32_f16 v[142:145], v[50:53], v[86:89], v[142:145]
	v_mfma_f32_16x16x32_f16 v[146:149], v[54:57], v[86:89], v[146:149]
	ds_read_b128 v[82:85], v151 offset:3424
	ds_read_b128 v[86:89], v151 offset:4032
	s_waitcnt lgkmcnt(1)
	v_mfma_f32_16x16x32_f16 v[210:213], v[50:53], v[82:85], v[212:215]
	v_mfma_f32_16x16x32_f16 v[214:217], v[54:57], v[82:85], v[224:227]
	s_waitcnt lgkmcnt(0)
	v_mfma_f32_16x16x32_f16 v[166:169], v[50:53], v[86:89], v[166:169]
	v_mfma_f32_16x16x32_f16 v[158:161], v[54:57], v[86:89], v[158:161]
	v_add_u32_e32 v82, 0xb3800, v150
	v_min_u32_e32 v82, v82, v157
	global_load_dwordx4 v[82:85], v82, s[8:9] nt
	s_waitcnt vmcnt(21)
	v_cvt_pk_f16_f32 v87, v92, v93
	v_cvt_pk_f16_f32 v86, v90, v91
	ds_write_b16 v234, v86 offset:4864
	ds_write_b16_d16_hi v235, v86 offset:4864
	ds_write_b16 v236, v87 offset:4864
	ds_write_b16_d16_hi v237, v87 offset:4864
	ds_read_b128 v[86:89], v151 offset:4640
	ds_read_b128 v[90:93], v151 offset:6464
	s_waitcnt lgkmcnt(1)
	v_mfma_f32_16x16x32_f16 v[170:173], v[50:53], v[86:89], v[170:173]
	v_mfma_f32_16x16x32_f16 v[162:165], v[54:57], v[86:89], v[162:165]
	ds_read_b128 v[86:89], v151 offset:5248
	ds_read_b128 v[224:227], v151 offset:5856
	s_waitcnt lgkmcnt(1)
	v_mfma_f32_16x16x32_f16 v[174:177], v[50:53], v[86:89], v[174:177]
	v_mfma_f32_16x16x32_f16 v[178:181], v[54:57], v[86:89], v[178:181]
	s_waitcnt lgkmcnt(0)
	v_mfma_f32_16x16x32_f16 v[186:189], v[50:53], v[224:227], v[186:189]
	v_mfma_f32_16x16x32_f16 v[190:193], v[54:57], v[224:227], v[190:193]
	v_mfma_f32_16x16x32_f16 v[194:197], v[50:53], v[90:93], v[194:197]
	v_mfma_f32_16x16x32_f16 v[182:185], v[54:57], v[90:93], v[182:185]
	v_add_u32_e32 v86, 0xc9e40, v244
	v_min_u32_e32 v86, v86, v157
	global_load_dwordx4 v[86:89], v86, s[8:9] nt
	s_waitcnt vmcnt(21)
	v_cvt_pk_f16_f32 v91, v96, v97
	v_cvt_pk_f16_f32 v90, v94, v95
	ds_write_b16 v238, v90 offset:5472
	ds_write_b16_d16_hi v239, v90 offset:5472
	ds_write_b16 v240, v91 offset:5472
	ds_write_b16_d16_hi v241, v91 offset:5472
	ds_read_b128 v[90:93], v151 offset:7072
	ds_read_b128 v[94:97], v151 offset:7680
	s_waitcnt lgkmcnt(1)
	v_mfma_f32_16x16x32_f16 v[202:205], v[50:53], v[90:93], v[202:205]
	v_mfma_f32_16x16x32_f16 v[206:209], v[54:57], v[90:93], v[206:209]
	s_waitcnt lgkmcnt(0)
	v_mfma_f32_16x16x32_f16 v[218:221], v[50:53], v[94:97], v[220:223]
	v_mfma_f32_16x16x32_f16 v[54:57], v[54:57], v[94:97], v[2:5]
	s_nop 2
	ds_read_b128 v[2:5], v151 offset:448
	ds_read_b128 v[50:53], v151 offset:1056
	s_waitcnt lgkmcnt(1)
	v_mfma_f32_16x16x32_f16 v[198:201], v[26:29], v[2:5], v[198:201]
	v_mfma_f32_16x16x32_f16 v[222:225], v[18:21], v[2:5], v[10:13]
	s_waitcnt lgkmcnt(0)
	v_mfma_f32_16x16x32_f16 v[226:229], v[26:29], v[50:53], v[38:41]
	v_mfma_f32_16x16x32_f16 v[122:125], v[18:21], v[50:53], v[122:125]
	v_add_u32_e32 v2, 0xe0480, v150
	v_min_u32_e32 v2, v2, v157
	global_load_dwordx4 v[90:93], v2, s[8:9] nt
	s_waitcnt vmcnt(21)
	v_cvt_pk_f16_f32 v3, v100, v101
	v_cvt_pk_f16_f32 v2, v98, v99
	ds_write_b16 v234, v2 offset:6080
	ds_write_b16_d16_hi v235, v2 offset:6080
	ds_write_b16 v236, v3 offset:6080
	ds_write_b16_d16_hi v237, v3 offset:6080
	ds_read_b128 v[2:5], v151 offset:1664
	ds_read_b128 v[10:13], v151 offset:2272
	s_waitcnt lgkmcnt(1)
	v_mfma_f32_16x16x32_f16 v[126:129], v[26:29], v[2:5], v[126:129]
	v_mfma_f32_16x16x32_f16 v[130:133], v[18:21], v[2:5], v[130:133]
	s_waitcnt lgkmcnt(0)
	v_mfma_f32_16x16x32_f16 v[134:137], v[26:29], v[10:13], v[134:137]
	v_mfma_f32_16x16x32_f16 v[138:141], v[18:21], v[10:13], v[138:141]
	ds_read_b128 v[2:5], v151 offset:2880
	ds_read_b128 v[10:13], v151 offset:3488
	s_waitcnt lgkmcnt(1)
	v_mfma_f32_16x16x32_f16 v[142:145], v[26:29], v[2:5], v[142:145]
	v_mfma_f32_16x16x32_f16 v[146:149], v[18:21], v[2:5], v[146:149]
	s_waitcnt lgkmcnt(0)
	v_mfma_f32_16x16x32_f16 v[210:213], v[26:29], v[10:13], v[210:213]
	v_mfma_f32_16x16x32_f16 v[214:217], v[18:21], v[10:13], v[214:217]
	v_add_u32_e32 v2, 0xf6ac0, v244
	v_min_u32_e32 v2, v2, v157
	global_load_dwordx4 v[94:97], v2, s[8:9] nt
	s_waitcnt vmcnt(21)
	v_cvt_pk_f16_f32 v3, v104, v105
	v_cvt_pk_f16_f32 v2, v102, v103
	ds_write_b16 v238, v2 offset:6688
	ds_write_b16_d16_hi v239, v2 offset:6688
	ds_write_b16 v240, v3 offset:6688
	ds_write_b16_d16_hi v241, v3 offset:6688
	ds_read_b128 v[2:5], v151 offset:4096
	ds_read_b128 v[10:13], v151 offset:4704
	s_waitcnt lgkmcnt(1)
	v_mfma_f32_16x16x32_f16 v[166:169], v[26:29], v[2:5], v[166:169]
	v_mfma_f32_16x16x32_f16 v[158:161], v[18:21], v[2:5], v[158:161]
	s_waitcnt lgkmcnt(0)
	v_mfma_f32_16x16x32_f16 v[170:173], v[26:29], v[10:13], v[170:173]
	v_mfma_f32_16x16x32_f16 v[162:165], v[18:21], v[10:13], v[162:165]
	ds_read_b128 v[2:5], v151 offset:5312
	ds_read_b128 v[10:13], v151 offset:5920
	s_waitcnt lgkmcnt(1)
	v_mfma_f32_16x16x32_f16 v[174:177], v[26:29], v[2:5], v[174:177]
	v_mfma_f32_16x16x32_f16 v[178:181], v[18:21], v[2:5], v[178:181]
	s_waitcnt lgkmcnt(0)
	v_mfma_f32_16x16x32_f16 v[186:189], v[26:29], v[10:13], v[186:189]
	v_mfma_f32_16x16x32_f16 v[190:193], v[18:21], v[10:13], v[190:193]
	v_add_u32_e32 v2, 0x10d100, v150
	v_min_u32_e32 v2, v2, v157
	v_cndmask_b32_e64 v2, 0, v2, s[0:1]
	global_load_dwordx4 v[98:101], v2, s[8:9] nt
	s_waitcnt vmcnt(21)
	v_cvt_pk_f16_f32 v3, v108, v109
	v_cvt_pk_f16_f32 v2, v106, v107
	ds_write_b16 v234, v2 offset:7296
	ds_write_b16_d16_hi v235, v2 offset:7296
	ds_write_b16 v236, v3 offset:7296
	ds_write_b16_d16_hi v237, v3 offset:7296
	ds_read_b128 v[2:5], v151 offset:6528
	ds_read_b128 v[10:13], v151 offset:7136
	s_mov_b32 s2, 0x30000
	ds_read_b128 v[102:105], v151 offset:7744
	s_waitcnt lgkmcnt(0)
	v_mfma_f32_16x16x32_f16 v[194:197], v[26:29], v[2:5], v[194:197]
	s_barrier
	v_sub_u32_e32 v245, v234, v243
	v_add_u32_e32 v246, 0xfffffdc0, v245
	v_min_u32_e32 v245, v245, v246
	v_add_u32_e32 v234, v242, v245
	v_sub_u32_e32 v245, v235, v243
	v_add_u32_e32 v246, 0xfffffdc0, v245
	v_min_u32_e32 v245, v245, v246
	v_add_u32_e32 v235, v242, v245
	v_sub_u32_e32 v245, v236, v243
	v_add_u32_e32 v246, 0xfffffdc0, v245
	v_min_u32_e32 v245, v245, v246
	v_add_u32_e32 v236, v242, v245
	v_sub_u32_e32 v245, v237, v243
	v_add_u32_e32 v246, 0xfffffdc0, v245
	v_min_u32_e32 v245, v245, v246
	v_add_u32_e32 v237, v242, v245
	v_sub_u32_e32 v245, v238, v243
	v_add_u32_e32 v246, 0xfffffdc0, v245
	v_min_u32_e32 v245, v245, v246
	v_add_u32_e32 v238, v242, v245
	v_sub_u32_e32 v245, v239, v243
	v_add_u32_e32 v246, 0xfffffdc0, v245
	v_min_u32_e32 v245, v245, v246
	v_add_u32_e32 v239, v242, v245
	v_sub_u32_e32 v245, v240, v243
	v_add_u32_e32 v246, 0xfffffdc0, v245
	v_min_u32_e32 v245, v245, v246
	v_add_u32_e32 v240, v242, v245
	v_sub_u32_e32 v245, v241, v243
	v_add_u32_e32 v246, 0xfffffdc0, v245
	v_min_u32_e32 v245, v245, v246
	v_add_u32_e32 v241, v242, v245
	v_mfma_f32_16x16x32_f16 v[182:185], v[18:21], v[2:5], v[182:185]
	v_add_co_u32_e32 v2, vcc, s2, v152
	s_mov_b32 s2, 0x34000
	s_nop 0
	v_addc_co_u32_e32 v3, vcc, 0, v153, vcc
	global_load_dwordx4 v[38:41], v[2:3], off sc1
	global_load_dwordx4 v[50:53], v[2:3], off offset:256 sc1
	v_add_co_u32_e32 v2, vcc, s2, v152
	v_mfma_f32_16x16x32_f16 v[202:205], v[26:29], v[10:13], v[202:205]
	s_nop 0
	v_addc_co_u32_e32 v3, vcc, 0, v153, vcc
	v_mfma_f32_16x16x32_f16 v[206:209], v[18:21], v[10:13], v[206:209]
	global_load_dwordx4 v[10:13], v[2:3], off sc1
	s_nop 0
	global_load_dwordx4 v[2:5], v[2:3], off offset:256 sc1
	v_mfma_f32_16x16x32_f16 v[26:29], v[26:29], v[102:105], v[218:221]
	v_mfma_f32_16x16x32_f16 v[18:21], v[18:21], v[102:105], v[54:57]
	v_add_u32_e32 v157, 0x11151cdc, v154
	s_nop 1
	ds_read_b128 v[54:57], v151 offset:512
	v_add_u32_e32 v102, 0x800, v150
	s_waitcnt vmcnt(24) lgkmcnt(0)
	v_mfma_f32_16x16x32_f16 v[198:201], v[42:45], v[54:57], v[198:201]
	s_waitcnt vmcnt(23)
	v_mfma_f32_16x16x32_f16 v[54:57], v[46:49], v[54:57], v[222:225]
	v_min_u32_e32 v102, v102, v157
	global_load_dwordx4 v[102:105], v102, s[8:9] nt
	s_waitcnt vmcnt(21)
	v_cvt_pk_f16_f32 v107, v112, v113
	v_cvt_pk_f16_f32 v106, v110, v111
	ds_write_b16 v234, v106 offset:0
	ds_write_b16_d16_hi v235, v106 offset:0
	ds_write_b16 v236, v107 offset:0
	ds_write_b16_d16_hi v237, v107 offset:0
	ds_read_b128 v[106:109], v151 offset:1120
	ds_read_b128 v[110:113], v151 offset:1728
	s_waitcnt lgkmcnt(1)
	v_mfma_f32_16x16x32_f16 v[218:221], v[42:45], v[106:109], v[226:229]
	v_mfma_f32_16x16x32_f16 v[122:125], v[46:49], v[106:109], v[122:125]
	s_waitcnt lgkmcnt(0)
	v_mfma_f32_16x16x32_f16 v[126:129], v[42:45], v[110:113], v[126:129]
	v_mfma_f32_16x16x32_f16 v[130:133], v[46:49], v[110:113], v[130:133]
	ds_read_b128 v[106:109], v151 offset:2336
	ds_read_b128 v[110:113], v151 offset:2944
	s_waitcnt lgkmcnt(1)
	v_mfma_f32_16x16x32_f16 v[134:137], v[42:45], v[106:109], v[134:137]
	v_mfma_f32_16x16x32_f16 v[138:141], v[46:49], v[106:109], v[138:141]
	s_waitcnt lgkmcnt(0)
	v_mfma_f32_16x16x32_f16 v[142:145], v[42:45], v[110:113], v[142:145]
	v_mfma_f32_16x16x32_f16 v[146:149], v[46:49], v[110:113], v[146:149]
	v_add_u32_e32 v106, 0x16e40, v244
	v_min_u32_e32 v106, v106, v157
	global_load_dwordx4 v[106:109], v106, s[8:9] nt
	s_waitcnt vmcnt(21)
	v_cvt_pk_f16_f32 v111, v116, v117
	v_cvt_pk_f16_f32 v110, v114, v115
	ds_write_b16 v238, v110 offset:608
	ds_write_b16_d16_hi v239, v110 offset:608
	ds_write_b16 v240, v111 offset:608
	ds_write_b16_d16_hi v241, v111 offset:608
	ds_read_b128 v[110:113], v151 offset:3552
	ds_read_b128 v[114:117], v151 offset:5376
	s_waitcnt lgkmcnt(1)
	v_mfma_f32_16x16x32_f16 v[210:213], v[42:45], v[110:113], v[210:213]
	v_mfma_f32_16x16x32_f16 v[214:217], v[46:49], v[110:113], v[214:217]
	ds_read_b128 v[110:113], v151 offset:4160
	ds_read_b128 v[222:225], v151 offset:4768
	s_waitcnt lgkmcnt(1)
	v_mfma_f32_16x16x32_f16 v[166:169], v[42:45], v[110:113], v[166:169]
	v_mfma_f32_16x16x32_f16 v[158:161], v[46:49], v[110:113], v[158:161]
	s_waitcnt lgkmcnt(0)
	v_mfma_f32_16x16x32_f16 v[170:173], v[42:45], v[222:225], v[170:173]
	v_mfma_f32_16x16x32_f16 v[162:165], v[46:49], v[222:225], v[162:165]
	v_mfma_f32_16x16x32_f16 v[174:177], v[42:45], v[114:117], v[174:177]
	v_mfma_f32_16x16x32_f16 v[178:181], v[46:49], v[114:117], v[178:181]
	v_add_u32_e32 v110, 0x2d480, v150
	v_min_u32_e32 v110, v110, v157
	global_load_dwordx4 v[110:113], v110, s[8:9] nt
	s_waitcnt vmcnt(21)
	v_cvt_pk_f16_f32 v115, v120, v121
	v_cvt_pk_f16_f32 v114, v118, v119
	ds_write_b16 v234, v114 offset:1216
	ds_write_b16_d16_hi v235, v114 offset:1216
	ds_write_b16 v236, v115 offset:1216
	ds_write_b16_d16_hi v237, v115 offset:1216
	ds_read_b128 v[114:117], v151 offset:5984
	ds_read_b128 v[118:121], v151 offset:6592
	s_waitcnt lgkmcnt(1)
	v_mfma_f32_16x16x32_f16 v[186:189], v[42:45], v[114:117], v[186:189]
	v_mfma_f32_16x16x32_f16 v[190:193], v[46:49], v[114:117], v[190:193]
	s_waitcnt lgkmcnt(0)
	v_mfma_f32_16x16x32_f16 v[194:197], v[42:45], v[118:121], v[194:197]
	v_mfma_f32_16x16x32_f16 v[182:185], v[46:49], v[118:121], v[182:185]
	ds_read_b128 v[114:117], v151 offset:7200
	ds_read_b128 v[118:121], v151 offset:7808
	s_waitcnt lgkmcnt(1)
	v_mfma_f32_16x16x32_f16 v[202:205], v[42:45], v[114:117], v[202:205]
	v_mfma_f32_16x16x32_f16 v[206:209], v[46:49], v[114:117], v[206:209]
	s_waitcnt lgkmcnt(0)
	v_mfma_f32_16x16x32_f16 v[26:29], v[42:45], v[118:121], v[26:29]
	v_mfma_f32_16x16x32_f16 v[42:45], v[46:49], v[118:121], v[18:21]
	s_nop 2
	v_add_u32_e32 v18, 0x43ac0, v244
	v_min_u32_e32 v18, v18, v157
	global_load_dwordx4 v[114:117], v18, s[8:9] nt
	s_waitcnt vmcnt(21)
	v_cvt_pk_f16_f32 v19, v36, v37
	v_cvt_pk_f16_f32 v18, v34, v35
	ds_write_b16 v238, v18 offset:1824
	ds_write_b16_d16_hi v239, v18 offset:1824
	ds_write_b16 v240, v19 offset:1824
	ds_write_b16_d16_hi v241, v19 offset:1824
	ds_read_b128 v[18:21], v151 offset:0
	ds_read_b128 v[34:37], v151 offset:608
	s_waitcnt lgkmcnt(1)
	v_mfma_f32_16x16x32_f16 v[46:49], v[22:25], v[18:21], v[198:201]
	v_mfma_f32_16x16x32_f16 v[198:201], v[6:9], v[18:21], v[54:57]
	s_waitcnt lgkmcnt(0)
	v_mfma_f32_16x16x32_f16 v[218:221], v[22:25], v[34:37], v[218:221]
	v_mfma_f32_16x16x32_f16 v[222:225], v[6:9], v[34:37], v[122:125]
	ds_read_b128 v[18:21], v151 offset:1216
	ds_read_b128 v[34:37], v151 offset:1824
	s_waitcnt lgkmcnt(1)
	v_mfma_f32_16x16x32_f16 v[126:129], v[22:25], v[18:21], v[126:129]
	v_mfma_f32_16x16x32_f16 v[130:133], v[6:9], v[18:21], v[130:133]
	s_waitcnt lgkmcnt(0)
	v_mfma_f32_16x16x32_f16 v[134:137], v[22:25], v[34:37], v[134:137]
	v_mfma_f32_16x16x32_f16 v[138:141], v[6:9], v[34:37], v[138:141]
	v_add_u32_e32 v18, 0x5a100, v150
	v_min_u32_e32 v18, v18, v157
	global_load_dwordx4 v[118:121], v18, s[8:9] nt
	s_waitcnt vmcnt(21)
	v_cvt_pk_f16_f32 v19, v68, v69
	v_cvt_pk_f16_f32 v18, v66, v67
	ds_write_b16 v234, v18 offset:2432
	ds_write_b16_d16_hi v235, v18 offset:2432
	ds_write_b16 v236, v19 offset:2432
	ds_write_b16_d16_hi v237, v19 offset:2432
	ds_read_b128 v[18:21], v151 offset:2432
	ds_read_b128 v[34:37], v151 offset:3040
	s_waitcnt lgkmcnt(1)
	v_mfma_f32_16x16x32_f16 v[142:145], v[22:25], v[18:21], v[142:145]
	v_mfma_f32_16x16x32_f16 v[146:149], v[6:9], v[18:21], v[146:149]
	s_waitcnt lgkmcnt(0)
	v_mfma_f32_16x16x32_f16 v[210:213], v[22:25], v[34:37], v[210:213]
	v_mfma_f32_16x16x32_f16 v[214:217], v[6:9], v[34:37], v[214:217]
	ds_read_b128 v[18:21], v151 offset:3648
	ds_read_b128 v[34:37], v151 offset:4256
	s_waitcnt lgkmcnt(1)
	v_mfma_f32_16x16x32_f16 v[166:169], v[22:25], v[18:21], v[166:169]
	v_mfma_f32_16x16x32_f16 v[158:161], v[6:9], v[18:21], v[158:161]
	s_waitcnt lgkmcnt(0)
	v_mfma_f32_16x16x32_f16 v[170:173], v[22:25], v[34:37], v[170:173]
	v_mfma_f32_16x16x32_f16 v[162:165], v[6:9], v[34:37], v[162:165]
	v_add_u32_e32 v18, 0x70740, v244
	v_min_u32_e32 v18, v18, v157
	global_load_dwordx4 v[122:125], v18, s[8:9] nt
	s_waitcnt vmcnt(21)
	v_cvt_pk_f16_f32 v19, v72, v73
	v_cvt_pk_f16_f32 v18, v70, v71
	ds_write_b16 v238, v18 offset:3040
	ds_write_b16_d16_hi v239, v18 offset:3040
	ds_write_b16 v240, v19 offset:3040
	ds_write_b16_d16_hi v241, v19 offset:3040
	ds_read_b128 v[18:21], v151 offset:4864
	ds_read_b128 v[34:37], v151 offset:5472
	s_waitcnt lgkmcnt(1)
	v_mfma_f32_16x16x32_f16 v[174:177], v[22:25], v[18:21], v[174:177]
	v_mfma_f32_16x16x32_f16 v[178:181], v[6:9], v[18:21], v[178:181]
	s_waitcnt lgkmcnt(0)
	v_mfma_f32_16x16x32_f16 v[186:189], v[22:25], v[34:37], v[186:189]
	v_mfma_f32_16x16x32_f16 v[190:193], v[6:9], v[34:37], v[190:193]
	ds_read_b128 v[18:21], v151 offset:6080
	ds_read_b128 v[34:37], v151 offset:6688
	s_waitcnt lgkmcnt(1)
	v_mfma_f32_16x16x32_f16 v[194:197], v[22:25], v[18:21], v[194:197]
	v_mfma_f32_16x16x32_f16 v[182:185], v[6:9], v[18:21], v[182:185]
	s_waitcnt lgkmcnt(0)
	v_mfma_f32_16x16x32_f16 v[202:205], v[22:25], v[34:37], v[202:205]
	v_mfma_f32_16x16x32_f16 v[206:209], v[6:9], v[34:37], v[206:209]
	v_add_u32_e32 v18, 0x86d80, v150
	v_min_u32_e32 v18, v18, v157
	global_load_dwordx4 v[70:73], v18, s[8:9] nt
	s_waitcnt vmcnt(21)
	v_cvt_pk_f16_f32 v19, v76, v77
	v_cvt_pk_f16_f32 v18, v74, v75
	ds_write_b16 v234, v18 offset:3648
	ds_write_b16_d16_hi v235, v18 offset:3648
	ds_write_b16 v236, v19 offset:3648
	ds_write_b16_d16_hi v237, v19 offset:3648
	s_mov_b32 s2, 0x38000
	v_add_co_u32_e32 v18, vcc, s2, v152
	s_mov_b32 s2, 0x3c000
	s_nop 0
	v_addc_co_u32_e32 v19, vcc, 0, v153, vcc
	ds_read_b128 v[74:77], v151 offset:7296
	global_load_dwordx4 v[54:57], v[18:19], off sc1
	global_load_dwordx4 v[66:69], v[18:19], off offset:256 sc1
	v_add_co_u32_e32 v18, vcc, s2, v152
	s_waitcnt lgkmcnt(0)
	v_mfma_f32_16x16x32_f16 v[22:25], v[22:25], v[74:77], v[26:29]
	v_addc_co_u32_e32 v19, vcc, 0, v153, vcc
	global_load_dwordx4 v[34:37], v[18:19], off sc1
	s_nop 0
	global_load_dwordx4 v[18:21], v[18:19], off offset:256 sc1
	v_mfma_f32_16x16x32_f16 v[6:9], v[6:9], v[74:77], v[42:45]
	ds_read_b128 v[26:29], v151 offset:64
	s_nop 1
	ds_read_b128 v[42:45], v151 offset:672
	s_waitcnt vmcnt(24) lgkmcnt(1)
	v_mfma_f32_16x16x32_f16 v[46:49], v[58:61], v[26:29], v[46:49]
	s_waitcnt vmcnt(23)
	v_mfma_f32_16x16x32_f16 v[26:29], v[62:65], v[26:29], v[198:201]
	s_nop 2
	ds_read_b128 v[198:201], v151 offset:1280
	s_waitcnt lgkmcnt(1)
	v_mfma_f32_16x16x32_f16 v[74:77], v[58:61], v[42:45], v[218:221]
	v_mfma_f32_16x16x32_f16 v[42:45], v[62:65], v[42:45], v[222:225]
	s_waitcnt lgkmcnt(0)
	v_mfma_f32_16x16x32_f16 v[218:221], v[58:61], v[198:201], v[126:129]
	v_mfma_f32_16x16x32_f16 v[130:133], v[62:65], v[198:201], v[130:133]
	s_nop 1
	v_add_u32_e32 v126, 0x9d3c0, v244
	v_min_u32_e32 v126, v126, v157
	global_load_dwordx4 v[126:129], v126, s[8:9] nt
	s_waitcnt vmcnt(21)
	v_cvt_pk_f16_f32 v81, v80, v81
	v_cvt_pk_f16_f32 v80, v78, v79
	ds_write_b16 v238, v80 offset:4256
	ds_write_b16_d16_hi v239, v80 offset:4256
	ds_write_b16 v240, v81 offset:4256
	ds_write_b16_d16_hi v241, v81 offset:4256
	ds_read_b128 v[78:81], v151 offset:1888
	ds_read_b128 v[198:201], v151 offset:2496
	s_waitcnt lgkmcnt(1)
	v_mfma_f32_16x16x32_f16 v[134:137], v[58:61], v[78:81], v[134:137]
	v_mfma_f32_16x16x32_f16 v[138:141], v[62:65], v[78:81], v[138:141]
	s_waitcnt lgkmcnt(0)
	v_mfma_f32_16x16x32_f16 v[142:145], v[58:61], v[198:201], v[142:145]
	v_mfma_f32_16x16x32_f16 v[146:149], v[62:65], v[198:201], v[146:149]
	ds_read_b128 v[78:81], v151 offset:3104
	ds_read_b128 v[198:201], v151 offset:3712
	s_waitcnt lgkmcnt(1)
	v_mfma_f32_16x16x32_f16 v[210:213], v[58:61], v[78:81], v[210:213]
	v_mfma_f32_16x16x32_f16 v[214:217], v[62:65], v[78:81], v[214:217]
	s_waitcnt lgkmcnt(0)
	v_mfma_f32_16x16x32_f16 v[166:169], v[58:61], v[198:201], v[166:169]
	v_mfma_f32_16x16x32_f16 v[158:161], v[62:65], v[198:201], v[158:161]
	v_add_u32_e32 v78, 0xb3a00, v150
	v_min_u32_e32 v78, v78, v157
	global_load_dwordx4 v[78:81], v78, s[8:9] nt
	s_waitcnt vmcnt(21)
	v_cvt_pk_f16_f32 v85, v84, v85
	v_cvt_pk_f16_f32 v84, v82, v83
	ds_write_b16 v234, v84 offset:4864
	ds_write_b16_d16_hi v235, v84 offset:4864
	ds_write_b16 v236, v85 offset:4864
	ds_write_b16_d16_hi v237, v85 offset:4864
	ds_read_b128 v[82:85], v151 offset:4320
	ds_read_b128 v[198:201], v151 offset:6144
	s_waitcnt lgkmcnt(1)
	v_mfma_f32_16x16x32_f16 v[170:173], v[58:61], v[82:85], v[170:173]
	v_mfma_f32_16x16x32_f16 v[162:165], v[62:65], v[82:85], v[162:165]
	ds_read_b128 v[82:85], v151 offset:4928
	ds_read_b128 v[222:225], v151 offset:5536
	s_waitcnt lgkmcnt(1)
	v_mfma_f32_16x16x32_f16 v[174:177], v[58:61], v[82:85], v[174:177]
	v_mfma_f32_16x16x32_f16 v[178:181], v[62:65], v[82:85], v[178:181]
	s_waitcnt lgkmcnt(0)
	v_mfma_f32_16x16x32_f16 v[186:189], v[58:61], v[222:225], v[186:189]
	v_mfma_f32_16x16x32_f16 v[190:193], v[62:65], v[222:225], v[190:193]
	v_mfma_f32_16x16x32_f16 v[194:197], v[58:61], v[198:201], v[194:197]
	v_mfma_f32_16x16x32_f16 v[182:185], v[62:65], v[198:201], v[182:185]
	v_add_u32_e32 v82, 0xca040, v244
	v_min_u32_e32 v82, v82, v157
	global_load_dwordx4 v[82:85], v82, s[8:9] nt
	s_waitcnt vmcnt(21)
	v_cvt_pk_f16_f32 v89, v88, v89
	v_cvt_pk_f16_f32 v88, v86, v87
	ds_write_b16 v238, v88 offset:5472
	ds_write_b16_d16_hi v239, v88 offset:5472
	ds_write_b16 v240, v89 offset:5472
	ds_write_b16_d16_hi v241, v89 offset:5472
	ds_read_b128 v[86:89], v151 offset:6752
	ds_read_b128 v[198:201], v151 offset:7360
	s_waitcnt lgkmcnt(1)
	v_mfma_f32_16x16x32_f16 v[202:205], v[58:61], v[86:89], v[202:205]
	s_waitcnt lgkmcnt(0)
	v_mfma_f32_16x16x32_f16 v[22:25], v[58:61], v[198:201], v[22:25]
	v_mfma_f32_16x16x32_f16 v[198:201], v[62:65], v[198:201], v[6:9]
	s_nop 2
	ds_read_b128 v[6:9], v151 offset:128
	ds_read_b128 v[58:61], v151 offset:736
	v_mfma_f32_16x16x32_f16 v[206:209], v[62:65], v[86:89], v[206:209]
	s_waitcnt lgkmcnt(1)
	v_mfma_f32_16x16x32_f16 v[222:225], v[30:33], v[6:9], v[46:49]
	v_mfma_f32_16x16x32_f16 v[226:229], v[14:17], v[6:9], v[26:29]
	s_waitcnt lgkmcnt(0)
	v_mfma_f32_16x16x32_f16 v[74:77], v[30:33], v[58:61], v[74:77]
	v_mfma_f32_16x16x32_f16 v[230:233], v[14:17], v[58:61], v[42:45]
	v_add_u32_e32 v6, 0xe0680, v150
	v_min_u32_e32 v6, v6, v157
	global_load_dwordx4 v[58:61], v6, s[8:9] nt
	s_waitcnt vmcnt(21)
	v_cvt_pk_f16_f32 v7, v92, v93
	v_cvt_pk_f16_f32 v6, v90, v91
	ds_write_b16 v234, v6 offset:6080
	ds_write_b16_d16_hi v235, v6 offset:6080
	ds_write_b16 v236, v7 offset:6080
	ds_write_b16_d16_hi v237, v7 offset:6080
	ds_read_b128 v[6:9], v151 offset:1344
	ds_read_b128 v[26:29], v151 offset:1952
	s_waitcnt lgkmcnt(1)
	v_mfma_f32_16x16x32_f16 v[90:93], v[30:33], v[6:9], v[218:221]
	v_mfma_f32_16x16x32_f16 v[130:133], v[14:17], v[6:9], v[130:133]
	s_waitcnt lgkmcnt(0)
	v_mfma_f32_16x16x32_f16 v[134:137], v[30:33], v[26:29], v[134:137]
	v_mfma_f32_16x16x32_f16 v[138:141], v[14:17], v[26:29], v[138:141]
	ds_read_b128 v[6:9], v151 offset:2560
	ds_read_b128 v[26:29], v151 offset:3168
	s_waitcnt lgkmcnt(1)
	v_mfma_f32_16x16x32_f16 v[142:145], v[30:33], v[6:9], v[142:145]
	v_mfma_f32_16x16x32_f16 v[146:149], v[14:17], v[6:9], v[146:149]
	s_waitcnt lgkmcnt(0)
	v_mfma_f32_16x16x32_f16 v[210:213], v[30:33], v[26:29], v[210:213]
	v_mfma_f32_16x16x32_f16 v[214:217], v[14:17], v[26:29], v[214:217]
	v_add_u32_e32 v6, 0xf6cc0, v244
	v_min_u32_e32 v6, v6, v157
	global_load_dwordx4 v[62:65], v6, s[8:9] nt
	s_waitcnt vmcnt(21)
	v_cvt_pk_f16_f32 v7, v96, v97
	v_cvt_pk_f16_f32 v6, v94, v95
	ds_write_b16 v238, v6 offset:6688
	ds_write_b16_d16_hi v239, v6 offset:6688
	ds_write_b16 v240, v7 offset:6688
	ds_write_b16_d16_hi v241, v7 offset:6688
	ds_read_b128 v[6:9], v151 offset:3776
	ds_read_b128 v[26:29], v151 offset:4384
	s_waitcnt lgkmcnt(1)
	v_mfma_f32_16x16x32_f16 v[94:97], v[30:33], v[6:9], v[166:169]
	v_mfma_f32_16x16x32_f16 v[158:161], v[14:17], v[6:9], v[158:161]
	s_waitcnt lgkmcnt(0)
	v_mfma_f32_16x16x32_f16 v[166:169], v[30:33], v[26:29], v[170:173]
	v_mfma_f32_16x16x32_f16 v[162:165], v[14:17], v[26:29], v[162:165]
	ds_read_b128 v[6:9], v151 offset:4992
	ds_read_b128 v[26:29], v151 offset:5600
	s_waitcnt lgkmcnt(1)
	v_mfma_f32_16x16x32_f16 v[170:173], v[30:33], v[6:9], v[174:177]
	v_mfma_f32_16x16x32_f16 v[174:177], v[14:17], v[6:9], v[178:181]
	s_waitcnt lgkmcnt(0)
	v_mfma_f32_16x16x32_f16 v[178:181], v[30:33], v[26:29], v[186:189]
	v_mfma_f32_16x16x32_f16 v[186:189], v[14:17], v[26:29], v[190:193]
	v_add_u32_e32 v6, 0x10d300, v150
	v_min_u32_e32 v6, v6, v157
	v_cndmask_b32_e64 v6, 0, v6, s[0:1]
	global_load_dwordx4 v[86:89], v6, s[8:9] nt
	s_waitcnt vmcnt(21)
	v_cvt_pk_f16_f32 v7, v100, v101
	v_cvt_pk_f16_f32 v6, v98, v99
	ds_write_b16 v234, v6 offset:7296
	ds_write_b16_d16_hi v235, v6 offset:7296
	ds_write_b16 v236, v7 offset:7296
	ds_write_b16_d16_hi v237, v7 offset:7296
	ds_read_b128 v[6:9], v151 offset:6208
	ds_read_b128 v[26:29], v151 offset:6816
	s_mov_b32 s2, 0x40000
	ds_read_b128 v[190:193], v151 offset:7424
	s_waitcnt lgkmcnt(0)
	v_mfma_f32_16x16x32_f16 v[98:101], v[30:33], v[6:9], v[194:197]
	s_barrier
	v_sub_u32_e32 v245, v234, v243
	v_add_u32_e32 v246, 0xfffffdc0, v245
	v_min_u32_e32 v245, v245, v246
	v_add_u32_e32 v234, v242, v245
	v_sub_u32_e32 v245, v235, v243
	v_add_u32_e32 v246, 0xfffffdc0, v245
	v_min_u32_e32 v245, v245, v246
	v_add_u32_e32 v235, v242, v245
	v_sub_u32_e32 v245, v236, v243
	v_add_u32_e32 v246, 0xfffffdc0, v245
	v_min_u32_e32 v245, v245, v246
	v_add_u32_e32 v236, v242, v245
	v_sub_u32_e32 v245, v237, v243
	v_add_u32_e32 v246, 0xfffffdc0, v245
	v_min_u32_e32 v245, v245, v246
	v_add_u32_e32 v237, v242, v245
	v_sub_u32_e32 v245, v238, v243
	v_add_u32_e32 v246, 0xfffffdc0, v245
	v_min_u32_e32 v245, v245, v246
	v_add_u32_e32 v238, v242, v245
	v_sub_u32_e32 v245, v239, v243
	v_add_u32_e32 v246, 0xfffffdc0, v245
	v_min_u32_e32 v245, v245, v246
	v_add_u32_e32 v239, v242, v245
	v_sub_u32_e32 v245, v240, v243
	v_add_u32_e32 v246, 0xfffffdc0, v245
	v_min_u32_e32 v245, v245, v246
	v_add_u32_e32 v240, v242, v245
	v_sub_u32_e32 v245, v241, v243
	v_add_u32_e32 v246, 0xfffffdc0, v245
	v_min_u32_e32 v245, v245, v246
	v_add_u32_e32 v241, v242, v245
	v_mfma_f32_16x16x32_f16 v[182:185], v[14:17], v[6:9], v[182:185]
	v_add_co_u32_e32 v6, vcc, s2, v152
	s_mov_b32 s2, 0x44000
	s_nop 0
	v_addc_co_u32_e32 v7, vcc, 0, v153, vcc
	global_load_dwordx4 v[42:45], v[6:7], off sc1
	global_load_dwordx4 v[46:49], v[6:7], off offset:256 sc1
	v_add_co_u32_e32 v6, vcc, s2, v152
	v_mfma_f32_16x16x32_f16 v[194:197], v[30:33], v[26:29], v[202:205]
	s_nop 0
	v_addc_co_u32_e32 v7, vcc, 0, v153, vcc
	v_mfma_f32_16x16x32_f16 v[202:205], v[14:17], v[26:29], v[206:209]
	global_load_dwordx4 v[26:29], v[6:7], off sc1
	s_nop 0
	global_load_dwordx4 v[6:9], v[6:7], off offset:256 sc1
	v_mfma_f32_16x16x32_f16 v[22:25], v[30:33], v[190:193], v[22:25]
	v_mfma_f32_16x16x32_f16 v[30:33], v[14:17], v[190:193], v[198:201]
	v_add_u32_e32 v157, 0x11151edc, v154
	ds_read_b128 v[14:17], v151 offset:192
	v_add_u32_e32 v206, 0xa00, v150
	s_waitcnt vmcnt(24) lgkmcnt(0)
	v_mfma_f32_16x16x32_f16 v[190:193], v[38:41], v[14:17], v[222:225]
	s_waitcnt vmcnt(23)
	v_mfma_f32_16x16x32_f16 v[198:201], v[50:53], v[14:17], v[226:229]
	v_min_u32_e32 v14, v206, v157
	global_load_dwordx4 v[14:17], v14, s[8:9] nt
	s_waitcnt vmcnt(21)
	v_cvt_pk_f16_f32 v105, v104, v105
	v_cvt_pk_f16_f32 v104, v102, v103
	ds_write_b16 v234, v104 offset:0
	ds_write_b16_d16_hi v235, v104 offset:0
	ds_write_b16 v236, v105 offset:0
	ds_write_b16_d16_hi v237, v105 offset:0
	ds_read_b128 v[102:105], v151 offset:800
	ds_read_b128 v[206:209], v151 offset:1408
	s_waitcnt lgkmcnt(1)
	v_mfma_f32_16x16x32_f16 v[74:77], v[38:41], v[102:105], v[74:77]
	s_waitcnt lgkmcnt(0)
	v_mfma_f32_16x16x32_f16 v[218:221], v[38:41], v[206:209], v[90:93]
	v_mfma_f32_16x16x32_f16 v[130:133], v[50:53], v[206:209], v[130:133]
	s_nop 1
	ds_read_b128 v[90:93], v151 offset:2016
	ds_read_b128 v[206:209], v151 offset:2624
	v_mfma_f32_16x16x32_f16 v[102:105], v[50:53], v[102:105], v[230:233]
	s_waitcnt lgkmcnt(1)
	v_mfma_f32_16x16x32_f16 v[134:137], v[38:41], v[90:93], v[134:137]
	v_mfma_f32_16x16x32_f16 v[138:141], v[50:53], v[90:93], v[138:141]
	s_waitcnt lgkmcnt(0)
	v_mfma_f32_16x16x32_f16 v[142:145], v[38:41], v[206:209], v[142:145]
	v_mfma_f32_16x16x32_f16 v[146:149], v[50:53], v[206:209], v[146:149]
	v_add_u32_e32 v90, 0x17040, v244
	v_min_u32_e32 v90, v90, v157
	global_load_dwordx4 v[90:93], v90, s[8:9] nt
	s_waitcnt vmcnt(21)
	v_cvt_pk_f16_f32 v109, v108, v109
	v_cvt_pk_f16_f32 v108, v106, v107
	ds_write_b16 v238, v108 offset:608
	ds_write_b16_d16_hi v239, v108 offset:608
	ds_write_b16 v240, v109 offset:608
	ds_write_b16_d16_hi v241, v109 offset:608
	ds_read_b128 v[106:109], v151 offset:3232
	ds_read_b128 v[206:209], v151 offset:5056
	s_waitcnt lgkmcnt(1)
	v_mfma_f32_16x16x32_f16 v[210:213], v[38:41], v[106:109], v[210:213]
	v_mfma_f32_16x16x32_f16 v[106:109], v[50:53], v[106:109], v[214:217]
	s_nop 2
	ds_read_b128 v[214:217], v151 offset:3840
	ds_read_b128 v[222:225], v151 offset:4448
	s_waitcnt lgkmcnt(1)
	v_mfma_f32_16x16x32_f16 v[226:229], v[38:41], v[214:217], v[94:97]
	v_mfma_f32_16x16x32_f16 v[158:161], v[50:53], v[214:217], v[158:161]
	s_waitcnt lgkmcnt(0)
	v_mfma_f32_16x16x32_f16 v[166:169], v[38:41], v[222:225], v[166:169]
	v_mfma_f32_16x16x32_f16 v[162:165], v[50:53], v[222:225], v[162:165]
	v_mfma_f32_16x16x32_f16 v[170:173], v[38:41], v[206:209], v[170:173]
	v_mfma_f32_16x16x32_f16 v[174:177], v[50:53], v[206:209], v[174:177]
	v_add_u32_e32 v94, 0x2d680, v150
	v_min_u32_e32 v94, v94, v157
	global_load_dwordx4 v[94:97], v94, s[8:9] nt
	s_waitcnt vmcnt(21)
	v_cvt_pk_f16_f32 v113, v112, v113
	v_cvt_pk_f16_f32 v112, v110, v111
	ds_write_b16 v234, v112 offset:1216
	ds_write_b16_d16_hi v235, v112 offset:1216
	ds_write_b16 v236, v113 offset:1216
	ds_write_b16_d16_hi v237, v113 offset:1216
	ds_read_b128 v[110:113], v151 offset:5664
	ds_read_b128 v[206:209], v151 offset:6272
	s_waitcnt lgkmcnt(1)
	v_mfma_f32_16x16x32_f16 v[178:181], v[38:41], v[110:113], v[178:181]
	v_mfma_f32_16x16x32_f16 v[110:113], v[50:53], v[110:113], v[186:189]
	s_waitcnt lgkmcnt(0)
	v_mfma_f32_16x16x32_f16 v[186:189], v[38:41], v[206:209], v[98:101]
	v_mfma_f32_16x16x32_f16 v[182:185], v[50:53], v[206:209], v[182:185]
	s_nop 1
	ds_read_b128 v[98:101], v151 offset:6880
	ds_read_b128 v[206:209], v151 offset:7488
	s_waitcnt lgkmcnt(1)
	v_mfma_f32_16x16x32_f16 v[194:197], v[38:41], v[98:101], v[194:197]
	v_mfma_f32_16x16x32_f16 v[202:205], v[50:53], v[98:101], v[202:205]
	s_waitcnt lgkmcnt(0)
	v_mfma_f32_16x16x32_f16 v[22:25], v[38:41], v[206:209], v[22:25]
	v_mfma_f32_16x16x32_f16 v[30:33], v[50:53], v[206:209], v[30:33]
	v_add_u32_e32 v38, 0x43cc0, v244
	v_min_u32_e32 v38, v38, v157
	global_load_dwordx4 v[98:101], v38, s[8:9] nt
	s_waitcnt vmcnt(21)
	v_cvt_pk_f16_f32 v39, v116, v117
	v_cvt_pk_f16_f32 v38, v114, v115
	ds_write_b16 v238, v38 offset:1824
	ds_write_b16_d16_hi v239, v38 offset:1824
	ds_write_b16 v240, v39 offset:1824
	ds_write_b16_d16_hi v241, v39 offset:1824
	ds_read_b128 v[38:41], v151 offset:256
	ds_read_b128 v[50:53], v151 offset:864
	s_waitcnt lgkmcnt(1)
	v_mfma_f32_16x16x32_f16 v[114:117], v[10:13], v[38:41], v[190:193]
	v_mfma_f32_16x16x32_f16 v[190:193], v[2:5], v[38:41], v[198:201]
	s_waitcnt lgkmcnt(0)
	v_mfma_f32_16x16x32_f16 v[198:201], v[10:13], v[50:53], v[74:77]
	ds_read_b128 v[38:41], v151 offset:1472
	s_nop 1
	ds_read_b128 v[74:77], v151 offset:2080
	v_mfma_f32_16x16x32_f16 v[50:53], v[2:5], v[50:53], v[102:105]
	s_waitcnt lgkmcnt(1)
	v_mfma_f32_16x16x32_f16 v[206:209], v[10:13], v[38:41], v[218:221]
	v_mfma_f32_16x16x32_f16 v[130:133], v[2:5], v[38:41], v[130:133]
	s_waitcnt lgkmcnt(0)
	v_mfma_f32_16x16x32_f16 v[134:137], v[10:13], v[74:77], v[134:137]
	v_mfma_f32_16x16x32_f16 v[138:141], v[2:5], v[74:77], v[138:141]
	v_add_u32_e32 v38, 0x5a300, v150
	v_min_u32_e32 v38, v38, v157
	global_load_dwordx4 v[102:105], v38, s[8:9] nt
	s_waitcnt vmcnt(21)
	v_cvt_pk_f16_f32 v39, v120, v121
	v_cvt_pk_f16_f32 v38, v118, v119
	ds_write_b16 v234, v38 offset:2432
	ds_write_b16_d16_hi v235, v38 offset:2432
	ds_write_b16 v236, v39 offset:2432
	ds_write_b16_d16_hi v237, v39 offset:2432
	ds_read_b128 v[38:41], v151 offset:2688
	ds_read_b128 v[74:77], v151 offset:3296
	s_waitcnt lgkmcnt(1)
	v_mfma_f32_16x16x32_f16 v[118:121], v[10:13], v[38:41], v[142:145]
	v_mfma_f32_16x16x32_f16 v[142:145], v[2:5], v[38:41], v[146:149]
	s_waitcnt lgkmcnt(0)
	v_mfma_f32_16x16x32_f16 v[146:149], v[10:13], v[74:77], v[210:213]
	v_mfma_f32_16x16x32_f16 v[210:213], v[2:5], v[74:77], v[106:109]
	ds_read_b128 v[38:41], v151 offset:3904
	ds_read_b128 v[74:77], v151 offset:4512
	s_waitcnt lgkmcnt(1)
	v_mfma_f32_16x16x32_f16 v[214:217], v[10:13], v[38:41], v[226:229]
	v_mfma_f32_16x16x32_f16 v[158:161], v[2:5], v[38:41], v[158:161]
	s_waitcnt lgkmcnt(0)
	v_mfma_f32_16x16x32_f16 v[166:169], v[10:13], v[74:77], v[166:169]
	v_mfma_f32_16x16x32_f16 v[162:165], v[2:5], v[74:77], v[162:165]
	v_add_u32_e32 v38, 0x70940, v244
	v_min_u32_e32 v38, v38, v157
	global_load_dwordx4 v[106:109], v38, s[8:9] nt
	s_waitcnt vmcnt(21)
	v_cvt_pk_f16_f32 v39, v124, v125
	v_cvt_pk_f16_f32 v38, v122, v123
	ds_write_b16 v238, v38 offset:3040
	ds_write_b16_d16_hi v239, v38 offset:3040
	ds_write_b16 v240, v39 offset:3040
	ds_write_b16_d16_hi v241, v39 offset:3040
	ds_read_b128 v[38:41], v151 offset:5120
	ds_read_b128 v[74:77], v151 offset:5728
	s_waitcnt lgkmcnt(1)
	v_mfma_f32_16x16x32_f16 v[122:125], v[10:13], v[38:41], v[170:173]
	v_mfma_f32_16x16x32_f16 v[170:173], v[2:5], v[38:41], v[174:177]
	s_waitcnt lgkmcnt(0)
	v_mfma_f32_16x16x32_f16 v[174:177], v[10:13], v[74:77], v[178:181]
	v_mfma_f32_16x16x32_f16 v[178:181], v[2:5], v[74:77], v[110:113]
	ds_read_b128 v[38:41], v151 offset:6336
	ds_read_b128 v[74:77], v151 offset:6944
	s_waitcnt lgkmcnt(1)
	v_mfma_f32_16x16x32_f16 v[186:189], v[10:13], v[38:41], v[186:189]
	v_mfma_f32_16x16x32_f16 v[182:185], v[2:5], v[38:41], v[182:185]
	s_waitcnt lgkmcnt(0)
	v_mfma_f32_16x16x32_f16 v[194:197], v[10:13], v[74:77], v[194:197]
	v_mfma_f32_16x16x32_f16 v[202:205], v[2:5], v[74:77], v[202:205]
	v_add_u32_e32 v38, 0x86f80, v150
	v_min_u32_e32 v38, v38, v157
	global_load_dwordx4 v[110:113], v38, s[8:9] nt
	s_waitcnt vmcnt(21)
	v_cvt_pk_f16_f32 v39, v72, v73
	v_cvt_pk_f16_f32 v38, v70, v71
	ds_write_b16 v234, v38 offset:3648
	ds_write_b16_d16_hi v235, v38 offset:3648
	ds_write_b16 v236, v39 offset:3648
	ds_write_b16_d16_hi v237, v39 offset:3648
	ds_read_b128 v[218:221], v151 offset:7552
	s_mov_b32 s2, 0x48000
	s_waitcnt lgkmcnt(0)
	v_mfma_f32_16x16x32_f16 v[10:13], v[10:13], v[218:221], v[22:25]
	s_nop 2
	v_add_co_u32_e32 v22, vcc, s2, v152
	s_mov_b32 s2, 0x4c000
	s_nop 0
	v_addc_co_u32_e32 v23, vcc, 0, v153, vcc
	global_load_dwordx4 v[70:73], v[22:23], off sc1
	global_load_dwordx4 v[74:77], v[22:23], off offset:256 sc1
	v_add_co_u32_e32 v22, vcc, s2, v152
	v_mfma_f32_16x16x32_f16 v[30:33], v[2:5], v[218:221], v[30:33]
	s_nop 0
	v_addc_co_u32_e32 v23, vcc, 0, v153, vcc
	global_load_dwordx4 v[38:41], v[22:23], off sc1
	s_nop 0
	global_load_dwordx4 v[22:25], v[22:23], off offset:256 sc1
	ds_read_b128 v[2:5], v151 offset:320
	ds_read_b128 v[218:221], v151 offset:928
	s_waitcnt vmcnt(24) lgkmcnt(1)
	v_mfma_f32_16x16x32_f16 v[222:225], v[54:57], v[2:5], v[114:117]
	s_waitcnt vmcnt(23)
	v_mfma_f32_16x16x32_f16 v[190:193], v[66:69], v[2:5], v[190:193]
	ds_read_b128 v[2:5], v151 offset:1536
	s_waitcnt lgkmcnt(1)
	v_mfma_f32_16x16x32_f16 v[198:201], v[54:57], v[218:221], v[198:201]
	v_mfma_f32_16x16x32_f16 v[50:53], v[66:69], v[218:221], v[50:53]
	s_waitcnt lgkmcnt(0)
	v_mfma_f32_16x16x32_f16 v[206:209], v[54:57], v[2:5], v[206:209]
	v_mfma_f32_16x16x32_f16 v[130:133], v[66:69], v[2:5], v[130:133]
	v_add_u32_e32 v2, 0x9d5c0, v244
	v_min_u32_e32 v2, v2, v157
	global_load_dwordx4 v[2:5], v2, s[8:9] nt
	s_waitcnt vmcnt(21)
	v_cvt_pk_f16_f32 v115, v128, v129
	v_cvt_pk_f16_f32 v114, v126, v127
	ds_write_b16 v238, v114 offset:4256
	ds_write_b16_d16_hi v239, v114 offset:4256
	ds_write_b16 v240, v115 offset:4256
	ds_write_b16_d16_hi v241, v115 offset:4256
	ds_read_b128 v[114:117], v151 offset:2144
	ds_read_b128 v[126:129], v151 offset:2752
	s_waitcnt lgkmcnt(1)
	v_mfma_f32_16x16x32_f16 v[134:137], v[54:57], v[114:117], v[134:137]
	v_mfma_f32_16x16x32_f16 v[138:141], v[66:69], v[114:117], v[138:141]
	s_waitcnt lgkmcnt(0)
	v_mfma_f32_16x16x32_f16 v[118:121], v[54:57], v[126:129], v[118:121]
	v_mfma_f32_16x16x32_f16 v[126:129], v[66:69], v[126:129], v[142:145]
	ds_read_b128 v[114:117], v151 offset:3360
	s_nop 1
	ds_read_b128 v[142:145], v151 offset:3968
	s_waitcnt lgkmcnt(1)
	v_mfma_f32_16x16x32_f16 v[146:149], v[54:57], v[114:117], v[146:149]
	v_mfma_f32_16x16x32_f16 v[210:213], v[66:69], v[114:117], v[210:213]
	s_waitcnt lgkmcnt(0)
	v_mfma_f32_16x16x32_f16 v[214:217], v[54:57], v[142:145], v[214:217]
	v_mfma_f32_16x16x32_f16 v[142:145], v[66:69], v[142:145], v[158:161]
	v_add_u32_e32 v114, 0xb3c00, v150
	v_min_u32_e32 v114, v114, v157
	global_load_dwordx4 v[114:117], v114, s[8:9] nt
	s_waitcnt vmcnt(21)
	v_cvt_pk_f16_f32 v81, v80, v81
	v_cvt_pk_f16_f32 v80, v78, v79
	ds_write_b16 v234, v80 offset:4864
	ds_write_b16_d16_hi v235, v80 offset:4864
	ds_write_b16 v236, v81 offset:4864
	ds_write_b16_d16_hi v237, v81 offset:4864
	ds_read_b128 v[78:81], v151 offset:4576
	ds_read_b128 v[158:161], v151 offset:6400
	s_waitcnt lgkmcnt(1)
	v_mfma_f32_16x16x32_f16 v[166:169], v[54:57], v[78:81], v[166:169]
	v_mfma_f32_16x16x32_f16 v[162:165], v[66:69], v[78:81], v[162:165]
	ds_read_b128 v[78:81], v151 offset:5184
	ds_read_b128 v[218:221], v151 offset:5792
	s_waitcnt lgkmcnt(1)
	v_mfma_f32_16x16x32_f16 v[122:125], v[54:57], v[78:81], v[122:125]
	v_mfma_f32_16x16x32_f16 v[170:173], v[66:69], v[78:81], v[170:173]
	s_waitcnt lgkmcnt(0)
	v_mfma_f32_16x16x32_f16 v[174:177], v[54:57], v[218:221], v[174:177]
	v_mfma_f32_16x16x32_f16 v[178:181], v[66:69], v[218:221], v[178:181]
	v_mfma_f32_16x16x32_f16 v[186:189], v[54:57], v[158:161], v[186:189]
	v_mfma_f32_16x16x32_f16 v[158:161], v[66:69], v[158:161], v[182:185]
	v_add_u32_e32 v78, 0xca240, v244
	v_min_u32_e32 v78, v78, v157
	global_load_dwordx4 v[78:81], v78, s[8:9] nt
	s_waitcnt vmcnt(21)
	v_cvt_pk_f16_f32 v85, v84, v85
	v_cvt_pk_f16_f32 v84, v82, v83
	ds_write_b16 v238, v84 offset:5472
	ds_write_b16_d16_hi v239, v84 offset:5472
	ds_write_b16 v240, v85 offset:5472
	ds_write_b16_d16_hi v241, v85 offset:5472
	ds_read_b128 v[82:85], v151 offset:7008
	ds_read_b128 v[182:185], v151 offset:7616
	s_waitcnt lgkmcnt(1)
	v_mfma_f32_16x16x32_f16 v[194:197], v[54:57], v[82:85], v[194:197]
	s_waitcnt lgkmcnt(0)
	v_mfma_f32_16x16x32_f16 v[10:13], v[54:57], v[182:185], v[10:13]
	v_mfma_f32_16x16x32_f16 v[182:185], v[66:69], v[182:185], v[30:33]
	s_nop 2
	ds_read_b128 v[30:33], v151 offset:384
	ds_read_b128 v[54:57], v151 offset:992
	v_mfma_f32_16x16x32_f16 v[202:205], v[66:69], v[82:85], v[202:205]
	s_waitcnt lgkmcnt(1)
	v_mfma_f32_16x16x32_f16 v[218:221], v[34:37], v[30:33], v[222:225]
	v_mfma_f32_16x16x32_f16 v[190:193], v[18:21], v[30:33], v[190:193]
	s_waitcnt lgkmcnt(0)
	v_mfma_f32_16x16x32_f16 v[198:201], v[34:37], v[54:57], v[198:201]
	v_mfma_f32_16x16x32_f16 v[222:225], v[18:21], v[54:57], v[50:53]
	v_add_u32_e32 v30, 0xe0880, v150
	v_min_u32_e32 v30, v30, v157
	global_load_dwordx4 v[66:69], v30, s[8:9] nt
	s_waitcnt vmcnt(21)
	v_cvt_pk_f16_f32 v31, v60, v61
	v_cvt_pk_f16_f32 v30, v58, v59
	ds_write_b16 v234, v30 offset:6080
	ds_write_b16_d16_hi v235, v30 offset:6080
	ds_write_b16 v236, v31 offset:6080
	ds_write_b16_d16_hi v237, v31 offset:6080
	ds_read_b128 v[30:33], v151 offset:1600
	ds_read_b128 v[50:53], v151 offset:2208
	s_waitcnt lgkmcnt(1)
	v_mfma_f32_16x16x32_f16 v[58:61], v[34:37], v[30:33], v[206:209]
	v_mfma_f32_16x16x32_f16 v[130:133], v[18:21], v[30:33], v[130:133]
	s_waitcnt lgkmcnt(0)
	v_mfma_f32_16x16x32_f16 v[134:137], v[34:37], v[50:53], v[134:137]
	v_mfma_f32_16x16x32_f16 v[138:141], v[18:21], v[50:53], v[138:141]
	ds_read_b128 v[30:33], v151 offset:2816
	ds_read_b128 v[50:53], v151 offset:3424
	s_waitcnt lgkmcnt(1)
	v_mfma_f32_16x16x32_f16 v[206:209], v[34:37], v[30:33], v[118:121]
	v_mfma_f32_16x16x32_f16 v[126:129], v[18:21], v[30:33], v[126:129]
	s_waitcnt lgkmcnt(0)
	v_mfma_f32_16x16x32_f16 v[146:149], v[34:37], v[50:53], v[146:149]
	v_mfma_f32_16x16x32_f16 v[210:213], v[18:21], v[50:53], v[210:213]
	v_add_u32_e32 v30, 0xf6ec0, v244
	v_min_u32_e32 v30, v30, v157
	global_load_dwordx4 v[82:85], v30, s[8:9] nt
	s_waitcnt vmcnt(21)
	v_cvt_pk_f16_f32 v31, v64, v65
	v_cvt_pk_f16_f32 v30, v62, v63
	ds_write_b16 v238, v30 offset:6688
	ds_write_b16_d16_hi v239, v30 offset:6688
	ds_write_b16 v240, v31 offset:6688
	ds_write_b16_d16_hi v241, v31 offset:6688
	ds_read_b128 v[30:33], v151 offset:4032
	ds_read_b128 v[50:53], v151 offset:4640
	s_waitcnt lgkmcnt(1)
	v_mfma_f32_16x16x32_f16 v[62:65], v[34:37], v[30:33], v[214:217]
	v_mfma_f32_16x16x32_f16 v[142:145], v[18:21], v[30:33], v[142:145]
	s_waitcnt lgkmcnt(0)
	v_mfma_f32_16x16x32_f16 v[166:169], v[34:37], v[50:53], v[166:169]
	v_mfma_f32_16x16x32_f16 v[162:165], v[18:21], v[50:53], v[162:165]
	ds_read_b128 v[30:33], v151 offset:5248
	ds_read_b128 v[50:53], v151 offset:5856
	s_waitcnt lgkmcnt(1)
	v_mfma_f32_16x16x32_f16 v[214:217], v[34:37], v[30:33], v[122:125]
	v_mfma_f32_16x16x32_f16 v[170:173], v[18:21], v[30:33], v[170:173]
	s_waitcnt lgkmcnt(0)
	v_mfma_f32_16x16x32_f16 v[174:177], v[34:37], v[50:53], v[174:177]
	v_mfma_f32_16x16x32_f16 v[178:181], v[18:21], v[50:53], v[178:181]
	v_add_u32_e32 v30, 0x10d500, v150
	v_min_u32_e32 v30, v30, v157
	v_cndmask_b32_e64 v30, 0, v30, s[0:1]
	global_load_dwordx4 v[118:121], v30, s[8:9] nt
	s_waitcnt vmcnt(21)
	v_cvt_pk_f16_f32 v31, v88, v89
	v_cvt_pk_f16_f32 v30, v86, v87
	ds_write_b16 v234, v30 offset:7296
	ds_write_b16_d16_hi v235, v30 offset:7296
	ds_write_b16 v236, v31 offset:7296
	ds_write_b16_d16_hi v237, v31 offset:7296
	ds_read_b128 v[30:33], v151 offset:6464
	ds_read_b128 v[50:53], v151 offset:7072
	ds_read_b128 v[122:125], v151 offset:7680
	s_mov_b32 s2, 0x50000
	s_waitcnt lgkmcnt(0)
	v_mfma_f32_16x16x32_f16 v[86:89], v[34:37], v[30:33], v[186:189]
	s_barrier
	v_sub_u32_e32 v245, v234, v243
	v_add_u32_e32 v246, 0xfffffdc0, v245
	v_min_u32_e32 v245, v245, v246
	v_add_u32_e32 v234, v242, v245
	v_sub_u32_e32 v245, v235, v243
	v_add_u32_e32 v246, 0xfffffdc0, v245
	v_min_u32_e32 v245, v245, v246
	v_add_u32_e32 v235, v242, v245
	v_sub_u32_e32 v245, v236, v243
	v_add_u32_e32 v246, 0xfffffdc0, v245
	v_min_u32_e32 v245, v245, v246
	v_add_u32_e32 v236, v242, v245
	v_sub_u32_e32 v245, v237, v243
	v_add_u32_e32 v246, 0xfffffdc0, v245
	v_min_u32_e32 v245, v245, v246
	v_add_u32_e32 v237, v242, v245
	v_sub_u32_e32 v245, v238, v243
	v_add_u32_e32 v246, 0xfffffdc0, v245
	v_min_u32_e32 v245, v245, v246
	v_add_u32_e32 v238, v242, v245
	v_sub_u32_e32 v245, v239, v243
	v_add_u32_e32 v246, 0xfffffdc0, v245
	v_min_u32_e32 v245, v245, v246
	v_add_u32_e32 v239, v242, v245
	v_sub_u32_e32 v245, v240, v243
	v_add_u32_e32 v246, 0xfffffdc0, v245
	v_min_u32_e32 v245, v245, v246
	v_add_u32_e32 v240, v242, v245
	v_sub_u32_e32 v245, v241, v243
	v_add_u32_e32 v246, 0xfffffdc0, v245
	v_min_u32_e32 v245, v245, v246
	v_add_u32_e32 v241, v242, v245
	v_mfma_f32_16x16x32_f16 v[158:161], v[18:21], v[30:33], v[158:161]
	v_add_co_u32_e32 v30, vcc, s2, v152
	s_mov_b32 s2, 0x54000
	s_nop 0
	v_addc_co_u32_e32 v31, vcc, 0, v153, vcc
	v_mfma_f32_16x16x32_f16 v[186:189], v[34:37], v[50:53], v[194:197]
	v_mfma_f32_16x16x32_f16 v[34:37], v[34:37], v[122:125], v[10:13]
	s_nop 2
	v_add_co_u32_e32 v10, vcc, s2, v152
	v_mfma_f32_16x16x32_f16 v[194:197], v[18:21], v[50:53], v[202:205]
	s_nop 0
	v_addc_co_u32_e32 v11, vcc, 0, v153, vcc
	global_load_dwordx4 v[50:53], v[30:31], off sc1
	global_load_dwordx4 v[54:57], v[30:31], off offset:256 sc1
	s_nop 0
	global_load_dwordx4 v[30:33], v[10:11], off sc1
	s_nop 0
	global_load_dwordx4 v[10:13], v[10:11], off offset:256 sc1
	v_mfma_f32_16x16x32_f16 v[182:185], v[18:21], v[122:125], v[182:185]
	v_add_u32_e32 v157, 0x111520dc, v154
	ds_read_b128 v[18:21], v151 offset:448
	v_add_u32_e32 v122, 0xc00, v150
	s_waitcnt vmcnt(24) lgkmcnt(0)
	v_mfma_f32_16x16x32_f16 v[202:205], v[42:45], v[18:21], v[218:221]
	s_waitcnt vmcnt(23)
	v_mfma_f32_16x16x32_f16 v[190:193], v[46:49], v[18:21], v[190:193]
	v_min_u32_e32 v18, v122, v157
	global_load_dwordx4 v[18:21], v18, s[8:9] nt
	s_waitcnt vmcnt(21)
	v_cvt_pk_f16_f32 v17, v16, v17
	v_cvt_pk_f16_f32 v16, v14, v15
	ds_write_b16 v234, v16 offset:0
	ds_write_b16_d16_hi v235, v16 offset:0
	ds_write_b16 v236, v17 offset:0
	ds_write_b16_d16_hi v237, v17 offset:0
	ds_read_b128 v[14:17], v151 offset:1056
	ds_read_b128 v[122:125], v151 offset:1664
	s_waitcnt lgkmcnt(1)
	v_mfma_f32_16x16x32_f16 v[198:201], v[42:45], v[14:17], v[198:201]
	s_waitcnt lgkmcnt(0)
	v_mfma_f32_16x16x32_f16 v[58:61], v[42:45], v[122:125], v[58:61]
	v_mfma_f32_16x16x32_f16 v[218:221], v[46:49], v[122:125], v[130:133]
	ds_read_b128 v[122:125], v151 offset:2272
	s_nop 1
	ds_read_b128 v[130:133], v151 offset:2880
	v_mfma_f32_16x16x32_f16 v[14:17], v[46:49], v[14:17], v[222:225]
	s_waitcnt lgkmcnt(1)
	v_mfma_f32_16x16x32_f16 v[134:137], v[42:45], v[122:125], v[134:137]
	v_mfma_f32_16x16x32_f16 v[138:141], v[46:49], v[122:125], v[138:141]
	s_waitcnt lgkmcnt(0)
	v_mfma_f32_16x16x32_f16 v[206:209], v[42:45], v[130:133], v[206:209]
	v_mfma_f32_16x16x32_f16 v[222:225], v[46:49], v[130:133], v[126:129]
	v_add_u32_e32 v122, 0x17240, v244
	v_min_u32_e32 v122, v122, v157
	global_load_dwordx4 v[122:125], v122, s[8:9] nt
	s_waitcnt vmcnt(21)
	v_cvt_pk_f16_f32 v93, v92, v93
	v_cvt_pk_f16_f32 v92, v90, v91
	ds_write_b16 v238, v92 offset:608
	ds_write_b16_d16_hi v239, v92 offset:608
	ds_write_b16 v240, v93 offset:608
	ds_write_b16_d16_hi v241, v93 offset:608
	ds_read_b128 v[90:93], v151 offset:3488
	ds_read_b128 v[126:129], v151 offset:5312
	s_waitcnt lgkmcnt(1)
	v_mfma_f32_16x16x32_f16 v[146:149], v[42:45], v[90:93], v[146:149]
	v_mfma_f32_16x16x32_f16 v[90:93], v[46:49], v[90:93], v[210:213]
	ds_read_b128 v[130:133], v151 offset:4096
	s_nop 1
	ds_read_b128 v[210:213], v151 offset:4704
	s_waitcnt lgkmcnt(1)
	v_mfma_f32_16x16x32_f16 v[62:65], v[42:45], v[130:133], v[62:65]
	v_mfma_f32_16x16x32_f16 v[142:145], v[46:49], v[130:133], v[142:145]
	s_waitcnt lgkmcnt(0)
	v_mfma_f32_16x16x32_f16 v[166:169], v[42:45], v[210:213], v[166:169]
	v_mfma_f32_16x16x32_f16 v[162:165], v[46:49], v[210:213], v[162:165]
	v_mfma_f32_16x16x32_f16 v[210:213], v[42:45], v[126:129], v[214:217]
	v_mfma_f32_16x16x32_f16 v[170:173], v[46:49], v[126:129], v[170:173]
	v_add_u32_e32 v126, 0x2d880, v150
	v_min_u32_e32 v126, v126, v157
	global_load_dwordx4 v[126:129], v126, s[8:9] nt
	s_waitcnt vmcnt(21)
	v_cvt_pk_f16_f32 v97, v96, v97
	v_cvt_pk_f16_f32 v96, v94, v95
	ds_write_b16 v234, v96 offset:1216
	ds_write_b16_d16_hi v235, v96 offset:1216
	ds_write_b16 v236, v97 offset:1216
	ds_write_b16_d16_hi v237, v97 offset:1216
	ds_read_b128 v[94:97], v151 offset:5920
	ds_read_b128 v[130:133], v151 offset:6528
	s_waitcnt lgkmcnt(1)
	v_mfma_f32_16x16x32_f16 v[174:177], v[42:45], v[94:97], v[174:177]
	v_mfma_f32_16x16x32_f16 v[94:97], v[46:49], v[94:97], v[178:181]
	s_waitcnt lgkmcnt(0)
	v_mfma_f32_16x16x32_f16 v[86:89], v[42:45], v[130:133], v[86:89]
	v_mfma_f32_16x16x32_f16 v[158:161], v[46:49], v[130:133], v[158:161]
	ds_read_b128 v[130:133], v151 offset:7136
	ds_read_b128 v[178:181], v151 offset:7744
	s_waitcnt lgkmcnt(1)
	v_mfma_f32_16x16x32_f16 v[186:189], v[42:45], v[130:133], v[186:189]
	v_mfma_f32_16x16x32_f16 v[194:197], v[46:49], v[130:133], v[194:197]
	s_waitcnt lgkmcnt(0)
	v_mfma_f32_16x16x32_f16 v[34:37], v[42:45], v[178:181], v[34:37]
	v_mfma_f32_16x16x32_f16 v[42:45], v[46:49], v[178:181], v[182:185]
	v_add_u32_e32 v46, 0x43ec0, v244
	v_min_u32_e32 v46, v46, v157
	global_load_dwordx4 v[130:133], v46, s[8:9] nt
	s_waitcnt vmcnt(21)
	v_cvt_pk_f16_f32 v47, v100, v101
	v_cvt_pk_f16_f32 v46, v98, v99
	ds_write_b16 v238, v46 offset:1824
	ds_write_b16_d16_hi v239, v46 offset:1824
	ds_write_b16 v240, v47 offset:1824
	ds_write_b16_d16_hi v241, v47 offset:1824
	ds_read_b128 v[46:49], v151 offset:512
	ds_read_b128 v[98:101], v151 offset:1120
	s_waitcnt lgkmcnt(1)
	v_mfma_f32_16x16x32_f16 v[178:181], v[26:29], v[46:49], v[202:205]
	v_mfma_f32_16x16x32_f16 v[46:49], v[6:9], v[46:49], v[190:193]
	s_waitcnt lgkmcnt(0)
	v_mfma_f32_16x16x32_f16 v[182:185], v[26:29], v[98:101], v[198:201]
	v_mfma_f32_16x16x32_f16 v[98:101], v[6:9], v[98:101], v[14:17]
	s_nop 2
	ds_read_b128 v[14:17], v151 offset:1728
	ds_read_b128 v[190:193], v151 offset:2336
	s_waitcnt lgkmcnt(1)
	v_mfma_f32_16x16x32_f16 v[198:201], v[26:29], v[14:17], v[58:61]
	v_mfma_f32_16x16x32_f16 v[202:205], v[6:9], v[14:17], v[218:221]
	s_waitcnt lgkmcnt(0)
	v_mfma_f32_16x16x32_f16 v[214:217], v[26:29], v[190:193], v[134:137]
	v_mfma_f32_16x16x32_f16 v[190:193], v[6:9], v[190:193], v[138:141]
	v_add_u32_e32 v14, 0x5a500, v150
	v_min_u32_e32 v14, v14, v157
	global_load_dwordx4 v[134:137], v14, s[8:9] nt
	s_waitcnt vmcnt(21)
	v_cvt_pk_f16_f32 v15, v104, v105
	v_cvt_pk_f16_f32 v14, v102, v103
	ds_write_b16 v234, v14 offset:2432
	ds_write_b16_d16_hi v235, v14 offset:2432
	ds_write_b16 v236, v15 offset:2432
	ds_write_b16_d16_hi v237, v15 offset:2432
	ds_read_b128 v[14:17], v151 offset:2944
	ds_read_b128 v[58:61], v151 offset:3552
	s_waitcnt lgkmcnt(1)
	v_mfma_f32_16x16x32_f16 v[102:105], v[26:29], v[14:17], v[206:209]
	v_mfma_f32_16x16x32_f16 v[206:209], v[6:9], v[14:17], v[222:225]
	s_waitcnt lgkmcnt(0)
	v_mfma_f32_16x16x32_f16 v[218:221], v[26:29], v[58:61], v[146:149]
	v_mfma_f32_16x16x32_f16 v[90:93], v[6:9], v[58:61], v[90:93]
	ds_read_b128 v[14:17], v151 offset:4160
	ds_read_b128 v[58:61], v151 offset:4768
	s_waitcnt lgkmcnt(1)
	v_mfma_f32_16x16x32_f16 v[222:225], v[26:29], v[14:17], v[62:65]
	v_mfma_f32_16x16x32_f16 v[226:229], v[6:9], v[14:17], v[142:145]
	s_waitcnt lgkmcnt(0)
	v_mfma_f32_16x16x32_f16 v[166:169], v[26:29], v[58:61], v[166:169]
	v_mfma_f32_16x16x32_f16 v[162:165], v[6:9], v[58:61], v[162:165]
	v_add_u32_e32 v14, 0x70b40, v244
	v_min_u32_e32 v14, v14, v157
	global_load_dwordx4 v[138:141], v14, s[8:9] nt
	s_waitcnt vmcnt(21)
	v_cvt_pk_f16_f32 v15, v108, v109
	v_cvt_pk_f16_f32 v14, v106, v107
	ds_write_b16 v238, v14 offset:3040
	ds_write_b16_d16_hi v239, v14 offset:3040
	ds_write_b16 v240, v15 offset:3040
	ds_write_b16_d16_hi v241, v15 offset:3040
	ds_read_b128 v[14:17], v151 offset:5376
	ds_read_b128 v[58:61], v151 offset:5984
	s_waitcnt lgkmcnt(1)
	v_mfma_f32_16x16x32_f16 v[106:109], v[26:29], v[14:17], v[210:213]
	v_mfma_f32_16x16x32_f16 v[170:173], v[6:9], v[14:17], v[170:173]
	s_waitcnt lgkmcnt(0)
	v_mfma_f32_16x16x32_f16 v[174:177], v[26:29], v[58:61], v[174:177]
	v_mfma_f32_16x16x32_f16 v[94:97], v[6:9], v[58:61], v[94:97]
	ds_read_b128 v[14:17], v151 offset:6592
	ds_read_b128 v[58:61], v151 offset:7200
	s_waitcnt lgkmcnt(1)
	v_mfma_f32_16x16x32_f16 v[86:89], v[26:29], v[14:17], v[86:89]
	v_mfma_f32_16x16x32_f16 v[158:161], v[6:9], v[14:17], v[158:161]
	s_waitcnt lgkmcnt(0)
	v_mfma_f32_16x16x32_f16 v[186:189], v[26:29], v[58:61], v[186:189]
	v_mfma_f32_16x16x32_f16 v[194:197], v[6:9], v[58:61], v[194:197]
	v_add_u32_e32 v14, 0x87180, v150
	v_min_u32_e32 v14, v14, v157
	global_load_dwordx4 v[142:145], v14, s[8:9] nt
	s_waitcnt vmcnt(21)
	v_cvt_pk_f16_f32 v15, v112, v113
	v_cvt_pk_f16_f32 v14, v110, v111
	ds_write_b16 v234, v14 offset:3648
	ds_write_b16_d16_hi v235, v14 offset:3648
	ds_write_b16 v236, v15 offset:3648
	ds_write_b16_d16_hi v237, v15 offset:3648
	ds_read_b128 v[110:113], v151 offset:7808
	s_mov_b32 s2, 0x58000
	v_add_co_u32_e32 v14, vcc, s2, v152
	s_mov_b32 s2, 0x5c000
	s_nop 0
	v_addc_co_u32_e32 v15, vcc, 0, v153, vcc
	global_load_dwordx4 v[58:61], v[14:15], off sc1
	global_load_dwordx4 v[62:65], v[14:15], off offset:256 sc1
	v_add_co_u32_e32 v14, vcc, s2, v152
	s_waitcnt lgkmcnt(0)
	v_mfma_f32_16x16x32_f16 v[26:29], v[26:29], v[110:113], v[34:37]
	v_addc_co_u32_e32 v15, vcc, 0, v153, vcc
	s_nop 1
	global_load_dwordx4 v[34:37], v[14:15], off sc1
	s_nop 0
	global_load_dwordx4 v[14:17], v[14:15], off offset:256 sc1
	v_mfma_f32_16x16x32_f16 v[42:45], v[6:9], v[110:113], v[42:45]
	ds_read_b128 v[6:9], v151 offset:0
	ds_read_b128 v[110:113], v151 offset:608
	s_waitcnt vmcnt(24) lgkmcnt(1)
	v_mfma_f32_16x16x32_f16 v[178:181], v[70:73], v[6:9], v[178:181]
	s_waitcnt vmcnt(23)
	v_mfma_f32_16x16x32_f16 v[46:49], v[74:77], v[6:9], v[46:49]
	ds_read_b128 v[6:9], v151 offset:1216
	s_waitcnt lgkmcnt(1)
	v_mfma_f32_16x16x32_f16 v[182:185], v[70:73], v[110:113], v[182:185]
	v_mfma_f32_16x16x32_f16 v[98:101], v[74:77], v[110:113], v[98:101]
	s_waitcnt lgkmcnt(0)
	v_mfma_f32_16x16x32_f16 v[198:201], v[70:73], v[6:9], v[198:201]
	v_mfma_f32_16x16x32_f16 v[202:205], v[74:77], v[6:9], v[202:205]
	v_add_u32_e32 v6, 0x9d7c0, v244
	v_min_u32_e32 v6, v6, v157
	global_load_dwordx4 v[146:149], v6, s[8:9] nt
	s_waitcnt vmcnt(21)
	v_cvt_pk_f16_f32 v5, v4, v5
	v_cvt_pk_f16_f32 v4, v2, v3
	ds_write_b16 v238, v4 offset:4256
	ds_write_b16_d16_hi v239, v4 offset:4256
	ds_write_b16 v240, v5 offset:4256
	ds_write_b16_d16_hi v241, v5 offset:4256
	ds_read_b128 v[2:5], v151 offset:1824
	ds_read_b128 v[6:9], v151 offset:2432
	s_waitcnt lgkmcnt(1)
	v_mfma_f32_16x16x32_f16 v[210:213], v[70:73], v[2:5], v[214:217]
	v_mfma_f32_16x16x32_f16 v[2:5], v[74:77], v[2:5], v[190:193]
	s_waitcnt lgkmcnt(0)
	v_mfma_f32_16x16x32_f16 v[102:105], v[70:73], v[6:9], v[102:105]
	v_mfma_f32_16x16x32_f16 v[190:193], v[74:77], v[6:9], v[206:209]
	ds_read_b128 v[6:9], v151 offset:3040
	ds_read_b128 v[110:113], v151 offset:3648
	s_waitcnt lgkmcnt(1)
	v_mfma_f32_16x16x32_f16 v[206:209], v[70:73], v[6:9], v[218:221]
	v_mfma_f32_16x16x32_f16 v[90:93], v[74:77], v[6:9], v[90:93]
	s_waitcnt lgkmcnt(0)
	v_mfma_f32_16x16x32_f16 v[214:217], v[70:73], v[110:113], v[222:225]
	v_mfma_f32_16x16x32_f16 v[218:221], v[74:77], v[110:113], v[226:229]
	v_add_u32_e32 v6, 0xb3e00, v150
	v_min_u32_e32 v6, v6, v157
	global_load_dwordx4 v[110:113], v6, s[8:9] nt
	s_waitcnt vmcnt(21)
	v_cvt_pk_f16_f32 v7, v116, v117
	v_cvt_pk_f16_f32 v6, v114, v115
	ds_write_b16 v234, v6 offset:4864
	ds_write_b16_d16_hi v235, v6 offset:4864
	ds_write_b16 v236, v7 offset:4864
	ds_write_b16_d16_hi v237, v7 offset:4864
	ds_read_b128 v[6:9], v151 offset:4256
	ds_read_b128 v[114:117], v151 offset:6080
	s_waitcnt lgkmcnt(1)
	v_mfma_f32_16x16x32_f16 v[166:169], v[70:73], v[6:9], v[166:169]
	v_mfma_f32_16x16x32_f16 v[162:165], v[74:77], v[6:9], v[162:165]
	ds_read_b128 v[6:9], v151 offset:4864
	ds_read_b128 v[222:225], v151 offset:5472
	s_waitcnt lgkmcnt(2)
	v_mfma_f32_16x16x32_f16 v[86:89], v[70:73], v[114:117], v[86:89]
	v_mfma_f32_16x16x32_f16 v[114:117], v[74:77], v[114:117], v[158:161]
	s_waitcnt lgkmcnt(1)
	v_mfma_f32_16x16x32_f16 v[106:109], v[70:73], v[6:9], v[106:109]
	v_mfma_f32_16x16x32_f16 v[170:173], v[74:77], v[6:9], v[170:173]
	s_waitcnt lgkmcnt(0)
	v_mfma_f32_16x16x32_f16 v[174:177], v[70:73], v[222:225], v[174:177]
	v_mfma_f32_16x16x32_f16 v[94:97], v[74:77], v[222:225], v[94:97]
	v_add_u32_e32 v6, 0xca440, v244
	v_min_u32_e32 v6, v6, v157
	global_load_dwordx4 v[6:9], v6, s[8:9] nt
	s_waitcnt vmcnt(21)
	v_cvt_pk_f16_f32 v81, v80, v81
	v_cvt_pk_f16_f32 v80, v78, v79
	ds_write_b16 v238, v80 offset:5472
	ds_write_b16_d16_hi v239, v80 offset:5472
	ds_write_b16 v240, v81 offset:5472
	ds_write_b16_d16_hi v241, v81 offset:5472
	ds_read_b128 v[78:81], v151 offset:6688
	ds_read_b128 v[158:161], v151 offset:7296
	s_waitcnt lgkmcnt(1)
	v_mfma_f32_16x16x32_f16 v[186:189], v[70:73], v[78:81], v[186:189]
	s_waitcnt lgkmcnt(0)
	v_mfma_f32_16x16x32_f16 v[26:29], v[70:73], v[158:161], v[26:29]
	v_mfma_f32_16x16x32_f16 v[158:161], v[74:77], v[158:161], v[42:45]
	s_nop 2
	ds_read_b128 v[42:45], v151 offset:64
	ds_read_b128 v[70:73], v151 offset:672
	v_mfma_f32_16x16x32_f16 v[194:197], v[74:77], v[78:81], v[194:197]
	s_waitcnt lgkmcnt(1)
	v_mfma_f32_16x16x32_f16 v[178:181], v[38:41], v[42:45], v[178:181]
	v_mfma_f32_16x16x32_f16 v[222:225], v[22:25], v[42:45], v[46:49]
	s_waitcnt lgkmcnt(0)
	v_mfma_f32_16x16x32_f16 v[182:185], v[38:41], v[70:73], v[182:185]
	v_mfma_f32_16x16x32_f16 v[98:101], v[22:25], v[70:73], v[98:101]
	v_add_u32_e32 v42, 0xe0a80, v150
	v_min_u32_e32 v42, v42, v157
	global_load_dwordx4 v[70:73], v42, s[8:9] nt
	s_waitcnt vmcnt(21)
	v_cvt_pk_f16_f32 v43, v68, v69
	v_cvt_pk_f16_f32 v42, v66, v67
	ds_write_b16 v234, v42 offset:6080
	ds_write_b16_d16_hi v235, v42 offset:6080
	ds_write_b16 v236, v43 offset:6080
	ds_write_b16_d16_hi v237, v43 offset:6080
	ds_read_b128 v[42:45], v151 offset:1280
	ds_read_b128 v[46:49], v151 offset:1888
	s_waitcnt lgkmcnt(1)
	v_mfma_f32_16x16x32_f16 v[66:69], v[38:41], v[42:45], v[198:201]
	v_mfma_f32_16x16x32_f16 v[198:201], v[22:25], v[42:45], v[202:205]
	s_waitcnt lgkmcnt(0)
	v_mfma_f32_16x16x32_f16 v[202:205], v[38:41], v[46:49], v[210:213]
	v_mfma_f32_16x16x32_f16 v[210:213], v[22:25], v[46:49], v[2:5]
	s_nop 2
	ds_read_b128 v[2:5], v151 offset:2496
	ds_read_b128 v[42:45], v151 offset:3104
	s_waitcnt lgkmcnt(1)
	v_mfma_f32_16x16x32_f16 v[102:105], v[38:41], v[2:5], v[102:105]
	v_mfma_f32_16x16x32_f16 v[190:193], v[22:25], v[2:5], v[190:193]
	s_waitcnt lgkmcnt(0)
	v_mfma_f32_16x16x32_f16 v[206:209], v[38:41], v[42:45], v[206:209]
	v_mfma_f32_16x16x32_f16 v[90:93], v[22:25], v[42:45], v[90:93]
	v_add_u32_e32 v2, 0xf70c0, v244
	v_min_u32_e32 v2, v2, v157
	global_load_dwordx4 v[74:77], v2, s[8:9] nt
	s_waitcnt vmcnt(21)
	v_cvt_pk_f16_f32 v3, v84, v85
	v_cvt_pk_f16_f32 v2, v82, v83
	ds_write_b16 v238, v2 offset:6688
	ds_write_b16_d16_hi v239, v2 offset:6688
	ds_write_b16 v240, v3 offset:6688
	ds_write_b16_d16_hi v241, v3 offset:6688
	ds_read_b128 v[2:5], v151 offset:3712
	ds_read_b128 v[42:45], v151 offset:4320
	s_waitcnt lgkmcnt(1)
	v_mfma_f32_16x16x32_f16 v[214:217], v[38:41], v[2:5], v[214:217]
	v_mfma_f32_16x16x32_f16 v[218:221], v[22:25], v[2:5], v[218:221]
	s_waitcnt lgkmcnt(0)
	v_mfma_f32_16x16x32_f16 v[166:169], v[38:41], v[42:45], v[166:169]
	v_mfma_f32_16x16x32_f16 v[162:165], v[22:25], v[42:45], v[162:165]
	ds_read_b128 v[2:5], v151 offset:4928
	ds_read_b128 v[42:45], v151 offset:5536
	s_waitcnt lgkmcnt(1)
	v_mfma_f32_16x16x32_f16 v[106:109], v[38:41], v[2:5], v[106:109]
	v_mfma_f32_16x16x32_f16 v[170:173], v[22:25], v[2:5], v[170:173]
	s_waitcnt lgkmcnt(0)
	v_mfma_f32_16x16x32_f16 v[174:177], v[38:41], v[42:45], v[174:177]
	v_mfma_f32_16x16x32_f16 v[94:97], v[22:25], v[42:45], v[94:97]
	v_add_u32_e32 v2, 0x10d700, v150
	v_min_u32_e32 v2, v2, v157
	v_cndmask_b32_e64 v2, 0, v2, s[0:1]
	global_load_dwordx4 v[78:81], v2, s[8:9] nt
	s_waitcnt vmcnt(21)
	v_cvt_pk_f16_f32 v3, v120, v121
	v_cvt_pk_f16_f32 v2, v118, v119
	ds_write_b16 v234, v2 offset:7296
	ds_write_b16_d16_hi v235, v2 offset:7296
	ds_write_b16 v236, v3 offset:7296
	ds_write_b16_d16_hi v237, v3 offset:7296
	ds_read_b128 v[2:5], v151 offset:6144
	ds_read_b128 v[42:45], v151 offset:6752
	ds_read_b128 v[82:85], v151 offset:7360
	s_mov_b32 s2, 0x60000
	s_waitcnt lgkmcnt(0)
	v_mfma_f32_16x16x32_f16 v[118:121], v[38:41], v[2:5], v[86:89]
	s_barrier
	v_sub_u32_e32 v245, v234, v243
	v_add_u32_e32 v246, 0xfffffdc0, v245
	v_min_u32_e32 v245, v245, v246
	v_add_u32_e32 v234, v242, v245
	v_sub_u32_e32 v245, v235, v243
	v_add_u32_e32 v246, 0xfffffdc0, v245
	v_min_u32_e32 v245, v245, v246
	v_add_u32_e32 v235, v242, v245
	v_sub_u32_e32 v245, v236, v243
	v_add_u32_e32 v246, 0xfffffdc0, v245
	v_min_u32_e32 v245, v245, v246
	v_add_u32_e32 v236, v242, v245
	v_sub_u32_e32 v245, v237, v243
	v_add_u32_e32 v246, 0xfffffdc0, v245
	v_min_u32_e32 v245, v245, v246
	v_add_u32_e32 v237, v242, v245
	v_sub_u32_e32 v245, v238, v243
	v_add_u32_e32 v246, 0xfffffdc0, v245
	v_min_u32_e32 v245, v245, v246
	v_add_u32_e32 v238, v242, v245
	v_sub_u32_e32 v245, v239, v243
	v_add_u32_e32 v246, 0xfffffdc0, v245
	v_min_u32_e32 v245, v245, v246
	v_add_u32_e32 v239, v242, v245
	v_sub_u32_e32 v245, v240, v243
	v_add_u32_e32 v246, 0xfffffdc0, v245
	v_min_u32_e32 v245, v245, v246
	v_add_u32_e32 v240, v242, v245
	v_sub_u32_e32 v245, v241, v243
	v_add_u32_e32 v246, 0xfffffdc0, v245
	v_min_u32_e32 v245, v245, v246
	v_add_u32_e32 v241, v242, v245
	v_mfma_f32_16x16x32_f16 v[114:117], v[22:25], v[2:5], v[114:117]
	v_add_co_u32_e32 v2, vcc, s2, v152
	s_mov_b32 s2, 0x64000
	s_nop 0
	v_addc_co_u32_e32 v3, vcc, 0, v153, vcc
	v_mfma_f32_16x16x32_f16 v[186:189], v[38:41], v[42:45], v[186:189]
	v_mfma_f32_16x16x32_f16 v[194:197], v[22:25], v[42:45], v[194:197]
	global_load_dwordx4 v[42:45], v[2:3], off sc1
	global_load_dwordx4 v[46:49], v[2:3], off offset:256 sc1
	v_add_co_u32_e32 v2, vcc, s2, v152
	v_mfma_f32_16x16x32_f16 v[38:41], v[38:41], v[82:85], v[26:29]
	s_nop 0
	v_addc_co_u32_e32 v3, vcc, 0, v153, vcc
	s_nop 0
	global_load_dwordx4 v[26:29], v[2:3], off sc1
	s_nop 0
	global_load_dwordx4 v[2:5], v[2:3], off offset:256 sc1
	v_mfma_f32_16x16x32_f16 v[22:25], v[22:25], v[82:85], v[158:161]
	v_add_u32_e32 v157, 0x111522dc, v154
	ds_read_b128 v[82:85], v151 offset:128
	v_add_u32_e32 v86, 0xe00, v150
	s_waitcnt vmcnt(24) lgkmcnt(0)
	v_mfma_f32_16x16x32_f16 v[158:161], v[50:53], v[82:85], v[178:181]
	s_waitcnt vmcnt(23)
	v_mfma_f32_16x16x32_f16 v[178:181], v[54:57], v[82:85], v[222:225]
	v_min_u32_e32 v82, v86, v157
	global_load_dwordx4 v[82:85], v82, s[8:9] nt
	s_waitcnt vmcnt(21)
	v_cvt_pk_f16_f32 v21, v20, v21
	v_cvt_pk_f16_f32 v20, v18, v19
	ds_write_b16 v234, v20 offset:0
	ds_write_b16_d16_hi v235, v20 offset:0
	ds_write_b16 v236, v21 offset:0
	ds_write_b16_d16_hi v237, v21 offset:0
	ds_read_b128 v[18:21], v151 offset:736
	ds_read_b128 v[86:89], v151 offset:1344
	s_waitcnt lgkmcnt(1)
	v_mfma_f32_16x16x32_f16 v[182:185], v[50:53], v[18:21], v[182:185]
	v_mfma_f32_16x16x32_f16 v[18:21], v[54:57], v[18:21], v[98:101]
	s_waitcnt lgkmcnt(0)
	v_mfma_f32_16x16x32_f16 v[66:69], v[50:53], v[86:89], v[66:69]
	v_mfma_f32_16x16x32_f16 v[98:101], v[54:57], v[86:89], v[198:201]
	ds_read_b128 v[86:89], v151 offset:1952
	s_nop 1
	ds_read_b128 v[198:201], v151 offset:2560
	s_waitcnt lgkmcnt(1)
	v_mfma_f32_16x16x32_f16 v[202:205], v[50:53], v[86:89], v[202:205]
	v_mfma_f32_16x16x32_f16 v[210:213], v[54:57], v[86:89], v[210:213]
	s_waitcnt lgkmcnt(0)
	v_mfma_f32_16x16x32_f16 v[102:105], v[50:53], v[198:201], v[102:105]
	v_mfma_f32_16x16x32_f16 v[190:193], v[54:57], v[198:201], v[190:193]
	v_add_u32_e32 v86, 0x17440, v244
	v_min_u32_e32 v86, v86, v157
	global_load_dwordx4 v[86:89], v86, s[8:9] nt
	s_waitcnt vmcnt(21)
	v_cvt_pk_f16_f32 v125, v124, v125
	v_cvt_pk_f16_f32 v124, v122, v123
	ds_write_b16 v238, v124 offset:608
	ds_write_b16_d16_hi v239, v124 offset:608
	ds_write_b16 v240, v125 offset:608
	ds_write_b16_d16_hi v241, v125 offset:608
	ds_read_b128 v[122:125], v151 offset:3168
	ds_read_b128 v[198:201], v151 offset:4992
	s_waitcnt lgkmcnt(1)
	v_mfma_f32_16x16x32_f16 v[206:209], v[50:53], v[122:125], v[206:209]
	v_mfma_f32_16x16x32_f16 v[122:125], v[54:57], v[122:125], v[90:93]
	s_nop 2
	ds_read_b128 v[90:93], v151 offset:3776
	ds_read_b128 v[222:225], v151 offset:4384
	s_waitcnt lgkmcnt(1)
	v_mfma_f32_16x16x32_f16 v[214:217], v[50:53], v[90:93], v[214:217]
	v_mfma_f32_16x16x32_f16 v[218:221], v[54:57], v[90:93], v[218:221]
	s_waitcnt lgkmcnt(0)
	v_mfma_f32_16x16x32_f16 v[166:169], v[50:53], v[222:225], v[166:169]
	v_mfma_f32_16x16x32_f16 v[162:165], v[54:57], v[222:225], v[162:165]
	v_mfma_f32_16x16x32_f16 v[106:109], v[50:53], v[198:201], v[106:109]
	v_mfma_f32_16x16x32_f16 v[170:173], v[54:57], v[198:201], v[170:173]
	v_add_u32_e32 v90, 0x2da80, v150
	v_min_u32_e32 v90, v90, v157
	global_load_dwordx4 v[90:93], v90, s[8:9] nt
	s_waitcnt vmcnt(21)
	v_cvt_pk_f16_f32 v129, v128, v129
	v_cvt_pk_f16_f32 v128, v126, v127
	ds_write_b16 v234, v128 offset:1216
	ds_write_b16_d16_hi v235, v128 offset:1216
	ds_write_b16 v236, v129 offset:1216
	ds_write_b16_d16_hi v237, v129 offset:1216
	ds_read_b128 v[126:129], v151 offset:5600
	ds_read_b128 v[198:201], v151 offset:6208
	s_waitcnt lgkmcnt(1)
	v_mfma_f32_16x16x32_f16 v[174:177], v[50:53], v[126:129], v[174:177]
	v_mfma_f32_16x16x32_f16 v[126:129], v[54:57], v[126:129], v[94:97]
	s_waitcnt lgkmcnt(0)
	v_mfma_f32_16x16x32_f16 v[118:121], v[50:53], v[198:201], v[118:121]
	v_mfma_f32_16x16x32_f16 v[114:117], v[54:57], v[198:201], v[114:117]
	ds_read_b128 v[94:97], v151 offset:6816
	ds_read_b128 v[198:201], v151 offset:7424
	s_waitcnt lgkmcnt(1)
	v_mfma_f32_16x16x32_f16 v[186:189], v[50:53], v[94:97], v[186:189]
	v_mfma_f32_16x16x32_f16 v[194:197], v[54:57], v[94:97], v[194:197]
	s_waitcnt lgkmcnt(0)
	v_mfma_f32_16x16x32_f16 v[38:41], v[50:53], v[198:201], v[38:41]
	v_mfma_f32_16x16x32_f16 v[22:25], v[54:57], v[198:201], v[22:25]
	v_add_u32_e32 v50, 0x440c0, v244
	v_min_u32_e32 v50, v50, v157
	global_load_dwordx4 v[94:97], v50, s[8:9] nt
	s_waitcnt vmcnt(21)
	v_cvt_pk_f16_f32 v51, v132, v133
	v_cvt_pk_f16_f32 v50, v130, v131
	ds_write_b16 v238, v50 offset:1824
	ds_write_b16_d16_hi v239, v50 offset:1824
	ds_write_b16 v240, v51 offset:1824
	ds_write_b16_d16_hi v241, v51 offset:1824
	ds_read_b128 v[50:53], v151 offset:192
	ds_read_b128 v[54:57], v151 offset:800
	s_waitcnt lgkmcnt(1)
	v_mfma_f32_16x16x32_f16 v[130:133], v[30:33], v[50:53], v[158:161]
	v_mfma_f32_16x16x32_f16 v[50:53], v[10:13], v[50:53], v[178:181]
	s_waitcnt lgkmcnt(0)
	v_mfma_f32_16x16x32_f16 v[158:161], v[30:33], v[54:57], v[182:185]
	v_mfma_f32_16x16x32_f16 v[178:181], v[10:13], v[54:57], v[18:21]
	s_nop 2
	ds_read_b128 v[18:21], v151 offset:1408
	ds_read_b128 v[54:57], v151 offset:2016
	s_waitcnt lgkmcnt(1)
	v_mfma_f32_16x16x32_f16 v[182:185], v[30:33], v[18:21], v[66:69]
	v_mfma_f32_16x16x32_f16 v[198:201], v[10:13], v[18:21], v[98:101]
	s_waitcnt lgkmcnt(0)
	v_mfma_f32_16x16x32_f16 v[202:205], v[30:33], v[54:57], v[202:205]
	v_mfma_f32_16x16x32_f16 v[210:213], v[10:13], v[54:57], v[210:213]
	v_add_u32_e32 v18, 0x5a700, v150
	v_min_u32_e32 v18, v18, v157
	global_load_dwordx4 v[98:101], v18, s[8:9] nt
	s_waitcnt vmcnt(21)
	v_cvt_pk_f16_f32 v19, v136, v137
	v_cvt_pk_f16_f32 v18, v134, v135
	ds_write_b16 v234, v18 offset:2432
	ds_write_b16_d16_hi v235, v18 offset:2432
	ds_write_b16 v236, v19 offset:2432
	ds_write_b16_d16_hi v237, v19 offset:2432
	ds_read_b128 v[18:21], v151 offset:2624
	ds_read_b128 v[54:57], v151 offset:3232
	s_waitcnt lgkmcnt(1)
	v_mfma_f32_16x16x32_f16 v[134:137], v[30:33], v[18:21], v[102:105]
	v_mfma_f32_16x16x32_f16 v[190:193], v[10:13], v[18:21], v[190:193]
	s_waitcnt lgkmcnt(0)
	v_mfma_f32_16x16x32_f16 v[206:209], v[30:33], v[54:57], v[206:209]
	v_mfma_f32_16x16x32_f16 v[122:125], v[10:13], v[54:57], v[122:125]
	ds_read_b128 v[18:21], v151 offset:3840
	ds_read_b128 v[54:57], v151 offset:4448
	s_waitcnt lgkmcnt(1)
	v_mfma_f32_16x16x32_f16 v[214:217], v[30:33], v[18:21], v[214:217]
	v_mfma_f32_16x16x32_f16 v[218:221], v[10:13], v[18:21], v[218:221]
	s_waitcnt lgkmcnt(0)
	v_mfma_f32_16x16x32_f16 v[166:169], v[30:33], v[54:57], v[166:169]
	v_mfma_f32_16x16x32_f16 v[162:165], v[10:13], v[54:57], v[162:165]
	v_add_u32_e32 v18, 0x70d40, v244
	v_min_u32_e32 v18, v18, v157
	global_load_dwordx4 v[102:105], v18, s[8:9] nt
	s_waitcnt vmcnt(21)
	v_cvt_pk_f16_f32 v19, v140, v141
	v_cvt_pk_f16_f32 v18, v138, v139
	ds_write_b16 v238, v18 offset:3040
	ds_write_b16_d16_hi v239, v18 offset:3040
	ds_write_b16 v240, v19 offset:3040
	ds_write_b16_d16_hi v241, v19 offset:3040
	ds_read_b128 v[18:21], v151 offset:5056
	ds_read_b128 v[54:57], v151 offset:5664
	s_waitcnt lgkmcnt(1)
	v_mfma_f32_16x16x32_f16 v[138:141], v[30:33], v[18:21], v[106:109]
	v_mfma_f32_16x16x32_f16 v[170:173], v[10:13], v[18:21], v[170:173]
	s_waitcnt lgkmcnt(0)
	v_mfma_f32_16x16x32_f16 v[174:177], v[30:33], v[54:57], v[174:177]
	v_mfma_f32_16x16x32_f16 v[126:129], v[10:13], v[54:57], v[126:129]
	ds_read_b128 v[18:21], v151 offset:6272
	ds_read_b128 v[54:57], v151 offset:6880
	s_waitcnt lgkmcnt(1)
	v_mfma_f32_16x16x32_f16 v[118:121], v[30:33], v[18:21], v[118:121]
	v_mfma_f32_16x16x32_f16 v[222:225], v[10:13], v[18:21], v[114:117]
	s_waitcnt lgkmcnt(0)
	v_mfma_f32_16x16x32_f16 v[186:189], v[30:33], v[54:57], v[186:189]
	v_mfma_f32_16x16x32_f16 v[194:197], v[10:13], v[54:57], v[194:197]
	v_add_u32_e32 v18, 0x87380, v150
	v_min_u32_e32 v18, v18, v157
	global_load_dwordx4 v[106:109], v18, s[8:9] nt
	s_waitcnt vmcnt(21)
	v_cvt_pk_f16_f32 v19, v144, v145
	v_cvt_pk_f16_f32 v18, v142, v143
	ds_write_b16 v234, v18 offset:3648
	ds_write_b16_d16_hi v235, v18 offset:3648
	ds_write_b16 v236, v19 offset:3648
	ds_write_b16_d16_hi v237, v19 offset:3648
	ds_read_b128 v[114:117], v151 offset:7488
	s_mov_b32 s2, 0x68000
	v_add_co_u32_e32 v18, vcc, s2, v152
	s_mov_b32 s2, 0x6c000
	s_nop 0
	v_addc_co_u32_e32 v19, vcc, 0, v153, vcc
	global_load_dwordx4 v[54:57], v[18:19], off sc1
	global_load_dwordx4 v[66:69], v[18:19], off offset:256 sc1
	v_add_co_u32_e32 v18, vcc, s2, v152
	s_waitcnt lgkmcnt(0)
	v_mfma_f32_16x16x32_f16 v[38:41], v[30:33], v[114:117], v[38:41]
	v_addc_co_u32_e32 v19, vcc, 0, v153, vcc
	global_load_dwordx4 v[30:33], v[18:19], off sc1
	s_nop 0
	global_load_dwordx4 v[18:21], v[18:19], off offset:256 sc1
	v_mfma_f32_16x16x32_f16 v[22:25], v[10:13], v[114:117], v[22:25]
	ds_read_b128 v[10:13], v151 offset:256
	ds_read_b128 v[114:117], v151 offset:864
	s_waitcnt vmcnt(24) lgkmcnt(1)
	v_mfma_f32_16x16x32_f16 v[130:133], v[58:61], v[10:13], v[130:133]
	s_waitcnt vmcnt(23)
	v_mfma_f32_16x16x32_f16 v[50:53], v[62:65], v[10:13], v[50:53]
	ds_read_b128 v[10:13], v151 offset:1472
	s_waitcnt lgkmcnt(1)
	v_mfma_f32_16x16x32_f16 v[142:145], v[58:61], v[114:117], v[158:161]
	v_mfma_f32_16x16x32_f16 v[158:161], v[62:65], v[114:117], v[178:181]
	s_waitcnt lgkmcnt(0)
	v_mfma_f32_16x16x32_f16 v[178:181], v[58:61], v[10:13], v[182:185]
	v_mfma_f32_16x16x32_f16 v[182:185], v[62:65], v[10:13], v[198:201]
	v_add_u32_e32 v10, 0x9d9c0, v244
	v_min_u32_e32 v10, v10, v157
	global_load_dwordx4 v[10:13], v10, s[8:9] nt
	s_waitcnt vmcnt(21)
	v_cvt_pk_f16_f32 v115, v148, v149
	v_cvt_pk_f16_f32 v114, v146, v147
	ds_write_b16 v238, v114 offset:4256
	ds_write_b16_d16_hi v239, v114 offset:4256
	ds_write_b16 v240, v115 offset:4256
	ds_write_b16_d16_hi v241, v115 offset:4256
	ds_read_b128 v[114:117], v151 offset:2080
	ds_read_b128 v[146:149], v151 offset:2688
	s_waitcnt lgkmcnt(1)
	v_mfma_f32_16x16x32_f16 v[198:201], v[58:61], v[114:117], v[202:205]
	v_mfma_f32_16x16x32_f16 v[202:205], v[62:65], v[114:117], v[210:213]
	s_waitcnt lgkmcnt(0)
	v_mfma_f32_16x16x32_f16 v[134:137], v[58:61], v[146:149], v[134:137]
	v_mfma_f32_16x16x32_f16 v[146:149], v[62:65], v[146:149], v[190:193]
	ds_read_b128 v[114:117], v151 offset:3296
	s_nop 1
	ds_read_b128 v[190:193], v151 offset:3904
	s_waitcnt lgkmcnt(1)
	v_mfma_f32_16x16x32_f16 v[206:209], v[58:61], v[114:117], v[206:209]
	v_mfma_f32_16x16x32_f16 v[122:125], v[62:65], v[114:117], v[122:125]
	s_waitcnt lgkmcnt(0)
	v_mfma_f32_16x16x32_f16 v[210:213], v[58:61], v[190:193], v[214:217]
	v_mfma_f32_16x16x32_f16 v[190:193], v[62:65], v[190:193], v[218:221]
	v_add_u32_e32 v114, 0xb4000, v150
	v_min_u32_e32 v114, v114, v157
	global_load_dwordx4 v[114:117], v114, s[8:9] nt
	s_waitcnt vmcnt(21)
	v_cvt_pk_f16_f32 v113, v112, v113
	v_cvt_pk_f16_f32 v112, v110, v111
	ds_write_b16 v234, v112 offset:4864
	ds_write_b16_d16_hi v235, v112 offset:4864
	ds_write_b16 v236, v113 offset:4864
	ds_write_b16_d16_hi v237, v113 offset:4864
	s_mov_b32 s2, 0xb4000
	ds_read_b128 v[110:113], v151 offset:4512
	ds_read_b128 v[214:217], v151 offset:6336
	s_waitcnt lgkmcnt(1)
	v_mfma_f32_16x16x32_f16 v[166:169], v[58:61], v[110:113], v[166:169]
	v_mfma_f32_16x16x32_f16 v[162:165], v[62:65], v[110:113], v[162:165]
	ds_read_b128 v[110:113], v151 offset:5120
	ds_read_b128 v[218:221], v151 offset:5728
	s_waitcnt lgkmcnt(1)
	v_mfma_f32_16x16x32_f16 v[138:141], v[58:61], v[110:113], v[138:141]
	v_mfma_f32_16x16x32_f16 v[170:173], v[62:65], v[110:113], v[170:173]
	s_waitcnt lgkmcnt(0)
	v_mfma_f32_16x16x32_f16 v[174:177], v[58:61], v[218:221], v[174:177]
	v_mfma_f32_16x16x32_f16 v[126:129], v[62:65], v[218:221], v[126:129]
	v_mfma_f32_16x16x32_f16 v[118:121], v[58:61], v[214:217], v[118:121]
	v_mfma_f32_16x16x32_f16 v[214:217], v[62:65], v[214:217], v[222:225]
	v_add_u32_e32 v110, 0xca640, v244
	v_min_u32_e32 v110, v110, v157
	global_load_dwordx4 v[110:113], v110, s[8:9] nt
	s_waitcnt vmcnt(21)
	v_cvt_pk_f16_f32 v9, v8, v9
	v_cvt_pk_f16_f32 v8, v6, v7
	ds_write_b16 v238, v8 offset:5472
	ds_write_b16_d16_hi v239, v8 offset:5472
	ds_write_b16 v240, v9 offset:5472
	ds_write_b16_d16_hi v241, v9 offset:5472
	ds_read_b128 v[6:9], v151 offset:6944
	ds_read_b128 v[218:221], v151 offset:7552
	s_waitcnt lgkmcnt(1)
	v_mfma_f32_16x16x32_f16 v[186:189], v[58:61], v[6:9], v[186:189]
	v_mfma_f32_16x16x32_f16 v[6:9], v[62:65], v[6:9], v[194:197]
	s_waitcnt lgkmcnt(0)
	v_mfma_f32_16x16x32_f16 v[58:61], v[58:61], v[218:221], v[38:41]
	v_mfma_f32_16x16x32_f16 v[194:197], v[62:65], v[218:221], v[22:25]
	s_nop 2
	ds_read_b128 v[22:25], v151 offset:320
	ds_read_b128 v[38:41], v151 offset:928
	s_waitcnt lgkmcnt(1)
	v_mfma_f32_16x16x32_f16 v[130:133], v[34:37], v[22:25], v[130:133]
	v_mfma_f32_16x16x32_f16 v[218:221], v[14:17], v[22:25], v[50:53]
	s_waitcnt lgkmcnt(0)
	v_mfma_f32_16x16x32_f16 v[142:145], v[34:37], v[38:41], v[142:145]
	v_mfma_f32_16x16x32_f16 v[158:161], v[14:17], v[38:41], v[158:161]
	v_add_u32_e32 v22, 0xe0c80, v150
	v_min_u32_e32 v22, v22, v157
	global_load_dwordx4 v[62:65], v22, s[8:9] nt
	s_waitcnt vmcnt(21)
	v_cvt_pk_f16_f32 v23, v72, v73
	v_cvt_pk_f16_f32 v22, v70, v71
	ds_write_b16 v234, v22 offset:6080
	ds_write_b16_d16_hi v235, v22 offset:6080
	ds_write_b16 v236, v23 offset:6080
	ds_write_b16_d16_hi v237, v23 offset:6080
	ds_read_b128 v[22:25], v151 offset:1536
	ds_read_b128 v[38:41], v151 offset:2144
	s_waitcnt lgkmcnt(1)
	v_mfma_f32_16x16x32_f16 v[178:181], v[34:37], v[22:25], v[178:181]
	v_mfma_f32_16x16x32_f16 v[182:185], v[14:17], v[22:25], v[182:185]
	s_waitcnt lgkmcnt(0)
	v_mfma_f32_16x16x32_f16 v[198:201], v[34:37], v[38:41], v[198:201]
	v_mfma_f32_16x16x32_f16 v[202:205], v[14:17], v[38:41], v[202:205]
	ds_read_b128 v[22:25], v151 offset:2752
	ds_read_b128 v[38:41], v151 offset:3360
	s_waitcnt lgkmcnt(1)
	v_mfma_f32_16x16x32_f16 v[134:137], v[34:37], v[22:25], v[134:137]
	v_mfma_f32_16x16x32_f16 v[146:149], v[14:17], v[22:25], v[146:149]
	s_waitcnt lgkmcnt(0)
	v_mfma_f32_16x16x32_f16 v[206:209], v[34:37], v[38:41], v[206:209]
	v_mfma_f32_16x16x32_f16 v[122:125], v[14:17], v[38:41], v[122:125]
	v_add_u32_e32 v22, 0xf72c0, v244
	v_min_u32_e32 v22, v22, v157
	global_load_dwordx4 v[70:73], v22, s[8:9] nt
	s_waitcnt vmcnt(21)
	v_cvt_pk_f16_f32 v23, v76, v77
	v_cvt_pk_f16_f32 v22, v74, v75
	ds_write_b16 v238, v22 offset:6688
	ds_write_b16_d16_hi v239, v22 offset:6688
	ds_write_b16 v240, v23 offset:6688
	ds_write_b16_d16_hi v241, v23 offset:6688
	ds_read_b128 v[22:25], v151 offset:3968
	ds_read_b128 v[38:41], v151 offset:4576
	s_waitcnt lgkmcnt(1)
	v_mfma_f32_16x16x32_f16 v[210:213], v[34:37], v[22:25], v[210:213]
	v_mfma_f32_16x16x32_f16 v[190:193], v[14:17], v[22:25], v[190:193]
	s_waitcnt lgkmcnt(0)
	v_mfma_f32_16x16x32_f16 v[166:169], v[34:37], v[38:41], v[166:169]
	v_mfma_f32_16x16x32_f16 v[162:165], v[14:17], v[38:41], v[162:165]
	ds_read_b128 v[22:25], v151 offset:5184
	ds_read_b128 v[38:41], v151 offset:5792
	s_waitcnt lgkmcnt(1)
	v_mfma_f32_16x16x32_f16 v[138:141], v[34:37], v[22:25], v[138:141]
	v_mfma_f32_16x16x32_f16 v[170:173], v[14:17], v[22:25], v[170:173]
	s_waitcnt lgkmcnt(0)
	v_mfma_f32_16x16x32_f16 v[174:177], v[34:37], v[38:41], v[174:177]
	v_mfma_f32_16x16x32_f16 v[126:129], v[14:17], v[38:41], v[126:129]
	v_add_u32_e32 v22, 0x10d900, v150
	v_min_u32_e32 v22, v22, v157
	v_cndmask_b32_e64 v22, 0, v22, s[0:1]
	global_load_dwordx4 v[74:77], v22, s[8:9] nt
	s_waitcnt vmcnt(21)
	v_cvt_pk_f16_f32 v23, v80, v81
	v_cvt_pk_f16_f32 v22, v78, v79
	ds_write_b16 v234, v22 offset:7296
	ds_write_b16_d16_hi v235, v22 offset:7296
	ds_write_b16 v236, v23 offset:7296
	ds_write_b16_d16_hi v237, v23 offset:7296
	ds_read_b128 v[22:25], v151 offset:6400
	ds_read_b128 v[38:41], v151 offset:7008
	s_mov_b32 s3, 0x70000
	ds_read_b128 v[78:81], v151 offset:7616
	s_waitcnt lgkmcnt(0)
	v_mfma_f32_16x16x32_f16 v[118:121], v[34:37], v[22:25], v[118:121]
	s_barrier
	v_sub_u32_e32 v245, v234, v243
	v_add_u32_e32 v246, 0xfffffdc0, v245
	v_min_u32_e32 v245, v245, v246
	v_add_u32_e32 v234, v242, v245
	v_sub_u32_e32 v245, v235, v243
	v_add_u32_e32 v246, 0xfffffdc0, v245
	v_min_u32_e32 v245, v245, v246
	v_add_u32_e32 v235, v242, v245
	v_sub_u32_e32 v245, v236, v243
	v_add_u32_e32 v246, 0xfffffdc0, v245
	v_min_u32_e32 v245, v245, v246
	v_add_u32_e32 v236, v242, v245
	v_sub_u32_e32 v245, v237, v243
	v_add_u32_e32 v246, 0xfffffdc0, v245
	v_min_u32_e32 v245, v245, v246
	v_add_u32_e32 v237, v242, v245
	v_sub_u32_e32 v245, v238, v243
	v_add_u32_e32 v246, 0xfffffdc0, v245
	v_min_u32_e32 v245, v245, v246
	v_add_u32_e32 v238, v242, v245
	v_sub_u32_e32 v245, v239, v243
	v_add_u32_e32 v246, 0xfffffdc0, v245
	v_min_u32_e32 v245, v245, v246
	v_add_u32_e32 v239, v242, v245
	v_sub_u32_e32 v245, v240, v243
	v_add_u32_e32 v246, 0xfffffdc0, v245
	v_min_u32_e32 v245, v245, v246
	v_add_u32_e32 v240, v242, v245
	v_sub_u32_e32 v245, v241, v243
	v_add_u32_e32 v246, 0xfffffdc0, v245
	v_min_u32_e32 v245, v245, v246
	v_add_u32_e32 v241, v242, v245
	v_mfma_f32_16x16x32_f16 v[214:217], v[14:17], v[22:25], v[214:217]
	v_add_co_u32_e32 v22, vcc, s3, v152
	s_mov_b32 s3, 0x74000
	s_nop 0
	v_addc_co_u32_e32 v23, vcc, 0, v153, vcc
	v_mfma_f32_16x16x32_f16 v[222:225], v[14:17], v[38:41], v[6:9]
	s_nop 2
	v_add_co_u32_e32 v6, vcc, s3, v152
	v_mfma_f32_16x16x32_f16 v[186:189], v[34:37], v[38:41], v[186:189]
	s_nop 0
	v_addc_co_u32_e32 v7, vcc, 0, v153, vcc
	global_load_dwordx4 v[38:41], v[22:23], off sc1
	global_load_dwordx4 v[50:53], v[22:23], off offset:256 sc1
	s_nop 0
	global_load_dwordx4 v[22:25], v[6:7], off sc1
	s_nop 0
	global_load_dwordx4 v[6:9], v[6:7], off offset:256 sc1
	v_mfma_f32_16x16x32_f16 v[34:37], v[34:37], v[78:81], v[58:61]
	v_mfma_f32_16x16x32_f16 v[14:17], v[14:17], v[78:81], v[194:197]
	v_add_u32_e32 v157, 0x111524dc, v154
	s_nop 0
	ds_read_b128 v[58:61], v151 offset:384
	v_add_u32_e32 v78, 0x1000, v150
	s_waitcnt vmcnt(24) lgkmcnt(0)
	v_mfma_f32_16x16x32_f16 v[130:133], v[42:45], v[58:61], v[130:133]
	s_waitcnt vmcnt(23)
	v_mfma_f32_16x16x32_f16 v[58:61], v[46:49], v[58:61], v[218:221]
	v_min_u32_e32 v78, v78, v157
	global_load_dwordx4 v[78:81], v78, s[8:9] nt
	s_waitcnt vmcnt(21)
	v_cvt_pk_f16_f32 v85, v84, v85
	v_cvt_pk_f16_f32 v84, v82, v83
	ds_write_b16 v234, v84 offset:0
	ds_write_b16_d16_hi v235, v84 offset:0
	ds_write_b16 v236, v85 offset:0
	ds_write_b16_d16_hi v237, v85 offset:0
	ds_read_b128 v[82:85], v151 offset:992
	ds_read_b128 v[194:197], v151 offset:1600
	s_waitcnt lgkmcnt(1)
	v_mfma_f32_16x16x32_f16 v[142:145], v[42:45], v[82:85], v[142:145]
	v_mfma_f32_16x16x32_f16 v[158:161], v[46:49], v[82:85], v[158:161]
	s_waitcnt lgkmcnt(0)
	v_mfma_f32_16x16x32_f16 v[178:181], v[42:45], v[194:197], v[178:181]
	v_mfma_f32_16x16x32_f16 v[182:185], v[46:49], v[194:197], v[182:185]
	ds_read_b128 v[82:85], v151 offset:2208
	ds_read_b128 v[194:197], v151 offset:2816
	s_waitcnt lgkmcnt(1)
	v_mfma_f32_16x16x32_f16 v[198:201], v[42:45], v[82:85], v[198:201]
	v_mfma_f32_16x16x32_f16 v[202:205], v[46:49], v[82:85], v[202:205]
	s_waitcnt lgkmcnt(0)
	v_mfma_f32_16x16x32_f16 v[134:137], v[42:45], v[194:197], v[134:137]
	v_mfma_f32_16x16x32_f16 v[146:149], v[46:49], v[194:197], v[146:149]
	v_add_u32_e32 v82, 0x17640, v244
	v_min_u32_e32 v82, v82, v157
	global_load_dwordx4 v[82:85], v82, s[8:9] nt
	s_waitcnt vmcnt(21)
	v_cvt_pk_f16_f32 v89, v88, v89
	v_cvt_pk_f16_f32 v88, v86, v87
	ds_write_b16 v238, v88 offset:608
	ds_write_b16_d16_hi v239, v88 offset:608
	ds_write_b16 v240, v89 offset:608
	ds_write_b16_d16_hi v241, v89 offset:608
	ds_read_b128 v[86:89], v151 offset:3424
	ds_read_b128 v[194:197], v151 offset:5248
	s_waitcnt lgkmcnt(1)
	v_mfma_f32_16x16x32_f16 v[206:209], v[42:45], v[86:89], v[206:209]
	v_mfma_f32_16x16x32_f16 v[122:125], v[46:49], v[86:89], v[122:125]
	ds_read_b128 v[86:89], v151 offset:4032
	ds_read_b128 v[218:221], v151 offset:4640
	s_waitcnt lgkmcnt(1)
	v_mfma_f32_16x16x32_f16 v[210:213], v[42:45], v[86:89], v[210:213]
	v_mfma_f32_16x16x32_f16 v[190:193], v[46:49], v[86:89], v[190:193]
	s_waitcnt lgkmcnt(0)
	v_mfma_f32_16x16x32_f16 v[166:169], v[42:45], v[218:221], v[166:169]
	v_mfma_f32_16x16x32_f16 v[162:165], v[46:49], v[218:221], v[162:165]
	v_mfma_f32_16x16x32_f16 v[138:141], v[42:45], v[194:197], v[138:141]
	v_mfma_f32_16x16x32_f16 v[170:173], v[46:49], v[194:197], v[170:173]
	v_add_u32_e32 v86, 0x2dc80, v150
	v_min_u32_e32 v86, v86, v157
	global_load_dwordx4 v[86:89], v86, s[8:9] nt
	s_waitcnt vmcnt(21)
	v_cvt_pk_f16_f32 v93, v92, v93
	v_cvt_pk_f16_f32 v92, v90, v91
	ds_write_b16 v234, v92 offset:1216
	ds_write_b16_d16_hi v235, v92 offset:1216
	ds_write_b16 v236, v93 offset:1216
	ds_write_b16_d16_hi v237, v93 offset:1216
	ds_read_b128 v[90:93], v151 offset:5856
	ds_read_b128 v[194:197], v151 offset:6464
	s_waitcnt lgkmcnt(1)
	v_mfma_f32_16x16x32_f16 v[174:177], v[42:45], v[90:93], v[174:177]
	v_mfma_f32_16x16x32_f16 v[126:129], v[46:49], v[90:93], v[126:129]
	s_waitcnt lgkmcnt(0)
	v_mfma_f32_16x16x32_f16 v[118:121], v[42:45], v[194:197], v[118:121]
	v_mfma_f32_16x16x32_f16 v[194:197], v[46:49], v[194:197], v[214:217]
	ds_read_b128 v[90:93], v151 offset:7072
	s_nop 1
	ds_read_b128 v[214:217], v151 offset:7680
	s_waitcnt lgkmcnt(1)
	v_mfma_f32_16x16x32_f16 v[186:189], v[42:45], v[90:93], v[186:189]
	v_mfma_f32_16x16x32_f16 v[218:221], v[46:49], v[90:93], v[222:225]
	s_waitcnt lgkmcnt(0)
	v_mfma_f32_16x16x32_f16 v[34:37], v[42:45], v[214:217], v[34:37]
	v_mfma_f32_16x16x32_f16 v[46:49], v[46:49], v[214:217], v[14:17]
	s_nop 2
	v_add_u32_e32 v14, 0x442c0, v244
	v_min_u32_e32 v14, v14, v157
	global_load_dwordx4 v[90:93], v14, s[8:9] nt
	s_waitcnt vmcnt(21)
	v_cvt_pk_f16_f32 v15, v96, v97
	v_cvt_pk_f16_f32 v14, v94, v95
	ds_write_b16 v238, v14 offset:1824
	ds_write_b16_d16_hi v239, v14 offset:1824
	ds_write_b16 v240, v15 offset:1824
	ds_write_b16_d16_hi v241, v15 offset:1824
	ds_read_b128 v[14:17], v151 offset:448
	ds_read_b128 v[42:45], v151 offset:1056
	s_waitcnt lgkmcnt(1)
	v_mfma_f32_16x16x32_f16 v[130:133], v[26:29], v[14:17], v[130:133]
	v_mfma_f32_16x16x32_f16 v[214:217], v[2:5], v[14:17], v[58:61]
	s_waitcnt lgkmcnt(0)
	v_mfma_f32_16x16x32_f16 v[142:145], v[26:29], v[42:45], v[142:145]
	v_mfma_f32_16x16x32_f16 v[158:161], v[2:5], v[42:45], v[158:161]
	ds_read_b128 v[14:17], v151 offset:1664
	ds_read_b128 v[42:45], v151 offset:2272
	s_waitcnt lgkmcnt(1)
	v_mfma_f32_16x16x32_f16 v[178:181], v[26:29], v[14:17], v[178:181]
	v_mfma_f32_16x16x32_f16 v[182:185], v[2:5], v[14:17], v[182:185]
	s_waitcnt lgkmcnt(0)
	v_mfma_f32_16x16x32_f16 v[198:201], v[26:29], v[42:45], v[198:201]
	v_mfma_f32_16x16x32_f16 v[202:205], v[2:5], v[42:45], v[202:205]
	v_add_u32_e32 v14, 0x5a900, v150
	v_min_u32_e32 v14, v14, v157
	global_load_dwordx4 v[94:97], v14, s[8:9] nt
	s_waitcnt vmcnt(21)
	v_cvt_pk_f16_f32 v15, v100, v101
	v_cvt_pk_f16_f32 v14, v98, v99
	ds_write_b16 v234, v14 offset:2432
	ds_write_b16_d16_hi v235, v14 offset:2432
	ds_write_b16 v236, v15 offset:2432
	ds_write_b16_d16_hi v237, v15 offset:2432
	ds_read_b128 v[14:17], v151 offset:2880
	ds_read_b128 v[42:45], v151 offset:3488
	s_waitcnt lgkmcnt(1)
	v_mfma_f32_16x16x32_f16 v[134:137], v[26:29], v[14:17], v[134:137]
	v_mfma_f32_16x16x32_f16 v[146:149], v[2:5], v[14:17], v[146:149]
	s_waitcnt lgkmcnt(0)
	v_mfma_f32_16x16x32_f16 v[206:209], v[26:29], v[42:45], v[206:209]
	v_mfma_f32_16x16x32_f16 v[122:125], v[2:5], v[42:45], v[122:125]
	ds_read_b128 v[14:17], v151 offset:4096
	ds_read_b128 v[42:45], v151 offset:4704
	s_waitcnt lgkmcnt(1)
	v_mfma_f32_16x16x32_f16 v[210:213], v[26:29], v[14:17], v[210:213]
	v_mfma_f32_16x16x32_f16 v[190:193], v[2:5], v[14:17], v[190:193]
	s_waitcnt lgkmcnt(0)
	v_mfma_f32_16x16x32_f16 v[166:169], v[26:29], v[42:45], v[166:169]
	v_mfma_f32_16x16x32_f16 v[162:165], v[2:5], v[42:45], v[162:165]
	v_add_u32_e32 v14, 0x70f40, v244
	v_min_u32_e32 v14, v14, v157
	global_load_dwordx4 v[98:101], v14, s[8:9] nt
	s_waitcnt vmcnt(21)
	v_cvt_pk_f16_f32 v15, v104, v105
	v_cvt_pk_f16_f32 v14, v102, v103
	ds_write_b16 v238, v14 offset:3040
	ds_write_b16_d16_hi v239, v14 offset:3040
	ds_write_b16 v240, v15 offset:3040
	ds_write_b16_d16_hi v241, v15 offset:3040
	ds_read_b128 v[14:17], v151 offset:5312
	ds_read_b128 v[42:45], v151 offset:5920
	s_waitcnt lgkmcnt(1)
	v_mfma_f32_16x16x32_f16 v[138:141], v[26:29], v[14:17], v[138:141]
	v_mfma_f32_16x16x32_f16 v[170:173], v[2:5], v[14:17], v[170:173]
	s_waitcnt lgkmcnt(0)
	v_mfma_f32_16x16x32_f16 v[174:177], v[26:29], v[42:45], v[174:177]
	v_mfma_f32_16x16x32_f16 v[126:129], v[2:5], v[42:45], v[126:129]
	ds_read_b128 v[14:17], v151 offset:6528
	ds_read_b128 v[42:45], v151 offset:7136
	s_waitcnt lgkmcnt(1)
	v_mfma_f32_16x16x32_f16 v[118:121], v[26:29], v[14:17], v[118:121]
	v_mfma_f32_16x16x32_f16 v[194:197], v[2:5], v[14:17], v[194:197]
	s_waitcnt lgkmcnt(0)
	v_mfma_f32_16x16x32_f16 v[186:189], v[26:29], v[42:45], v[186:189]
	v_mfma_f32_16x16x32_f16 v[218:221], v[2:5], v[42:45], v[218:221]
	v_add_u32_e32 v14, 0x87580, v150
	v_min_u32_e32 v14, v14, v157
	global_load_dwordx4 v[102:105], v14, s[8:9] nt
	s_waitcnt vmcnt(21)
	v_cvt_pk_f16_f32 v15, v108, v109
	v_cvt_pk_f16_f32 v14, v106, v107
	ds_write_b16 v234, v14 offset:3648
	ds_write_b16_d16_hi v235, v14 offset:3648
	ds_write_b16 v236, v15 offset:3648
	ds_write_b16_d16_hi v237, v15 offset:3648
	ds_read_b128 v[106:109], v151 offset:7744
	s_mov_b32 s3, 0x78000
	v_add_co_u32_e32 v14, vcc, s3, v152
	s_mov_b32 s3, 0x7c000
	s_nop 0
	v_addc_co_u32_e32 v15, vcc, 0, v153, vcc
	global_load_dwordx4 v[42:45], v[14:15], off sc1
	global_load_dwordx4 v[58:61], v[14:15], off offset:256 sc1
	v_add_co_u32_e32 v14, vcc, s3, v152
	s_waitcnt lgkmcnt(0)
	v_mfma_f32_16x16x32_f16 v[26:29], v[26:29], v[106:109], v[34:37]
	v_addc_co_u32_e32 v15, vcc, 0, v153, vcc
	s_nop 1
	global_load_dwordx4 v[34:37], v[14:15], off sc1
	s_nop 0
	global_load_dwordx4 v[14:17], v[14:15], off offset:256 sc1
	v_mfma_f32_16x16x32_f16 v[46:49], v[2:5], v[106:109], v[46:49]
	ds_read_b128 v[2:5], v151 offset:512
	ds_read_b128 v[106:109], v151 offset:1120
	s_waitcnt vmcnt(24) lgkmcnt(1)
	v_mfma_f32_16x16x32_f16 v[130:133], v[54:57], v[2:5], v[130:133]
	s_waitcnt vmcnt(23)
	v_mfma_f32_16x16x32_f16 v[214:217], v[66:69], v[2:5], v[214:217]
	ds_read_b128 v[2:5], v151 offset:1728
	s_waitcnt lgkmcnt(1)
	v_mfma_f32_16x16x32_f16 v[142:145], v[54:57], v[106:109], v[142:145]
	v_mfma_f32_16x16x32_f16 v[158:161], v[66:69], v[106:109], v[158:161]
	s_waitcnt lgkmcnt(0)
	v_mfma_f32_16x16x32_f16 v[178:181], v[54:57], v[2:5], v[178:181]
	v_mfma_f32_16x16x32_f16 v[182:185], v[66:69], v[2:5], v[182:185]
	v_add_u32_e32 v2, 0x9dbc0, v244
	v_min_u32_e32 v2, v2, v157
	global_load_dwordx4 v[2:5], v2, s[8:9] nt
	s_waitcnt vmcnt(21)
	v_cvt_pk_f16_f32 v13, v12, v13
	v_cvt_pk_f16_f32 v12, v10, v11
	ds_write_b16 v238, v12 offset:4256
	ds_write_b16_d16_hi v239, v12 offset:4256
	ds_write_b16 v240, v13 offset:4256
	ds_write_b16_d16_hi v241, v13 offset:4256
	ds_read_b128 v[10:13], v151 offset:2336
	ds_read_b128 v[106:109], v151 offset:2944
	s_waitcnt lgkmcnt(1)
	v_mfma_f32_16x16x32_f16 v[198:201], v[54:57], v[10:13], v[198:201]
	v_mfma_f32_16x16x32_f16 v[10:13], v[66:69], v[10:13], v[202:205]
	s_waitcnt lgkmcnt(0)
	v_mfma_f32_16x16x32_f16 v[134:137], v[54:57], v[106:109], v[134:137]
	v_mfma_f32_16x16x32_f16 v[146:149], v[66:69], v[106:109], v[146:149]
	ds_read_b128 v[106:109], v151 offset:3552
	ds_read_b128 v[202:205], v151 offset:4160
	s_waitcnt lgkmcnt(1)
	v_mfma_f32_16x16x32_f16 v[206:209], v[54:57], v[106:109], v[206:209]
	v_mfma_f32_16x16x32_f16 v[122:125], v[66:69], v[106:109], v[122:125]
	s_waitcnt lgkmcnt(0)
	v_mfma_f32_16x16x32_f16 v[210:213], v[54:57], v[202:205], v[210:213]
	v_mfma_f32_16x16x32_f16 v[190:193], v[66:69], v[202:205], v[190:193]
	v_add_u32_e32 v106, 0xb4200, v150
	v_min_u32_e32 v106, v106, v157
	global_load_dwordx4 v[106:109], v106, s[8:9] nt
	s_waitcnt vmcnt(21)
	v_cvt_pk_f16_f32 v117, v116, v117
	v_cvt_pk_f16_f32 v116, v114, v115
	ds_write_b16 v234, v116 offset:4864
	ds_write_b16_d16_hi v235, v116 offset:4864
	ds_write_b16 v236, v117 offset:4864
	ds_write_b16_d16_hi v237, v117 offset:4864
	ds_read_b128 v[114:117], v151 offset:4768
	ds_read_b128 v[202:205], v151 offset:6592
	s_waitcnt lgkmcnt(1)
	v_mfma_f32_16x16x32_f16 v[166:169], v[54:57], v[114:117], v[166:169]
	v_mfma_f32_16x16x32_f16 v[162:165], v[66:69], v[114:117], v[162:165]
	ds_read_b128 v[114:117], v151 offset:5376
	ds_read_b128 v[222:225], v151 offset:5984
	s_waitcnt lgkmcnt(1)
	v_mfma_f32_16x16x32_f16 v[138:141], v[54:57], v[114:117], v[138:141]
	v_mfma_f32_16x16x32_f16 v[170:173], v[66:69], v[114:117], v[170:173]
	s_waitcnt lgkmcnt(0)
	v_mfma_f32_16x16x32_f16 v[174:177], v[54:57], v[222:225], v[174:177]
	v_mfma_f32_16x16x32_f16 v[126:129], v[66:69], v[222:225], v[126:129]
	v_mfma_f32_16x16x32_f16 v[222:225], v[54:57], v[202:205], v[118:121]
	v_mfma_f32_16x16x32_f16 v[194:197], v[66:69], v[202:205], v[194:197]
	v_add_u32_e32 v114, 0xca840, v244
	v_min_u32_e32 v114, v114, v157
	global_load_dwordx4 v[114:117], v114, s[8:9] nt
	s_waitcnt vmcnt(21)
	v_cvt_pk_f16_f32 v113, v112, v113
	v_cvt_pk_f16_f32 v112, v110, v111
	ds_write_b16 v238, v112 offset:5472
	ds_write_b16_d16_hi v239, v112 offset:5472
	ds_write_b16 v240, v113 offset:5472
	ds_write_b16_d16_hi v241, v113 offset:5472
	ds_read_b128 v[110:113], v151 offset:7200
	ds_read_b128 v[118:121], v151 offset:7808
	s_waitcnt lgkmcnt(1)
	v_mfma_f32_16x16x32_f16 v[186:189], v[54:57], v[110:113], v[186:189]
	v_mfma_f32_16x16x32_f16 v[202:205], v[66:69], v[110:113], v[218:221]
	s_waitcnt lgkmcnt(0)
	v_mfma_f32_16x16x32_f16 v[26:29], v[54:57], v[118:121], v[26:29]
	v_mfma_f32_16x16x32_f16 v[66:69], v[66:69], v[118:121], v[46:49]
	s_nop 2
	ds_read_b128 v[46:49], v151 offset:0
	ds_read_b128 v[54:57], v151 offset:608
	s_waitcnt lgkmcnt(1)
	v_mfma_f32_16x16x32_f16 v[130:133], v[30:33], v[46:49], v[130:133]
	v_mfma_f32_16x16x32_f16 v[214:217], v[18:21], v[46:49], v[214:217]
	s_waitcnt lgkmcnt(0)
	v_mfma_f32_16x16x32_f16 v[142:145], v[30:33], v[54:57], v[142:145]
	v_mfma_f32_16x16x32_f16 v[158:161], v[18:21], v[54:57], v[158:161]
	v_add_u32_e32 v46, 0xe0e80, v150
	v_min_u32_e32 v46, v46, v157
	global_load_dwordx4 v[110:113], v46, s[8:9] nt
	s_waitcnt vmcnt(21)
	v_cvt_pk_f16_f32 v47, v64, v65
	v_cvt_pk_f16_f32 v46, v62, v63
	ds_write_b16 v234, v46 offset:6080
	ds_write_b16_d16_hi v235, v46 offset:6080
	ds_write_b16 v236, v47 offset:6080
	ds_write_b16_d16_hi v237, v47 offset:6080
	ds_read_b128 v[46:49], v151 offset:1216
	ds_read_b128 v[54:57], v151 offset:1824
	s_waitcnt lgkmcnt(1)
	v_mfma_f32_16x16x32_f16 v[62:65], v[30:33], v[46:49], v[178:181]
	v_mfma_f32_16x16x32_f16 v[178:181], v[18:21], v[46:49], v[182:185]
	s_waitcnt lgkmcnt(0)
	v_mfma_f32_16x16x32_f16 v[182:185], v[30:33], v[54:57], v[198:201]
	v_mfma_f32_16x16x32_f16 v[198:201], v[18:21], v[54:57], v[10:13]
	s_nop 2
	ds_read_b128 v[10:13], v151 offset:2432
	ds_read_b128 v[46:49], v151 offset:3040
	s_waitcnt lgkmcnt(1)
	v_mfma_f32_16x16x32_f16 v[134:137], v[30:33], v[10:13], v[134:137]
	v_mfma_f32_16x16x32_f16 v[146:149], v[18:21], v[10:13], v[146:149]
	s_waitcnt lgkmcnt(0)
	v_mfma_f32_16x16x32_f16 v[206:209], v[30:33], v[46:49], v[206:209]
	v_mfma_f32_16x16x32_f16 v[122:125], v[18:21], v[46:49], v[122:125]
	v_add_u32_e32 v10, 0xf74c0, v244
	v_min_u32_e32 v10, v10, v157
	global_load_dwordx4 v[118:121], v10, s[8:9] nt
	s_waitcnt vmcnt(21)
	v_cvt_pk_f16_f32 v11, v72, v73
	v_cvt_pk_f16_f32 v10, v70, v71
	ds_write_b16 v238, v10 offset:6688
	ds_write_b16_d16_hi v239, v10 offset:6688
	ds_write_b16 v240, v11 offset:6688
	ds_write_b16_d16_hi v241, v11 offset:6688
	ds_read_b128 v[10:13], v151 offset:3648
	ds_read_b128 v[46:49], v151 offset:4256
	s_waitcnt lgkmcnt(1)
	v_mfma_f32_16x16x32_f16 v[210:213], v[30:33], v[10:13], v[210:213]
	v_mfma_f32_16x16x32_f16 v[190:193], v[18:21], v[10:13], v[190:193]
	s_waitcnt lgkmcnt(0)
	v_mfma_f32_16x16x32_f16 v[166:169], v[30:33], v[46:49], v[166:169]
	v_mfma_f32_16x16x32_f16 v[162:165], v[18:21], v[46:49], v[162:165]
	ds_read_b128 v[10:13], v151 offset:4864
	ds_read_b128 v[46:49], v151 offset:5472
	s_waitcnt lgkmcnt(1)
	v_mfma_f32_16x16x32_f16 v[138:141], v[30:33], v[10:13], v[138:141]
	v_mfma_f32_16x16x32_f16 v[170:173], v[18:21], v[10:13], v[170:173]
	s_waitcnt lgkmcnt(0)
	v_mfma_f32_16x16x32_f16 v[174:177], v[30:33], v[46:49], v[174:177]
	v_mfma_f32_16x16x32_f16 v[126:129], v[18:21], v[46:49], v[126:129]
	v_add_u32_e32 v10, 0x10db00, v150
	v_min_u32_e32 v10, v10, v157
	v_cndmask_b32_e64 v10, 0, v10, s[0:1]
	global_load_dwordx4 v[70:73], v10, s[8:9] nt
	s_waitcnt vmcnt(21)
	v_cvt_pk_f16_f32 v11, v76, v77
	v_cvt_pk_f16_f32 v10, v74, v75
	ds_write_b16 v234, v10 offset:7296
	ds_write_b16_d16_hi v235, v10 offset:7296
	ds_write_b16 v236, v11 offset:7296
	ds_write_b16_d16_hi v237, v11 offset:7296
	ds_read_b128 v[10:13], v151 offset:6080
	ds_read_b128 v[46:49], v151 offset:6688
	ds_read_b128 v[74:77], v151 offset:7296
	s_mov_b32 s3, 0x80000
	s_waitcnt lgkmcnt(0)
	v_mfma_f32_16x16x32_f16 v[218:221], v[30:33], v[10:13], v[222:225]
	s_barrier
	v_sub_u32_e32 v245, v234, v243
	v_add_u32_e32 v246, 0xfffffdc0, v245
	v_min_u32_e32 v245, v245, v246
	v_add_u32_e32 v234, v242, v245
	v_sub_u32_e32 v245, v235, v243
	v_add_u32_e32 v246, 0xfffffdc0, v245
	v_min_u32_e32 v245, v245, v246
	v_add_u32_e32 v235, v242, v245
	v_sub_u32_e32 v245, v236, v243
	v_add_u32_e32 v246, 0xfffffdc0, v245
	v_min_u32_e32 v245, v245, v246
	v_add_u32_e32 v236, v242, v245
	v_sub_u32_e32 v245, v237, v243
	v_add_u32_e32 v246, 0xfffffdc0, v245
	v_min_u32_e32 v245, v245, v246
	v_add_u32_e32 v237, v242, v245
	v_sub_u32_e32 v245, v238, v243
	v_add_u32_e32 v246, 0xfffffdc0, v245
	v_min_u32_e32 v245, v245, v246
	v_add_u32_e32 v238, v242, v245
	v_sub_u32_e32 v245, v239, v243
	v_add_u32_e32 v246, 0xfffffdc0, v245
	v_min_u32_e32 v245, v245, v246
	v_add_u32_e32 v239, v242, v245
	v_sub_u32_e32 v245, v240, v243
	v_add_u32_e32 v246, 0xfffffdc0, v245
	v_min_u32_e32 v245, v245, v246
	v_add_u32_e32 v240, v242, v245
	v_sub_u32_e32 v245, v241, v243
	v_add_u32_e32 v246, 0xfffffdc0, v245
	v_min_u32_e32 v245, v245, v246
	v_add_u32_e32 v241, v242, v245
	v_mfma_f32_16x16x32_f16 v[194:197], v[18:21], v[10:13], v[194:197]
	v_add_co_u32_e32 v10, vcc, s3, v152
	s_mov_b32 s3, 0x84000
	s_nop 0
	v_addc_co_u32_e32 v11, vcc, 0, v153, vcc
	v_mfma_f32_16x16x32_f16 v[186:189], v[30:33], v[46:49], v[186:189]
	v_mfma_f32_16x16x32_f16 v[202:205], v[18:21], v[46:49], v[202:205]
	global_load_dwordx4 v[46:49], v[10:11], off sc1
	global_load_dwordx4 v[54:57], v[10:11], off offset:256 sc1
	v_add_co_u32_e32 v10, vcc, s3, v152
	v_mfma_f32_16x16x32_f16 v[30:33], v[30:33], v[74:77], v[26:29]
	s_nop 0
	v_addc_co_u32_e32 v11, vcc, 0, v153, vcc
	s_nop 0
	global_load_dwordx4 v[26:29], v[10:11], off sc1
	s_nop 0
	global_load_dwordx4 v[10:13], v[10:11], off offset:256 sc1
	v_mfma_f32_16x16x32_f16 v[18:21], v[18:21], v[74:77], v[66:69]
	v_add_u32_e32 v157, 0x111526dc, v154
	s_nop 1
	ds_read_b128 v[66:69], v151 offset:64
	v_add_u32_e32 v74, 0x1200, v150
	s_waitcnt vmcnt(24) lgkmcnt(0)
	v_mfma_f32_16x16x32_f16 v[130:133], v[38:41], v[66:69], v[130:133]
	s_waitcnt vmcnt(23)
	v_mfma_f32_16x16x32_f16 v[66:69], v[50:53], v[66:69], v[214:217]
	v_min_u32_e32 v74, v74, v157
	global_load_dwordx4 v[74:77], v74, s[8:9] nt
	s_waitcnt vmcnt(21)
	v_cvt_pk_f16_f32 v81, v80, v81
	v_cvt_pk_f16_f32 v80, v78, v79
	ds_write_b16 v234, v80 offset:0
	ds_write_b16_d16_hi v235, v80 offset:0
	ds_write_b16 v236, v81 offset:0
	ds_write_b16_d16_hi v237, v81 offset:0
	ds_read_b128 v[78:81], v151 offset:672
	ds_read_b128 v[214:217], v151 offset:1280
	s_waitcnt lgkmcnt(1)
	v_mfma_f32_16x16x32_f16 v[142:145], v[38:41], v[78:81], v[142:145]
	v_mfma_f32_16x16x32_f16 v[158:161], v[50:53], v[78:81], v[158:161]
	s_waitcnt lgkmcnt(0)
	v_mfma_f32_16x16x32_f16 v[62:65], v[38:41], v[214:217], v[62:65]
	v_mfma_f32_16x16x32_f16 v[178:181], v[50:53], v[214:217], v[178:181]
	ds_read_b128 v[78:81], v151 offset:1888
	ds_read_b128 v[214:217], v151 offset:2496
	s_waitcnt lgkmcnt(1)
	v_mfma_f32_16x16x32_f16 v[182:185], v[38:41], v[78:81], v[182:185]
	v_mfma_f32_16x16x32_f16 v[198:201], v[50:53], v[78:81], v[198:201]
	s_waitcnt lgkmcnt(0)
	v_mfma_f32_16x16x32_f16 v[134:137], v[38:41], v[214:217], v[134:137]
	v_mfma_f32_16x16x32_f16 v[146:149], v[50:53], v[214:217], v[146:149]
	v_add_u32_e32 v78, 0x17840, v244
	v_min_u32_e32 v78, v78, v157
	global_load_dwordx4 v[78:81], v78, s[8:9] nt
	s_waitcnt vmcnt(21)
	v_cvt_pk_f16_f32 v85, v84, v85
	v_cvt_pk_f16_f32 v84, v82, v83
	ds_write_b16 v238, v84 offset:608
	ds_write_b16_d16_hi v239, v84 offset:608
	ds_write_b16 v240, v85 offset:608
	ds_write_b16_d16_hi v241, v85 offset:608
	ds_read_b128 v[82:85], v151 offset:3104
	ds_read_b128 v[214:217], v151 offset:4928
	s_waitcnt lgkmcnt(1)
	v_mfma_f32_16x16x32_f16 v[206:209], v[38:41], v[82:85], v[206:209]
	v_mfma_f32_16x16x32_f16 v[122:125], v[50:53], v[82:85], v[122:125]
	ds_read_b128 v[82:85], v151 offset:3712
	ds_read_b128 v[222:225], v151 offset:4320
	s_waitcnt lgkmcnt(1)
	v_mfma_f32_16x16x32_f16 v[210:213], v[38:41], v[82:85], v[210:213]
	v_mfma_f32_16x16x32_f16 v[190:193], v[50:53], v[82:85], v[190:193]
	s_waitcnt lgkmcnt(0)
	v_mfma_f32_16x16x32_f16 v[166:169], v[38:41], v[222:225], v[166:169]
	v_mfma_f32_16x16x32_f16 v[162:165], v[50:53], v[222:225], v[162:165]
	v_mfma_f32_16x16x32_f16 v[138:141], v[38:41], v[214:217], v[138:141]
	v_mfma_f32_16x16x32_f16 v[170:173], v[50:53], v[214:217], v[170:173]
	v_add_u32_e32 v82, 0x2de80, v150
	v_min_u32_e32 v82, v82, v157
	global_load_dwordx4 v[82:85], v82, s[8:9] nt
	s_waitcnt vmcnt(21)
	v_cvt_pk_f16_f32 v89, v88, v89
	v_cvt_pk_f16_f32 v88, v86, v87
	ds_write_b16 v234, v88 offset:1216
	ds_write_b16_d16_hi v235, v88 offset:1216
	ds_write_b16 v236, v89 offset:1216
	ds_write_b16_d16_hi v237, v89 offset:1216
	ds_read_b128 v[86:89], v151 offset:5536
	ds_read_b128 v[214:217], v151 offset:6144
	s_waitcnt lgkmcnt(1)
	v_mfma_f32_16x16x32_f16 v[174:177], v[38:41], v[86:89], v[174:177]
	v_mfma_f32_16x16x32_f16 v[126:129], v[50:53], v[86:89], v[126:129]
	s_waitcnt lgkmcnt(0)
	v_mfma_f32_16x16x32_f16 v[218:221], v[38:41], v[214:217], v[218:221]
	v_mfma_f32_16x16x32_f16 v[194:197], v[50:53], v[214:217], v[194:197]
	ds_read_b128 v[86:89], v151 offset:6752
	ds_read_b128 v[214:217], v151 offset:7360
	s_waitcnt lgkmcnt(1)
	v_mfma_f32_16x16x32_f16 v[186:189], v[38:41], v[86:89], v[186:189]
	v_mfma_f32_16x16x32_f16 v[202:205], v[50:53], v[86:89], v[202:205]
	s_waitcnt lgkmcnt(0)
	v_mfma_f32_16x16x32_f16 v[30:33], v[38:41], v[214:217], v[30:33]
	v_mfma_f32_16x16x32_f16 v[38:41], v[50:53], v[214:217], v[18:21]
	s_nop 2
	v_add_u32_e32 v18, 0x444c0, v244
	v_min_u32_e32 v18, v18, v157
	global_load_dwordx4 v[50:53], v18, s[8:9] nt
	s_waitcnt vmcnt(21)
	v_cvt_pk_f16_f32 v19, v92, v93
	v_cvt_pk_f16_f32 v18, v90, v91
	ds_write_b16 v238, v18 offset:1824
	ds_write_b16_d16_hi v239, v18 offset:1824
	ds_write_b16 v240, v19 offset:1824
	ds_write_b16_d16_hi v241, v19 offset:1824
	ds_read_b128 v[18:21], v151 offset:128
	ds_read_b128 v[86:89], v151 offset:736
	s_waitcnt lgkmcnt(1)
	v_mfma_f32_16x16x32_f16 v[130:133], v[22:25], v[18:21], v[130:133]
	v_mfma_f32_16x16x32_f16 v[214:217], v[6:9], v[18:21], v[66:69]
	ds_read_b128 v[18:21], v151 offset:1344
	s_nop 1
	ds_read_b128 v[66:69], v151 offset:1952
	s_waitcnt lgkmcnt(2)
	v_mfma_f32_16x16x32_f16 v[142:145], v[22:25], v[86:89], v[142:145]
	v_mfma_f32_16x16x32_f16 v[158:161], v[6:9], v[86:89], v[158:161]
	s_waitcnt lgkmcnt(1)
	v_mfma_f32_16x16x32_f16 v[222:225], v[22:25], v[18:21], v[62:65]
	v_mfma_f32_16x16x32_f16 v[178:181], v[6:9], v[18:21], v[178:181]
	s_waitcnt lgkmcnt(0)
	v_mfma_f32_16x16x32_f16 v[182:185], v[22:25], v[66:69], v[182:185]
	v_mfma_f32_16x16x32_f16 v[198:201], v[6:9], v[66:69], v[198:201]
	v_add_u32_e32 v18, 0x5ab00, v150
	v_min_u32_e32 v18, v18, v157
	global_load_dwordx4 v[86:89], v18, s[8:9] nt
	s_waitcnt vmcnt(21)
	v_cvt_pk_f16_f32 v19, v96, v97
	v_cvt_pk_f16_f32 v18, v94, v95
	ds_write_b16 v234, v18 offset:2432
	ds_write_b16_d16_hi v235, v18 offset:2432
	ds_write_b16 v236, v19 offset:2432
	ds_write_b16_d16_hi v237, v19 offset:2432
	ds_read_b128 v[18:21], v151 offset:2560
	ds_read_b128 v[62:65], v151 offset:3168
	s_waitcnt lgkmcnt(1)
	v_mfma_f32_16x16x32_f16 v[134:137], v[22:25], v[18:21], v[134:137]
	v_mfma_f32_16x16x32_f16 v[146:149], v[6:9], v[18:21], v[146:149]
	s_waitcnt lgkmcnt(0)
	v_mfma_f32_16x16x32_f16 v[206:209], v[22:25], v[62:65], v[206:209]
	v_mfma_f32_16x16x32_f16 v[122:125], v[6:9], v[62:65], v[122:125]
	ds_read_b128 v[18:21], v151 offset:3776
	ds_read_b128 v[62:65], v151 offset:4384
	s_waitcnt lgkmcnt(1)
	v_mfma_f32_16x16x32_f16 v[210:213], v[22:25], v[18:21], v[210:213]
	v_mfma_f32_16x16x32_f16 v[190:193], v[6:9], v[18:21], v[190:193]
	s_waitcnt lgkmcnt(0)
	v_mfma_f32_16x16x32_f16 v[166:169], v[22:25], v[62:65], v[166:169]
	v_mfma_f32_16x16x32_f16 v[162:165], v[6:9], v[62:65], v[162:165]
	v_add_u32_e32 v18, 0x71140, v244
	v_min_u32_e32 v18, v18, v157
	global_load_dwordx4 v[90:93], v18, s[8:9] nt
	s_waitcnt vmcnt(21)
	v_cvt_pk_f16_f32 v19, v100, v101
	v_cvt_pk_f16_f32 v18, v98, v99
	ds_write_b16 v238, v18 offset:3040
	ds_write_b16_d16_hi v239, v18 offset:3040
	ds_write_b16 v240, v19 offset:3040
	ds_write_b16_d16_hi v241, v19 offset:3040
	ds_read_b128 v[18:21], v151 offset:4992
	ds_read_b128 v[62:65], v151 offset:5600
	s_waitcnt lgkmcnt(1)
	v_mfma_f32_16x16x32_f16 v[98:101], v[22:25], v[18:21], v[138:141]
	v_mfma_f32_16x16x32_f16 v[138:141], v[6:9], v[18:21], v[170:173]
	s_waitcnt lgkmcnt(0)
	v_mfma_f32_16x16x32_f16 v[170:173], v[22:25], v[62:65], v[174:177]
	v_mfma_f32_16x16x32_f16 v[126:129], v[6:9], v[62:65], v[126:129]
	ds_read_b128 v[18:21], v151 offset:6208
	ds_read_b128 v[62:65], v151 offset:6816
	s_waitcnt lgkmcnt(1)
	v_mfma_f32_16x16x32_f16 v[174:177], v[22:25], v[18:21], v[218:221]
	v_mfma_f32_16x16x32_f16 v[194:197], v[6:9], v[18:21], v[194:197]
	s_waitcnt lgkmcnt(0)
	v_mfma_f32_16x16x32_f16 v[186:189], v[22:25], v[62:65], v[186:189]
	v_mfma_f32_16x16x32_f16 v[202:205], v[6:9], v[62:65], v[202:205]
	v_add_u32_e32 v18, 0x87780, v150
	v_min_u32_e32 v18, v18, v157
	global_load_dwordx4 v[94:97], v18, s[8:9] nt
	s_waitcnt vmcnt(21)
	v_cvt_pk_f16_f32 v19, v104, v105
	v_cvt_pk_f16_f32 v18, v102, v103
	ds_write_b16 v234, v18 offset:3648
	ds_write_b16_d16_hi v235, v18 offset:3648
	ds_write_b16 v236, v19 offset:3648
	ds_write_b16_d16_hi v237, v19 offset:3648
	ds_read_b128 v[102:105], v151 offset:7424
	s_mov_b32 s3, 0x88000
	v_add_co_u32_e32 v18, vcc, s3, v152
	s_mov_b32 s3, 0x8c000
	s_nop 0
	v_addc_co_u32_e32 v19, vcc, 0, v153, vcc
	global_load_dwordx4 v[62:65], v[18:19], off sc1
	global_load_dwordx4 v[66:69], v[18:19], off offset:256 sc1
	v_add_co_u32_e32 v18, vcc, s3, v152
	s_waitcnt lgkmcnt(0)
	v_mfma_f32_16x16x32_f16 v[22:25], v[22:25], v[102:105], v[30:33]
	v_addc_co_u32_e32 v19, vcc, 0, v153, vcc
	s_nop 1
	global_load_dwordx4 v[30:33], v[18:19], off sc1
	s_nop 0
	global_load_dwordx4 v[18:21], v[18:19], off offset:256 sc1
	v_mfma_f32_16x16x32_f16 v[38:41], v[6:9], v[102:105], v[38:41]
	ds_read_b128 v[6:9], v151 offset:192
	ds_read_b128 v[102:105], v151 offset:800
	s_waitcnt vmcnt(24) lgkmcnt(1)
	v_mfma_f32_16x16x32_f16 v[130:133], v[42:45], v[6:9], v[130:133]
	s_waitcnt vmcnt(23)
	v_mfma_f32_16x16x32_f16 v[214:217], v[58:61], v[6:9], v[214:217]
	ds_read_b128 v[6:9], v151 offset:1408
	s_waitcnt lgkmcnt(1)
	v_mfma_f32_16x16x32_f16 v[142:145], v[42:45], v[102:105], v[142:145]
	v_mfma_f32_16x16x32_f16 v[158:161], v[58:61], v[102:105], v[158:161]
	s_waitcnt lgkmcnt(0)
	v_mfma_f32_16x16x32_f16 v[218:221], v[42:45], v[6:9], v[222:225]
	v_mfma_f32_16x16x32_f16 v[178:181], v[58:61], v[6:9], v[178:181]
	v_add_u32_e32 v6, 0x9ddc0, v244
	v_min_u32_e32 v6, v6, v157
	global_load_dwordx4 v[6:9], v6, s[8:9] nt
	s_waitcnt vmcnt(21)
	v_cvt_pk_f16_f32 v5, v4, v5
	v_cvt_pk_f16_f32 v4, v2, v3
	ds_write_b16 v238, v4 offset:4256
	ds_write_b16_d16_hi v239, v4 offset:4256
	ds_write_b16 v240, v5 offset:4256
	ds_write_b16_d16_hi v241, v5 offset:4256
	ds_read_b128 v[2:5], v151 offset:2016
	ds_read_b128 v[102:105], v151 offset:2624
	s_waitcnt lgkmcnt(1)
	v_mfma_f32_16x16x32_f16 v[182:185], v[42:45], v[2:5], v[182:185]
	v_mfma_f32_16x16x32_f16 v[2:5], v[58:61], v[2:5], v[198:201]
	s_waitcnt lgkmcnt(0)
	v_mfma_f32_16x16x32_f16 v[134:137], v[42:45], v[102:105], v[134:137]
	v_mfma_f32_16x16x32_f16 v[146:149], v[58:61], v[102:105], v[146:149]
	ds_read_b128 v[102:105], v151 offset:3232
	ds_read_b128 v[198:201], v151 offset:3840
	s_waitcnt lgkmcnt(1)
	v_mfma_f32_16x16x32_f16 v[206:209], v[42:45], v[102:105], v[206:209]
	v_mfma_f32_16x16x32_f16 v[122:125], v[58:61], v[102:105], v[122:125]
	s_waitcnt lgkmcnt(0)
	v_mfma_f32_16x16x32_f16 v[210:213], v[42:45], v[198:201], v[210:213]
	v_mfma_f32_16x16x32_f16 v[190:193], v[58:61], v[198:201], v[190:193]
	v_add_u32_e32 v102, 0xb4400, v150
	v_min_u32_e32 v102, v102, v157
	global_load_dwordx4 v[102:105], v102, s[8:9] nt
	s_waitcnt vmcnt(21)
	v_cvt_pk_f16_f32 v109, v108, v109
	v_cvt_pk_f16_f32 v108, v106, v107
	ds_write_b16 v234, v108 offset:4864
	ds_write_b16_d16_hi v235, v108 offset:4864
	ds_write_b16 v236, v109 offset:4864
	ds_write_b16_d16_hi v237, v109 offset:4864
	ds_read_b128 v[106:109], v151 offset:4448
	ds_read_b128 v[198:201], v151 offset:6272
	s_waitcnt lgkmcnt(1)
	v_mfma_f32_16x16x32_f16 v[166:169], v[42:45], v[106:109], v[166:169]
	v_mfma_f32_16x16x32_f16 v[162:165], v[58:61], v[106:109], v[162:165]
	ds_read_b128 v[106:109], v151 offset:5056
	ds_read_b128 v[222:225], v151 offset:5664
	s_waitcnt lgkmcnt(1)
	v_mfma_f32_16x16x32_f16 v[98:101], v[42:45], v[106:109], v[98:101]
	v_mfma_f32_16x16x32_f16 v[138:141], v[58:61], v[106:109], v[138:141]
	s_waitcnt lgkmcnt(0)
	v_mfma_f32_16x16x32_f16 v[170:173], v[42:45], v[222:225], v[170:173]
	v_mfma_f32_16x16x32_f16 v[126:129], v[58:61], v[222:225], v[126:129]
	v_mfma_f32_16x16x32_f16 v[174:177], v[42:45], v[198:201], v[174:177]
	v_mfma_f32_16x16x32_f16 v[194:197], v[58:61], v[198:201], v[194:197]
	v_add_u32_e32 v106, 0xcaa40, v244
	v_min_u32_e32 v106, v106, v157
	global_load_dwordx4 v[106:109], v106, s[8:9] nt
	s_waitcnt vmcnt(21)
	v_cvt_pk_f16_f32 v117, v116, v117
	v_cvt_pk_f16_f32 v116, v114, v115
	ds_write_b16 v238, v116 offset:5472
	ds_write_b16_d16_hi v239, v116 offset:5472
	ds_write_b16 v240, v117 offset:5472
	ds_write_b16_d16_hi v241, v117 offset:5472
	ds_read_b128 v[114:117], v151 offset:6880
	ds_read_b128 v[198:201], v151 offset:7488
	s_waitcnt lgkmcnt(1)
	v_mfma_f32_16x16x32_f16 v[186:189], v[42:45], v[114:117], v[186:189]
	v_mfma_f32_16x16x32_f16 v[202:205], v[58:61], v[114:117], v[202:205]
	s_waitcnt lgkmcnt(0)
	v_mfma_f32_16x16x32_f16 v[22:25], v[42:45], v[198:201], v[22:25]
	v_mfma_f32_16x16x32_f16 v[58:61], v[58:61], v[198:201], v[38:41]
	s_nop 2
	ds_read_b128 v[38:41], v151 offset:256
	ds_read_b128 v[42:45], v151 offset:864
	s_waitcnt lgkmcnt(1)
	v_mfma_f32_16x16x32_f16 v[130:133], v[34:37], v[38:41], v[130:133]
	v_mfma_f32_16x16x32_f16 v[198:201], v[14:17], v[38:41], v[214:217]
	s_waitcnt lgkmcnt(0)
	v_mfma_f32_16x16x32_f16 v[142:145], v[34:37], v[42:45], v[142:145]
	v_mfma_f32_16x16x32_f16 v[158:161], v[14:17], v[42:45], v[158:161]
	v_add_u32_e32 v38, 0xe1080, v150
	v_min_u32_e32 v38, v38, v157
	global_load_dwordx4 v[114:117], v38, s[8:9] nt
	s_waitcnt vmcnt(21)
	v_cvt_pk_f16_f32 v39, v112, v113
	v_cvt_pk_f16_f32 v38, v110, v111
	ds_write_b16 v234, v38 offset:6080
	ds_write_b16_d16_hi v235, v38 offset:6080
	ds_write_b16 v236, v39 offset:6080
	ds_write_b16_d16_hi v237, v39 offset:6080
	ds_read_b128 v[38:41], v151 offset:1472
	ds_read_b128 v[42:45], v151 offset:2080
	s_waitcnt lgkmcnt(1)
	v_mfma_f32_16x16x32_f16 v[214:217], v[34:37], v[38:41], v[218:221]
	v_mfma_f32_16x16x32_f16 v[178:181], v[14:17], v[38:41], v[178:181]
	s_waitcnt lgkmcnt(0)
	v_mfma_f32_16x16x32_f16 v[218:221], v[14:17], v[42:45], v[2:5]
	s_nop 2
	ds_read_b128 v[2:5], v151 offset:2688
	ds_read_b128 v[38:41], v151 offset:3296
	v_mfma_f32_16x16x32_f16 v[182:185], v[34:37], v[42:45], v[182:185]
	s_waitcnt lgkmcnt(1)
	v_mfma_f32_16x16x32_f16 v[134:137], v[34:37], v[2:5], v[134:137]
	v_mfma_f32_16x16x32_f16 v[146:149], v[14:17], v[2:5], v[146:149]
	s_waitcnt lgkmcnt(0)
	v_mfma_f32_16x16x32_f16 v[206:209], v[34:37], v[38:41], v[206:209]
	v_mfma_f32_16x16x32_f16 v[122:125], v[14:17], v[38:41], v[122:125]
	v_add_u32_e32 v2, 0xf76c0, v244
	v_min_u32_e32 v2, v2, v157
	global_load_dwordx4 v[110:113], v2, s[8:9] nt
	s_waitcnt vmcnt(21)
	v_cvt_pk_f16_f32 v3, v120, v121
	v_cvt_pk_f16_f32 v2, v118, v119
	ds_write_b16 v238, v2 offset:6688
	ds_write_b16_d16_hi v239, v2 offset:6688
	ds_write_b16 v240, v3 offset:6688
	ds_write_b16_d16_hi v241, v3 offset:6688
	ds_read_b128 v[2:5], v151 offset:3904
	ds_read_b128 v[38:41], v151 offset:4512
	s_waitcnt lgkmcnt(1)
	v_mfma_f32_16x16x32_f16 v[210:213], v[34:37], v[2:5], v[210:213]
	v_mfma_f32_16x16x32_f16 v[190:193], v[14:17], v[2:5], v[190:193]
	s_waitcnt lgkmcnt(0)
	v_mfma_f32_16x16x32_f16 v[166:169], v[34:37], v[38:41], v[166:169]
	v_mfma_f32_16x16x32_f16 v[162:165], v[14:17], v[38:41], v[162:165]
	ds_read_b128 v[2:5], v151 offset:5120
	ds_read_b128 v[38:41], v151 offset:5728
	s_waitcnt lgkmcnt(1)
	v_mfma_f32_16x16x32_f16 v[98:101], v[34:37], v[2:5], v[98:101]
	v_mfma_f32_16x16x32_f16 v[138:141], v[14:17], v[2:5], v[138:141]
	s_waitcnt lgkmcnt(0)
	v_mfma_f32_16x16x32_f16 v[170:173], v[34:37], v[38:41], v[170:173]
	v_mfma_f32_16x16x32_f16 v[126:129], v[14:17], v[38:41], v[126:129]
	v_add_u32_e32 v2, 0x10dd00, v150
	v_min_u32_e32 v2, v2, v157
	v_cndmask_b32_e64 v2, 0, v2, s[0:1]
	global_load_dwordx4 v[118:121], v2, s[8:9] nt
	s_waitcnt vmcnt(21)
	v_cvt_pk_f16_f32 v3, v72, v73
	v_cvt_pk_f16_f32 v2, v70, v71
	ds_write_b16 v234, v2 offset:7296
	ds_write_b16_d16_hi v235, v2 offset:7296
	ds_write_b16 v236, v3 offset:7296
	ds_write_b16_d16_hi v237, v3 offset:7296
	ds_read_b128 v[2:5], v151 offset:6336
	ds_read_b128 v[38:41], v151 offset:6944
	ds_read_b128 v[70:73], v151 offset:7552
	s_mov_b32 s3, 0x90000
	s_waitcnt lgkmcnt(0)
	v_mfma_f32_16x16x32_f16 v[174:177], v[34:37], v[2:5], v[174:177]
	s_barrier
	v_sub_u32_e32 v245, v234, v243
	v_add_u32_e32 v246, 0xfffffdc0, v245
	v_min_u32_e32 v245, v245, v246
	v_add_u32_e32 v234, v242, v245
	v_sub_u32_e32 v245, v235, v243
	v_add_u32_e32 v246, 0xfffffdc0, v245
	v_min_u32_e32 v245, v245, v246
	v_add_u32_e32 v235, v242, v245
	v_sub_u32_e32 v245, v236, v243
	v_add_u32_e32 v246, 0xfffffdc0, v245
	v_min_u32_e32 v245, v245, v246
	v_add_u32_e32 v236, v242, v245
	v_sub_u32_e32 v245, v237, v243
	v_add_u32_e32 v246, 0xfffffdc0, v245
	v_min_u32_e32 v245, v245, v246
	v_add_u32_e32 v237, v242, v245
	v_sub_u32_e32 v245, v238, v243
	v_add_u32_e32 v246, 0xfffffdc0, v245
	v_min_u32_e32 v245, v245, v246
	v_add_u32_e32 v238, v242, v245
	v_sub_u32_e32 v245, v239, v243
	v_add_u32_e32 v246, 0xfffffdc0, v245
	v_min_u32_e32 v245, v245, v246
	v_add_u32_e32 v239, v242, v245
	v_sub_u32_e32 v245, v240, v243
	v_add_u32_e32 v246, 0xfffffdc0, v245
	v_min_u32_e32 v245, v245, v246
	v_add_u32_e32 v240, v242, v245
	v_sub_u32_e32 v245, v241, v243
	v_add_u32_e32 v246, 0xfffffdc0, v245
	v_min_u32_e32 v245, v245, v246
	v_add_u32_e32 v241, v242, v245
	v_mfma_f32_16x16x32_f16 v[194:197], v[14:17], v[2:5], v[194:197]
	v_add_co_u32_e32 v2, vcc, s3, v152
	s_mov_b32 s3, 0x94000
	s_nop 0
	v_addc_co_u32_e32 v3, vcc, 0, v153, vcc
	v_mfma_f32_16x16x32_f16 v[186:189], v[34:37], v[38:41], v[186:189]
	v_mfma_f32_16x16x32_f16 v[202:205], v[14:17], v[38:41], v[202:205]
	global_load_dwordx4 v[38:41], v[2:3], off sc1
	global_load_dwordx4 v[42:45], v[2:3], off offset:256 sc1
	v_add_co_u32_e32 v2, vcc, s3, v152
	v_mfma_f32_16x16x32_f16 v[34:37], v[34:37], v[70:73], v[22:25]
	s_nop 0
	v_addc_co_u32_e32 v3, vcc, 0, v153, vcc
	s_nop 0
	global_load_dwordx4 v[22:25], v[2:3], off sc1
	s_nop 0
	global_load_dwordx4 v[2:5], v[2:3], off offset:256 sc1
	v_mfma_f32_16x16x32_f16 v[14:17], v[14:17], v[70:73], v[58:61]
	v_add_u32_e32 v157, 0x111528dc, v154
	s_nop 1
	ds_read_b128 v[58:61], v151 offset:320
	v_add_u32_e32 v70, 0x1400, v150
	s_waitcnt vmcnt(24) lgkmcnt(0)
	v_mfma_f32_16x16x32_f16 v[130:133], v[46:49], v[58:61], v[130:133]
	s_waitcnt vmcnt(23)
	v_mfma_f32_16x16x32_f16 v[198:201], v[54:57], v[58:61], v[198:201]
	v_min_u32_e32 v58, v70, v157
	global_load_dwordx4 v[58:61], v58, s[8:9] nt
	s_waitcnt vmcnt(21)
	v_cvt_pk_f16_f32 v71, v76, v77
	v_cvt_pk_f16_f32 v70, v74, v75
	ds_write_b16 v234, v70 offset:0
	ds_write_b16_d16_hi v235, v70 offset:0
	ds_write_b16 v236, v71 offset:0
	ds_write_b16_d16_hi v237, v71 offset:0
	ds_read_b128 v[70:73], v151 offset:928
	ds_read_b128 v[74:77], v151 offset:1536
	s_waitcnt lgkmcnt(1)
	v_mfma_f32_16x16x32_f16 v[142:145], v[46:49], v[70:73], v[142:145]
	v_mfma_f32_16x16x32_f16 v[158:161], v[54:57], v[70:73], v[158:161]
	s_waitcnt lgkmcnt(0)
	v_mfma_f32_16x16x32_f16 v[214:217], v[46:49], v[74:77], v[214:217]
	v_mfma_f32_16x16x32_f16 v[178:181], v[54:57], v[74:77], v[178:181]
	ds_read_b128 v[70:73], v151 offset:2144
	ds_read_b128 v[74:77], v151 offset:2752
	s_waitcnt lgkmcnt(1)
	v_mfma_f32_16x16x32_f16 v[182:185], v[46:49], v[70:73], v[182:185]
	v_mfma_f32_16x16x32_f16 v[218:221], v[54:57], v[70:73], v[218:221]
	s_waitcnt lgkmcnt(0)
	v_mfma_f32_16x16x32_f16 v[134:137], v[46:49], v[74:77], v[134:137]
	v_mfma_f32_16x16x32_f16 v[146:149], v[54:57], v[74:77], v[146:149]
	v_add_u32_e32 v70, 0x17a40, v244
	v_min_u32_e32 v70, v70, v157
	global_load_dwordx4 v[70:73], v70, s[8:9] nt
	s_waitcnt vmcnt(21)
	v_cvt_pk_f16_f32 v75, v80, v81
	v_cvt_pk_f16_f32 v74, v78, v79
	ds_write_b16 v238, v74 offset:608
	ds_write_b16_d16_hi v239, v74 offset:608
	ds_write_b16 v240, v75 offset:608
	ds_write_b16_d16_hi v241, v75 offset:608
	ds_read_b128 v[74:77], v151 offset:3360
	ds_read_b128 v[78:81], v151 offset:5184
	s_waitcnt lgkmcnt(1)
	v_mfma_f32_16x16x32_f16 v[206:209], v[46:49], v[74:77], v[206:209]
	v_mfma_f32_16x16x32_f16 v[122:125], v[54:57], v[74:77], v[122:125]
	ds_read_b128 v[74:77], v151 offset:3968
	ds_read_b128 v[222:225], v151 offset:4576
	s_waitcnt lgkmcnt(1)
	v_mfma_f32_16x16x32_f16 v[210:213], v[46:49], v[74:77], v[210:213]
	v_mfma_f32_16x16x32_f16 v[190:193], v[54:57], v[74:77], v[190:193]
	s_waitcnt lgkmcnt(0)
	v_mfma_f32_16x16x32_f16 v[166:169], v[46:49], v[222:225], v[166:169]
	v_mfma_f32_16x16x32_f16 v[162:165], v[54:57], v[222:225], v[162:165]
	v_mfma_f32_16x16x32_f16 v[98:101], v[46:49], v[78:81], v[98:101]
	v_mfma_f32_16x16x32_f16 v[138:141], v[54:57], v[78:81], v[138:141]
	v_add_u32_e32 v74, 0x2e080, v150
	v_min_u32_e32 v74, v74, v157
	global_load_dwordx4 v[74:77], v74, s[8:9] nt
	s_waitcnt vmcnt(21)
	v_cvt_pk_f16_f32 v79, v84, v85
	v_cvt_pk_f16_f32 v78, v82, v83
	ds_write_b16 v234, v78 offset:1216
	ds_write_b16_d16_hi v235, v78 offset:1216
	ds_write_b16 v236, v79 offset:1216
	ds_write_b16_d16_hi v237, v79 offset:1216
	ds_read_b128 v[78:81], v151 offset:5792
	ds_read_b128 v[82:85], v151 offset:6400
	s_waitcnt lgkmcnt(1)
	v_mfma_f32_16x16x32_f16 v[170:173], v[46:49], v[78:81], v[170:173]
	v_mfma_f32_16x16x32_f16 v[126:129], v[54:57], v[78:81], v[126:129]
	s_waitcnt lgkmcnt(0)
	v_mfma_f32_16x16x32_f16 v[174:177], v[46:49], v[82:85], v[174:177]
	v_mfma_f32_16x16x32_f16 v[194:197], v[54:57], v[82:85], v[194:197]
	ds_read_b128 v[78:81], v151 offset:7008
	ds_read_b128 v[82:85], v151 offset:7616
	s_waitcnt lgkmcnt(1)
	v_mfma_f32_16x16x32_f16 v[186:189], v[46:49], v[78:81], v[186:189]
	v_mfma_f32_16x16x32_f16 v[202:205], v[54:57], v[78:81], v[202:205]
	s_waitcnt lgkmcnt(0)
	v_mfma_f32_16x16x32_f16 v[34:37], v[46:49], v[82:85], v[34:37]
	v_mfma_f32_16x16x32_f16 v[46:49], v[54:57], v[82:85], v[14:17]
	s_nop 2
	v_add_u32_e32 v14, 0x446c0, v244
	v_min_u32_e32 v14, v14, v157
	global_load_dwordx4 v[78:81], v14, s[8:9] nt
	s_waitcnt vmcnt(21)
	v_cvt_pk_f16_f32 v15, v52, v53
	v_cvt_pk_f16_f32 v14, v50, v51
	ds_write_b16 v238, v14 offset:1824
	ds_write_b16_d16_hi v239, v14 offset:1824
	ds_write_b16 v240, v15 offset:1824
	ds_write_b16_d16_hi v241, v15 offset:1824
	ds_read_b128 v[14:17], v151 offset:384
	ds_read_b128 v[50:53], v151 offset:992
	s_waitcnt lgkmcnt(1)
	v_mfma_f32_16x16x32_f16 v[130:133], v[26:29], v[14:17], v[130:133]
	v_mfma_f32_16x16x32_f16 v[198:201], v[10:13], v[14:17], v[198:201]
	s_waitcnt lgkmcnt(0)
	v_mfma_f32_16x16x32_f16 v[142:145], v[26:29], v[50:53], v[142:145]
	v_mfma_f32_16x16x32_f16 v[158:161], v[10:13], v[50:53], v[158:161]
	ds_read_b128 v[14:17], v151 offset:1600
	ds_read_b128 v[50:53], v151 offset:2208
	s_waitcnt lgkmcnt(1)
	v_mfma_f32_16x16x32_f16 v[214:217], v[26:29], v[14:17], v[214:217]
	v_mfma_f32_16x16x32_f16 v[178:181], v[10:13], v[14:17], v[178:181]
	s_waitcnt lgkmcnt(0)
	v_mfma_f32_16x16x32_f16 v[182:185], v[26:29], v[50:53], v[182:185]
	v_mfma_f32_16x16x32_f16 v[218:221], v[10:13], v[50:53], v[218:221]
	v_add_u32_e32 v14, 0x5ad00, v150
	v_min_u32_e32 v14, v14, v157
	global_load_dwordx4 v[82:85], v14, s[8:9] nt
	s_waitcnt vmcnt(21)
	v_cvt_pk_f16_f32 v15, v88, v89
	v_cvt_pk_f16_f32 v14, v86, v87
	ds_write_b16 v234, v14 offset:2432
	ds_write_b16_d16_hi v235, v14 offset:2432
	ds_write_b16 v236, v15 offset:2432
	ds_write_b16_d16_hi v237, v15 offset:2432
	ds_read_b128 v[14:17], v151 offset:2816
	ds_read_b128 v[50:53], v151 offset:3424
	s_waitcnt lgkmcnt(1)
	v_mfma_f32_16x16x32_f16 v[134:137], v[26:29], v[14:17], v[134:137]
	v_mfma_f32_16x16x32_f16 v[146:149], v[10:13], v[14:17], v[146:149]
	s_waitcnt lgkmcnt(0)
	v_mfma_f32_16x16x32_f16 v[206:209], v[26:29], v[50:53], v[206:209]
	v_mfma_f32_16x16x32_f16 v[122:125], v[10:13], v[50:53], v[122:125]
	ds_read_b128 v[14:17], v151 offset:4032
	ds_read_b128 v[50:53], v151 offset:4640
	s_waitcnt lgkmcnt(1)
	v_mfma_f32_16x16x32_f16 v[210:213], v[26:29], v[14:17], v[210:213]
	v_mfma_f32_16x16x32_f16 v[190:193], v[10:13], v[14:17], v[190:193]
	s_waitcnt lgkmcnt(0)
	v_mfma_f32_16x16x32_f16 v[166:169], v[26:29], v[50:53], v[166:169]
	v_mfma_f32_16x16x32_f16 v[162:165], v[10:13], v[50:53], v[162:165]
	v_add_u32_e32 v14, 0x71340, v244
	v_min_u32_e32 v14, v14, v157
	global_load_dwordx4 v[86:89], v14, s[8:9] nt
	s_waitcnt vmcnt(21)
	v_cvt_pk_f16_f32 v15, v92, v93
	v_cvt_pk_f16_f32 v14, v90, v91
	ds_write_b16 v238, v14 offset:3040
	ds_write_b16_d16_hi v239, v14 offset:3040
	ds_write_b16 v240, v15 offset:3040
	ds_write_b16_d16_hi v241, v15 offset:3040
	ds_read_b128 v[14:17], v151 offset:5248
	ds_read_b128 v[50:53], v151 offset:5856
	s_waitcnt lgkmcnt(1)
	v_mfma_f32_16x16x32_f16 v[222:225], v[26:29], v[14:17], v[98:101]
	v_mfma_f32_16x16x32_f16 v[138:141], v[10:13], v[14:17], v[138:141]
	s_waitcnt lgkmcnt(0)
	v_mfma_f32_16x16x32_f16 v[170:173], v[26:29], v[50:53], v[170:173]
	v_mfma_f32_16x16x32_f16 v[126:129], v[10:13], v[50:53], v[126:129]
	ds_read_b128 v[14:17], v151 offset:6464
	ds_read_b128 v[50:53], v151 offset:7072
	s_waitcnt lgkmcnt(1)
	v_mfma_f32_16x16x32_f16 v[174:177], v[26:29], v[14:17], v[174:177]
	v_mfma_f32_16x16x32_f16 v[194:197], v[10:13], v[14:17], v[194:197]
	s_waitcnt lgkmcnt(0)
	v_mfma_f32_16x16x32_f16 v[186:189], v[26:29], v[50:53], v[186:189]
	v_mfma_f32_16x16x32_f16 v[202:205], v[10:13], v[50:53], v[202:205]
	v_add_u32_e32 v14, 0x87980, v150
	v_min_u32_e32 v14, v14, v157
	global_load_dwordx4 v[90:93], v14, s[8:9] nt
	s_waitcnt vmcnt(21)
	v_cvt_pk_f16_f32 v15, v96, v97
	v_cvt_pk_f16_f32 v14, v94, v95
	ds_write_b16 v234, v14 offset:3648
	ds_write_b16_d16_hi v235, v14 offset:3648
	ds_write_b16 v236, v15 offset:3648
	ds_write_b16_d16_hi v237, v15 offset:3648
	ds_read_b128 v[94:97], v151 offset:7680
	s_mov_b32 s3, 0x98000
	v_add_co_u32_e32 v14, vcc, s3, v152
	s_mov_b32 s3, 0x9c000
	s_nop 0
	v_addc_co_u32_e32 v15, vcc, 0, v153, vcc
	global_load_dwordx4 v[50:53], v[14:15], off sc1
	global_load_dwordx4 v[54:57], v[14:15], off offset:256 sc1
	v_add_co_u32_e32 v14, vcc, s3, v152
	s_waitcnt lgkmcnt(0)
	v_mfma_f32_16x16x32_f16 v[34:37], v[26:29], v[94:97], v[34:37]
	v_addc_co_u32_e32 v15, vcc, 0, v153, vcc
	global_load_dwordx4 v[26:29], v[14:15], off sc1
	s_nop 0
	global_load_dwordx4 v[14:17], v[14:15], off offset:256 sc1
	v_mfma_f32_16x16x32_f16 v[10:13], v[10:13], v[94:97], v[46:49]
	s_nop 2
	ds_read_b128 v[46:49], v151 offset:448
	ds_read_b128 v[94:97], v151 offset:1056
	s_waitcnt vmcnt(24) lgkmcnt(1)
	v_mfma_f32_16x16x32_f16 v[130:133], v[62:65], v[46:49], v[130:133]
	s_waitcnt lgkmcnt(0)
	v_mfma_f32_16x16x32_f16 v[142:145], v[62:65], v[94:97], v[142:145]
	s_waitcnt vmcnt(23)
	v_mfma_f32_16x16x32_f16 v[158:161], v[66:69], v[94:97], v[158:161]
	ds_read_b128 v[94:97], v151 offset:1664
	v_mfma_f32_16x16x32_f16 v[46:49], v[66:69], v[46:49], v[198:201]
	s_waitcnt lgkmcnt(0)
	v_mfma_f32_16x16x32_f16 v[198:201], v[62:65], v[94:97], v[214:217]
	v_mfma_f32_16x16x32_f16 v[178:181], v[66:69], v[94:97], v[178:181]
	v_add_u32_e32 v94, 0x9dfc0, v244
	v_min_u32_e32 v94, v94, v157
	global_load_dwordx4 v[94:97], v94, s[8:9] nt
	s_waitcnt vmcnt(21)
	v_cvt_pk_f16_f32 v9, v8, v9
	v_cvt_pk_f16_f32 v8, v6, v7
	ds_write_b16 v238, v8 offset:4256
	ds_write_b16_d16_hi v239, v8 offset:4256
	ds_write_b16 v240, v9 offset:4256
	ds_write_b16_d16_hi v241, v9 offset:4256
	ds_read_b128 v[6:9], v151 offset:2272
	ds_read_b128 v[98:101], v151 offset:2880
	s_waitcnt lgkmcnt(1)
	v_mfma_f32_16x16x32_f16 v[182:185], v[62:65], v[6:9], v[182:185]
	s_waitcnt lgkmcnt(0)
	v_mfma_f32_16x16x32_f16 v[134:137], v[62:65], v[98:101], v[134:137]
	v_mfma_f32_16x16x32_f16 v[146:149], v[66:69], v[98:101], v[146:149]
	ds_read_b128 v[98:101], v151 offset:3488
	ds_read_b128 v[214:217], v151 offset:4096
	v_mfma_f32_16x16x32_f16 v[6:9], v[66:69], v[6:9], v[218:221]
	s_waitcnt lgkmcnt(1)
	v_mfma_f32_16x16x32_f16 v[206:209], v[62:65], v[98:101], v[206:209]
	v_mfma_f32_16x16x32_f16 v[122:125], v[66:69], v[98:101], v[122:125]
	s_waitcnt lgkmcnt(0)
	v_mfma_f32_16x16x32_f16 v[210:213], v[62:65], v[214:217], v[210:213]
	v_mfma_f32_16x16x32_f16 v[190:193], v[66:69], v[214:217], v[190:193]
	v_add_u32_e32 v98, 0xb4600, v150
	v_min_u32_e32 v98, v98, v157
	global_load_dwordx4 v[98:101], v98, s[8:9] nt
	s_waitcnt vmcnt(21)
	v_cvt_pk_f16_f32 v105, v104, v105
	v_cvt_pk_f16_f32 v104, v102, v103
	ds_write_b16 v234, v104 offset:4864
	ds_write_b16_d16_hi v235, v104 offset:4864
	ds_write_b16 v236, v105 offset:4864
	ds_write_b16_d16_hi v237, v105 offset:4864
	ds_read_b128 v[102:105], v151 offset:4704
	ds_read_b128 v[214:217], v151 offset:6528
	s_waitcnt lgkmcnt(1)
	v_mfma_f32_16x16x32_f16 v[166:169], v[62:65], v[102:105], v[166:169]
	v_mfma_f32_16x16x32_f16 v[162:165], v[66:69], v[102:105], v[162:165]
	ds_read_b128 v[102:105], v151 offset:5312
	ds_read_b128 v[218:221], v151 offset:5920
	s_waitcnt lgkmcnt(1)
	v_mfma_f32_16x16x32_f16 v[222:225], v[62:65], v[102:105], v[222:225]
	v_mfma_f32_16x16x32_f16 v[138:141], v[66:69], v[102:105], v[138:141]
	s_waitcnt lgkmcnt(0)
	v_mfma_f32_16x16x32_f16 v[170:173], v[62:65], v[218:221], v[170:173]
	v_mfma_f32_16x16x32_f16 v[126:129], v[66:69], v[218:221], v[126:129]
	v_mfma_f32_16x16x32_f16 v[174:177], v[62:65], v[214:217], v[174:177]
	v_mfma_f32_16x16x32_f16 v[194:197], v[66:69], v[214:217], v[194:197]
	v_add_u32_e32 v102, 0xcac40, v244
	v_min_u32_e32 v102, v102, v157
	global_load_dwordx4 v[102:105], v102, s[8:9] nt
	s_waitcnt vmcnt(21)
	v_cvt_pk_f16_f32 v109, v108, v109
	v_cvt_pk_f16_f32 v108, v106, v107
	ds_write_b16 v238, v108 offset:5472
	ds_write_b16_d16_hi v239, v108 offset:5472
	ds_write_b16 v240, v109 offset:5472
	ds_write_b16_d16_hi v241, v109 offset:5472
	ds_read_b128 v[106:109], v151 offset:7136
	ds_read_b128 v[214:217], v151 offset:7744
	s_waitcnt lgkmcnt(1)
	v_mfma_f32_16x16x32_f16 v[186:189], v[62:65], v[106:109], v[186:189]
	s_waitcnt lgkmcnt(0)
	v_mfma_f32_16x16x32_f16 v[218:221], v[62:65], v[214:217], v[34:37]
	v_mfma_f32_16x16x32_f16 v[214:217], v[66:69], v[214:217], v[10:13]
	s_nop 2
	ds_read_b128 v[10:13], v151 offset:512
	ds_read_b128 v[34:37], v151 offset:1120
	v_mfma_f32_16x16x32_f16 v[202:205], v[66:69], v[106:109], v[202:205]
	s_waitcnt lgkmcnt(1)
	v_mfma_f32_16x16x32_f16 v[130:133], v[30:33], v[10:13], v[130:133]
	v_mfma_f32_16x16x32_f16 v[226:229], v[18:21], v[10:13], v[46:49]
	s_waitcnt lgkmcnt(0)
	v_mfma_f32_16x16x32_f16 v[142:145], v[30:33], v[34:37], v[142:145]
	v_mfma_f32_16x16x32_f16 v[158:161], v[18:21], v[34:37], v[158:161]
	v_add_u32_e32 v10, 0xe1280, v150
	v_min_u32_e32 v10, v10, v157
	global_load_dwordx4 v[62:65], v10, s[8:9] nt
	s_waitcnt vmcnt(21)
	v_cvt_pk_f16_f32 v11, v116, v117
	v_cvt_pk_f16_f32 v10, v114, v115
	ds_write_b16 v234, v10 offset:6080
	ds_write_b16_d16_hi v235, v10 offset:6080
	ds_write_b16 v236, v11 offset:6080
	ds_write_b16_d16_hi v237, v11 offset:6080
	ds_read_b128 v[10:13], v151 offset:1728
	ds_read_b128 v[34:37], v151 offset:2336
	s_waitcnt lgkmcnt(1)
	v_mfma_f32_16x16x32_f16 v[114:117], v[30:33], v[10:13], v[198:201]
	v_mfma_f32_16x16x32_f16 v[178:181], v[18:21], v[10:13], v[178:181]
	s_waitcnt lgkmcnt(0)
	v_mfma_f32_16x16x32_f16 v[198:201], v[18:21], v[34:37], v[6:9]
	s_nop 2
	ds_read_b128 v[6:9], v151 offset:2944
	ds_read_b128 v[10:13], v151 offset:3552
	v_mfma_f32_16x16x32_f16 v[182:185], v[30:33], v[34:37], v[182:185]
	s_waitcnt lgkmcnt(1)
	v_mfma_f32_16x16x32_f16 v[134:137], v[30:33], v[6:9], v[134:137]
	v_mfma_f32_16x16x32_f16 v[146:149], v[18:21], v[6:9], v[146:149]
	s_waitcnt lgkmcnt(0)
	v_mfma_f32_16x16x32_f16 v[206:209], v[30:33], v[10:13], v[206:209]
	v_mfma_f32_16x16x32_f16 v[122:125], v[18:21], v[10:13], v[122:125]
	v_add_u32_e32 v6, 0xf78c0, v244
	v_min_u32_e32 v6, v6, v157
	global_load_dwordx4 v[66:69], v6, s[8:9] nt
	s_waitcnt vmcnt(21)
	v_cvt_pk_f16_f32 v7, v112, v113
	v_cvt_pk_f16_f32 v6, v110, v111
	ds_write_b16 v238, v6 offset:6688
	ds_write_b16_d16_hi v239, v6 offset:6688
	ds_write_b16 v240, v7 offset:6688
	ds_write_b16_d16_hi v241, v7 offset:6688
	ds_read_b128 v[6:9], v151 offset:4160
	ds_read_b128 v[10:13], v151 offset:4768
	s_waitcnt lgkmcnt(1)
	v_mfma_f32_16x16x32_f16 v[210:213], v[30:33], v[6:9], v[210:213]
	v_mfma_f32_16x16x32_f16 v[190:193], v[18:21], v[6:9], v[190:193]
	s_waitcnt lgkmcnt(0)
	v_mfma_f32_16x16x32_f16 v[166:169], v[30:33], v[10:13], v[166:169]
	v_mfma_f32_16x16x32_f16 v[162:165], v[18:21], v[10:13], v[162:165]
	ds_read_b128 v[6:9], v151 offset:5376
	ds_read_b128 v[10:13], v151 offset:5984
	s_waitcnt lgkmcnt(1)
	v_mfma_f32_16x16x32_f16 v[222:225], v[30:33], v[6:9], v[222:225]
	v_mfma_f32_16x16x32_f16 v[138:141], v[18:21], v[6:9], v[138:141]
	s_waitcnt lgkmcnt(0)
	v_mfma_f32_16x16x32_f16 v[170:173], v[30:33], v[10:13], v[170:173]
	v_mfma_f32_16x16x32_f16 v[126:129], v[18:21], v[10:13], v[126:129]
	v_add_u32_e32 v6, 0x10df00, v150
	v_min_u32_e32 v6, v6, v157
	v_cndmask_b32_e64 v6, 0, v6, s[0:1]
	global_load_dwordx4 v[106:109], v6, s[8:9] nt
	s_waitcnt vmcnt(21)
	v_cvt_pk_f16_f32 v7, v120, v121
	v_cvt_pk_f16_f32 v6, v118, v119
	ds_write_b16 v234, v6 offset:7296
	ds_write_b16_d16_hi v235, v6 offset:7296
	ds_write_b16 v236, v7 offset:7296
	ds_write_b16_d16_hi v237, v7 offset:7296
	ds_read_b128 v[6:9], v151 offset:6592
	ds_read_b128 v[10:13], v151 offset:7200
	s_mov_b32 s3, 0xa0000
	ds_read_b128 v[110:113], v151 offset:7808
	s_waitcnt lgkmcnt(0)
	v_mfma_f32_16x16x32_f16 v[118:121], v[30:33], v[6:9], v[174:177]
	s_barrier
	v_sub_u32_e32 v245, v234, v243
	v_add_u32_e32 v246, 0xfffffdc0, v245
	v_min_u32_e32 v245, v245, v246
	v_add_u32_e32 v234, v242, v245
	v_sub_u32_e32 v245, v235, v243
	v_add_u32_e32 v246, 0xfffffdc0, v245
	v_min_u32_e32 v245, v245, v246
	v_add_u32_e32 v235, v242, v245
	v_sub_u32_e32 v245, v236, v243
	v_add_u32_e32 v246, 0xfffffdc0, v245
	v_min_u32_e32 v245, v245, v246
	v_add_u32_e32 v236, v242, v245
	v_sub_u32_e32 v245, v237, v243
	v_add_u32_e32 v246, 0xfffffdc0, v245
	v_min_u32_e32 v245, v245, v246
	v_add_u32_e32 v237, v242, v245
	v_sub_u32_e32 v245, v238, v243
	v_add_u32_e32 v246, 0xfffffdc0, v245
	v_min_u32_e32 v245, v245, v246
	v_add_u32_e32 v238, v242, v245
	v_sub_u32_e32 v245, v239, v243
	v_add_u32_e32 v246, 0xfffffdc0, v245
	v_min_u32_e32 v245, v245, v246
	v_add_u32_e32 v239, v242, v245
	v_sub_u32_e32 v245, v240, v243
	v_add_u32_e32 v246, 0xfffffdc0, v245
	v_min_u32_e32 v245, v245, v246
	v_add_u32_e32 v240, v242, v245
	v_sub_u32_e32 v245, v241, v243
	v_add_u32_e32 v246, 0xfffffdc0, v245
	v_min_u32_e32 v245, v245, v246
	v_add_u32_e32 v241, v242, v245
	v_mfma_f32_16x16x32_f16 v[174:177], v[18:21], v[6:9], v[194:197]
	v_add_co_u32_e32 v6, vcc, s3, v152
	s_mov_b32 s3, 0xa4000
	s_nop 0
	v_addc_co_u32_e32 v7, vcc, 0, v153, vcc
	global_load_dwordx4 v[34:37], v[6:7], off sc1
	global_load_dwordx4 v[46:49], v[6:7], off offset:256 sc1
	v_add_co_u32_e32 v6, vcc, s3, v152
	v_mfma_f32_16x16x32_f16 v[186:189], v[30:33], v[10:13], v[186:189]
	s_nop 0
	v_addc_co_u32_e32 v7, vcc, 0, v153, vcc
	v_mfma_f32_16x16x32_f16 v[194:197], v[18:21], v[10:13], v[202:205]
	global_load_dwordx4 v[10:13], v[6:7], off sc1
	s_nop 0
	global_load_dwordx4 v[6:9], v[6:7], off offset:256 sc1
	v_mfma_f32_16x16x32_f16 v[30:33], v[30:33], v[110:113], v[218:221]
	v_mfma_f32_16x16x32_f16 v[18:21], v[18:21], v[110:113], v[214:217]
	v_min_u32_e32 v110, 0x54, v154
	v_add_u32_e32 v154, 0x11152adc, v110
	ds_read_b128 v[110:113], v151 offset:0
	v_add_u32_e32 v157, 0x1600, v150
	s_waitcnt vmcnt(24) lgkmcnt(0)
	v_mfma_f32_16x16x32_f16 v[130:133], v[38:41], v[110:113], v[130:133]
	s_waitcnt vmcnt(23)
	v_mfma_f32_16x16x32_f16 v[202:205], v[42:45], v[110:113], v[226:229]
	v_min_u32_e32 v110, v157, v154
	global_load_dwordx4 v[110:113], v110, s[8:9] nt
	s_waitcnt vmcnt(21)
	v_cvt_pk_f16_f32 v61, v60, v61
	v_cvt_pk_f16_f32 v60, v58, v59
	ds_write_b16 v234, v60 offset:0
	ds_write_b16_d16_hi v235, v60 offset:0
	ds_write_b16 v236, v61 offset:0
	ds_write_b16_d16_hi v237, v61 offset:0
	ds_read_b128 v[58:61], v151 offset:608
	ds_read_b128 v[214:217], v151 offset:1216
	s_waitcnt lgkmcnt(1)
	v_mfma_f32_16x16x32_f16 v[142:145], v[38:41], v[58:61], v[142:145]
	v_mfma_f32_16x16x32_f16 v[158:161], v[42:45], v[58:61], v[158:161]
	s_waitcnt lgkmcnt(0)
	v_mfma_f32_16x16x32_f16 v[114:117], v[38:41], v[214:217], v[114:117]
	v_mfma_f32_16x16x32_f16 v[178:181], v[42:45], v[214:217], v[178:181]
	ds_read_b128 v[58:61], v151 offset:1824
	ds_read_b128 v[214:217], v151 offset:2432
	s_waitcnt lgkmcnt(1)
	v_mfma_f32_16x16x32_f16 v[182:185], v[38:41], v[58:61], v[182:185]
	v_mfma_f32_16x16x32_f16 v[198:201], v[42:45], v[58:61], v[198:201]
	s_waitcnt lgkmcnt(0)
	v_mfma_f32_16x16x32_f16 v[134:137], v[38:41], v[214:217], v[134:137]
	v_mfma_f32_16x16x32_f16 v[146:149], v[42:45], v[214:217], v[146:149]
	v_add_u32_e32 v58, 0x17c40, v244
	v_min_u32_e32 v58, v58, v154
	global_load_dwordx4 v[58:61], v58, s[8:9] nt
	s_waitcnt vmcnt(21)
	v_cvt_pk_f16_f32 v73, v72, v73
	v_cvt_pk_f16_f32 v72, v70, v71
	ds_write_b16 v238, v72 offset:608
	ds_write_b16_d16_hi v239, v72 offset:608
	ds_write_b16 v240, v73 offset:608
	ds_write_b16_d16_hi v241, v73 offset:608
	ds_read_b128 v[70:73], v151 offset:3040
	ds_read_b128 v[214:217], v151 offset:4864
	s_waitcnt lgkmcnt(1)
	v_mfma_f32_16x16x32_f16 v[206:209], v[38:41], v[70:73], v[206:209]
	v_mfma_f32_16x16x32_f16 v[122:125], v[42:45], v[70:73], v[122:125]
	ds_read_b128 v[70:73], v151 offset:3648
	ds_read_b128 v[218:221], v151 offset:4256
	s_waitcnt lgkmcnt(1)
	v_mfma_f32_16x16x32_f16 v[210:213], v[38:41], v[70:73], v[210:213]
	v_mfma_f32_16x16x32_f16 v[190:193], v[42:45], v[70:73], v[190:193]
	s_waitcnt lgkmcnt(0)
	v_mfma_f32_16x16x32_f16 v[166:169], v[38:41], v[218:221], v[166:169]
	v_mfma_f32_16x16x32_f16 v[162:165], v[42:45], v[218:221], v[162:165]
	v_mfma_f32_16x16x32_f16 v[218:221], v[38:41], v[214:217], v[222:225]
	v_mfma_f32_16x16x32_f16 v[138:141], v[42:45], v[214:217], v[138:141]
	v_add_u32_e32 v70, 0x2e280, v150
	v_min_u32_e32 v70, v70, v154
	global_load_dwordx4 v[70:73], v70, s[8:9] nt
	s_waitcnt vmcnt(21)
	v_cvt_pk_f16_f32 v77, v76, v77
	v_cvt_pk_f16_f32 v76, v74, v75
	ds_write_b16 v234, v76 offset:1216
	ds_write_b16_d16_hi v235, v76 offset:1216
	ds_write_b16 v236, v77 offset:1216
	ds_write_b16_d16_hi v237, v77 offset:1216
	ds_read_b128 v[74:77], v151 offset:5472
	ds_read_b128 v[214:217], v151 offset:6080
	s_waitcnt lgkmcnt(1)
	v_mfma_f32_16x16x32_f16 v[170:173], v[38:41], v[74:77], v[170:173]
	v_mfma_f32_16x16x32_f16 v[126:129], v[42:45], v[74:77], v[126:129]
	s_waitcnt lgkmcnt(0)
	v_mfma_f32_16x16x32_f16 v[118:121], v[38:41], v[214:217], v[118:121]
	v_mfma_f32_16x16x32_f16 v[174:177], v[42:45], v[214:217], v[174:177]
	ds_read_b128 v[74:77], v151 offset:6688
	ds_read_b128 v[214:217], v151 offset:7296
	s_waitcnt lgkmcnt(1)
	v_mfma_f32_16x16x32_f16 v[186:189], v[38:41], v[74:77], v[186:189]
	v_mfma_f32_16x16x32_f16 v[194:197], v[42:45], v[74:77], v[194:197]
	s_waitcnt lgkmcnt(0)
	v_mfma_f32_16x16x32_f16 v[30:33], v[38:41], v[214:217], v[30:33]
	v_mfma_f32_16x16x32_f16 v[214:217], v[42:45], v[214:217], v[18:21]
	s_nop 2
	v_add_u32_e32 v18, 0x448c0, v244
	v_min_u32_e32 v18, v18, v154
	global_load_dwordx4 v[42:45], v18, s[8:9] nt
	s_waitcnt vmcnt(21)
	v_cvt_pk_f16_f32 v19, v80, v81
	v_cvt_pk_f16_f32 v18, v78, v79
	ds_write_b16 v238, v18 offset:1824
	ds_write_b16_d16_hi v239, v18 offset:1824
	ds_write_b16 v240, v19 offset:1824
	ds_write_b16_d16_hi v241, v19 offset:1824
	ds_read_b128 v[18:21], v151 offset:64
	ds_read_b128 v[38:41], v151 offset:672
	s_waitcnt lgkmcnt(1)
	v_mfma_f32_16x16x32_f16 v[130:133], v[22:25], v[18:21], v[130:133]
	v_mfma_f32_16x16x32_f16 v[202:205], v[2:5], v[18:21], v[202:205]
	s_waitcnt lgkmcnt(0)
	v_mfma_f32_16x16x32_f16 v[142:145], v[22:25], v[38:41], v[142:145]
	v_mfma_f32_16x16x32_f16 v[158:161], v[2:5], v[38:41], v[158:161]
	ds_read_b128 v[18:21], v151 offset:1280
	ds_read_b128 v[38:41], v151 offset:1888
	s_waitcnt lgkmcnt(1)
	v_mfma_f32_16x16x32_f16 v[114:117], v[22:25], v[18:21], v[114:117]
	v_mfma_f32_16x16x32_f16 v[178:181], v[2:5], v[18:21], v[178:181]
	s_waitcnt lgkmcnt(0)
	v_mfma_f32_16x16x32_f16 v[182:185], v[22:25], v[38:41], v[182:185]
	v_mfma_f32_16x16x32_f16 v[198:201], v[2:5], v[38:41], v[198:201]
	v_add_u32_e32 v18, 0x5af00, v150
	v_min_u32_e32 v18, v18, v154
	global_load_dwordx4 v[74:77], v18, s[8:9] nt
	s_waitcnt vmcnt(21)
	v_cvt_pk_f16_f32 v19, v84, v85
	v_cvt_pk_f16_f32 v18, v82, v83
	ds_write_b16 v234, v18 offset:2432
	ds_write_b16_d16_hi v235, v18 offset:2432
	ds_write_b16 v236, v19 offset:2432
	ds_write_b16_d16_hi v237, v19 offset:2432
	ds_read_b128 v[18:21], v151 offset:2496
	ds_read_b128 v[38:41], v151 offset:3104
	s_waitcnt lgkmcnt(1)
	v_mfma_f32_16x16x32_f16 v[134:137], v[22:25], v[18:21], v[134:137]
	v_mfma_f32_16x16x32_f16 v[146:149], v[2:5], v[18:21], v[146:149]
	s_waitcnt lgkmcnt(0)
	v_mfma_f32_16x16x32_f16 v[206:209], v[22:25], v[38:41], v[206:209]
	v_mfma_f32_16x16x32_f16 v[122:125], v[2:5], v[38:41], v[122:125]
	ds_read_b128 v[18:21], v151 offset:3712
	ds_read_b128 v[38:41], v151 offset:4320
	s_waitcnt lgkmcnt(1)
	v_mfma_f32_16x16x32_f16 v[210:213], v[22:25], v[18:21], v[210:213]
	v_mfma_f32_16x16x32_f16 v[190:193], v[2:5], v[18:21], v[190:193]
	s_waitcnt lgkmcnt(0)
	v_mfma_f32_16x16x32_f16 v[166:169], v[22:25], v[38:41], v[166:169]
	v_mfma_f32_16x16x32_f16 v[162:165], v[2:5], v[38:41], v[162:165]
	v_add_u32_e32 v18, 0x71540, v244
	v_min_u32_e32 v18, v18, v154
	global_load_dwordx4 v[78:81], v18, s[8:9] nt
	s_waitcnt vmcnt(21)
	v_cvt_pk_f16_f32 v19, v88, v89
	v_cvt_pk_f16_f32 v18, v86, v87
	ds_write_b16 v238, v18 offset:3040
	ds_write_b16_d16_hi v239, v18 offset:3040
	ds_write_b16 v240, v19 offset:3040
	ds_write_b16_d16_hi v241, v19 offset:3040
	ds_read_b128 v[18:21], v151 offset:4928
	ds_read_b128 v[38:41], v151 offset:5536
	s_waitcnt lgkmcnt(1)
	v_mfma_f32_16x16x32_f16 v[218:221], v[22:25], v[18:21], v[218:221]
	v_mfma_f32_16x16x32_f16 v[138:141], v[2:5], v[18:21], v[138:141]
	s_waitcnt lgkmcnt(0)
	v_mfma_f32_16x16x32_f16 v[170:173], v[22:25], v[38:41], v[170:173]
	v_mfma_f32_16x16x32_f16 v[126:129], v[2:5], v[38:41], v[126:129]
	ds_read_b128 v[18:21], v151 offset:6144
	ds_read_b128 v[38:41], v151 offset:6752
	s_waitcnt lgkmcnt(1)
	v_mfma_f32_16x16x32_f16 v[118:121], v[22:25], v[18:21], v[118:121]
	v_mfma_f32_16x16x32_f16 v[174:177], v[2:5], v[18:21], v[174:177]
	s_waitcnt lgkmcnt(0)
	v_mfma_f32_16x16x32_f16 v[186:189], v[22:25], v[38:41], v[186:189]
	v_mfma_f32_16x16x32_f16 v[194:197], v[2:5], v[38:41], v[194:197]
	v_add_u32_e32 v18, 0x87b80, v150
	v_min_u32_e32 v18, v18, v154
	global_load_dwordx4 v[82:85], v18, s[8:9] nt
	s_waitcnt vmcnt(21)
	v_cvt_pk_f16_f32 v19, v92, v93
	v_cvt_pk_f16_f32 v18, v90, v91
	ds_write_b16 v234, v18 offset:3648
	ds_write_b16_d16_hi v235, v18 offset:3648
	ds_write_b16 v236, v19 offset:3648
	ds_write_b16_d16_hi v237, v19 offset:3648
	ds_read_b128 v[86:89], v151 offset:7360
	s_mov_b32 s3, 0xa8000
	v_add_co_u32_e32 v18, vcc, s3, v152
	s_mov_b32 s3, 0xac000
	s_nop 0
	v_addc_co_u32_e32 v19, vcc, 0, v153, vcc
	s_waitcnt lgkmcnt(0)
	v_mfma_f32_16x16x32_f16 v[222:225], v[22:25], v[86:89], v[30:33]
	s_nop 2
	global_load_dwordx4 v[30:33], v[18:19], off sc1
	global_load_dwordx4 v[38:41], v[18:19], off offset:256 sc1
	v_add_co_u32_e32 v18, vcc, s3, v152
	v_mfma_f32_16x16x32_f16 v[2:5], v[2:5], v[86:89], v[214:217]
	s_nop 0
	v_addc_co_u32_e32 v19, vcc, 0, v153, vcc
	global_load_dwordx4 v[22:25], v[18:19], off sc1
	s_nop 0
	global_load_dwordx4 v[18:21], v[18:19], off offset:256 sc1
	ds_read_b128 v[86:89], v151 offset:128
	ds_read_b128 v[90:93], v151 offset:736
	s_waitcnt vmcnt(24) lgkmcnt(1)
	v_mfma_f32_16x16x32_f16 v[130:133], v[50:53], v[86:89], v[130:133]
	s_waitcnt vmcnt(23)
	v_mfma_f32_16x16x32_f16 v[202:205], v[54:57], v[86:89], v[202:205]
	ds_read_b128 v[86:89], v151 offset:1344
	s_waitcnt lgkmcnt(0)
	v_mfma_f32_16x16x32_f16 v[114:117], v[50:53], v[86:89], v[114:117]
	v_mfma_f32_16x16x32_f16 v[142:145], v[50:53], v[90:93], v[142:145]
	v_mfma_f32_16x16x32_f16 v[158:161], v[54:57], v[90:93], v[158:161]
	v_mfma_f32_16x16x32_f16 v[178:181], v[54:57], v[86:89], v[178:181]
	v_add_u32_e32 v86, 0x9e1c0, v244
	v_min_u32_e32 v86, v86, v154
	global_load_dwordx4 v[86:89], v86, s[8:9] nt
	s_waitcnt vmcnt(21)
	v_cvt_pk_f16_f32 v91, v96, v97
	v_cvt_pk_f16_f32 v90, v94, v95
	ds_write_b16 v238, v90 offset:4256
	ds_write_b16_d16_hi v239, v90 offset:4256
	ds_write_b16 v240, v91 offset:4256
	ds_write_b16_d16_hi v241, v91 offset:4256
	ds_read_b128 v[90:93], v151 offset:1952
	ds_read_b128 v[94:97], v151 offset:2560
	s_waitcnt lgkmcnt(1)
	v_mfma_f32_16x16x32_f16 v[182:185], v[50:53], v[90:93], v[182:185]
	v_mfma_f32_16x16x32_f16 v[198:201], v[54:57], v[90:93], v[198:201]
	s_waitcnt lgkmcnt(0)
	v_mfma_f32_16x16x32_f16 v[134:137], v[50:53], v[94:97], v[134:137]
	v_mfma_f32_16x16x32_f16 v[146:149], v[54:57], v[94:97], v[146:149]
	ds_read_b128 v[90:93], v151 offset:3168
	ds_read_b128 v[94:97], v151 offset:3776
	s_waitcnt lgkmcnt(1)
	v_mfma_f32_16x16x32_f16 v[206:209], v[50:53], v[90:93], v[206:209]
	v_mfma_f32_16x16x32_f16 v[122:125], v[54:57], v[90:93], v[122:125]
	s_waitcnt lgkmcnt(0)
	v_mfma_f32_16x16x32_f16 v[210:213], v[50:53], v[94:97], v[210:213]
	v_mfma_f32_16x16x32_f16 v[190:193], v[54:57], v[94:97], v[190:193]
	v_add_u32_e32 v90, 0xb4800, v150
	v_min_u32_e32 v90, v90, v154
	global_load_dwordx4 v[90:93], v90, s[8:9] nt
	s_waitcnt vmcnt(21)
	v_cvt_pk_f16_f32 v95, v100, v101
	v_cvt_pk_f16_f32 v94, v98, v99
	ds_write_b16 v234, v94 offset:4864
	ds_write_b16_d16_hi v235, v94 offset:4864
	ds_write_b16 v236, v95 offset:4864
	ds_write_b16_d16_hi v237, v95 offset:4864
	ds_read_b128 v[94:97], v151 offset:4384
	ds_read_b128 v[98:101], v151 offset:6208
	s_waitcnt lgkmcnt(1)
	v_mfma_f32_16x16x32_f16 v[166:169], v[50:53], v[94:97], v[166:169]
	v_mfma_f32_16x16x32_f16 v[162:165], v[54:57], v[94:97], v[162:165]
	ds_read_b128 v[94:97], v151 offset:4992
	ds_read_b128 v[214:217], v151 offset:5600
	s_waitcnt lgkmcnt(1)
	v_mfma_f32_16x16x32_f16 v[218:221], v[50:53], v[94:97], v[218:221]
	v_mfma_f32_16x16x32_f16 v[138:141], v[54:57], v[94:97], v[138:141]
	s_waitcnt lgkmcnt(0)
	v_mfma_f32_16x16x32_f16 v[170:173], v[50:53], v[214:217], v[170:173]
	v_mfma_f32_16x16x32_f16 v[126:129], v[54:57], v[214:217], v[126:129]
	v_mfma_f32_16x16x32_f16 v[118:121], v[50:53], v[98:101], v[118:121]
	v_mfma_f32_16x16x32_f16 v[174:177], v[54:57], v[98:101], v[174:177]
	v_add_u32_e32 v94, 0xcae40, v244
	v_min_u32_e32 v94, v94, v154
	global_load_dwordx4 v[94:97], v94, s[8:9] nt
	s_waitcnt vmcnt(21)
	v_cvt_pk_f16_f32 v99, v104, v105
	v_cvt_pk_f16_f32 v98, v102, v103
	ds_write_b16 v238, v98 offset:5472
	ds_write_b16_d16_hi v239, v98 offset:5472
	ds_write_b16 v240, v99 offset:5472
	ds_write_b16_d16_hi v241, v99 offset:5472
	ds_read_b128 v[98:101], v151 offset:6816
	ds_read_b128 v[102:105], v151 offset:7424
	s_waitcnt lgkmcnt(1)
	v_mfma_f32_16x16x32_f16 v[186:189], v[50:53], v[98:101], v[186:189]
	s_waitcnt lgkmcnt(0)
	v_mfma_f32_16x16x32_f16 v[214:217], v[50:53], v[102:105], v[222:225]
	v_mfma_f32_16x16x32_f16 v[102:105], v[54:57], v[102:105], v[2:5]
	s_nop 2
	ds_read_b128 v[2:5], v151 offset:192
	ds_read_b128 v[50:53], v151 offset:800
	v_mfma_f32_16x16x32_f16 v[194:197], v[54:57], v[98:101], v[194:197]
	s_waitcnt lgkmcnt(1)
	v_mfma_f32_16x16x32_f16 v[130:133], v[26:29], v[2:5], v[130:133]
	v_mfma_f32_16x16x32_f16 v[202:205], v[14:17], v[2:5], v[202:205]
	s_waitcnt lgkmcnt(0)
	v_mfma_f32_16x16x32_f16 v[142:145], v[26:29], v[50:53], v[142:145]
	v_mfma_f32_16x16x32_f16 v[158:161], v[14:17], v[50:53], v[158:161]
	v_add_u32_e32 v2, 0xe1480, v150
	v_min_u32_e32 v2, v2, v154
	global_load_dwordx4 v[98:101], v2, s[8:9] nt
	s_waitcnt vmcnt(21)
	v_cvt_pk_f16_f32 v3, v64, v65
	v_cvt_pk_f16_f32 v2, v62, v63
	ds_write_b16 v234, v2 offset:6080
	ds_write_b16_d16_hi v235, v2 offset:6080
	ds_write_b16 v236, v3 offset:6080
	ds_write_b16_d16_hi v237, v3 offset:6080
	ds_read_b128 v[2:5], v151 offset:1408
	ds_read_b128 v[50:53], v151 offset:2016
	s_waitcnt lgkmcnt(1)
	v_mfma_f32_16x16x32_f16 v[222:225], v[26:29], v[2:5], v[114:117]
	v_mfma_f32_16x16x32_f16 v[178:181], v[14:17], v[2:5], v[178:181]
	s_waitcnt lgkmcnt(0)
	v_mfma_f32_16x16x32_f16 v[182:185], v[26:29], v[50:53], v[182:185]
	v_mfma_f32_16x16x32_f16 v[198:201], v[14:17], v[50:53], v[198:201]
	ds_read_b128 v[2:5], v151 offset:2624
	ds_read_b128 v[50:53], v151 offset:3232
	s_waitcnt lgkmcnt(1)
	v_mfma_f32_16x16x32_f16 v[134:137], v[26:29], v[2:5], v[134:137]
	v_mfma_f32_16x16x32_f16 v[146:149], v[14:17], v[2:5], v[146:149]
	s_waitcnt lgkmcnt(0)
	v_mfma_f32_16x16x32_f16 v[206:209], v[26:29], v[50:53], v[206:209]
	v_mfma_f32_16x16x32_f16 v[122:125], v[14:17], v[50:53], v[122:125]
	v_add_u32_e32 v2, 0xf7ac0, v244
	v_min_u32_e32 v2, v2, v154
	global_load_dwordx4 v[62:65], v2, s[8:9] nt
	s_waitcnt vmcnt(21)
	v_cvt_pk_f16_f32 v3, v68, v69
	v_cvt_pk_f16_f32 v2, v66, v67
	ds_write_b16 v238, v2 offset:6688
	ds_write_b16_d16_hi v239, v2 offset:6688
	ds_write_b16 v240, v3 offset:6688
	ds_write_b16_d16_hi v241, v3 offset:6688
	ds_read_b128 v[2:5], v151 offset:3840
	ds_read_b128 v[50:53], v151 offset:4448
	s_waitcnt lgkmcnt(1)
	v_mfma_f32_16x16x32_f16 v[210:213], v[26:29], v[2:5], v[210:213]
	v_mfma_f32_16x16x32_f16 v[190:193], v[14:17], v[2:5], v[190:193]
	s_waitcnt lgkmcnt(0)
	v_mfma_f32_16x16x32_f16 v[166:169], v[26:29], v[50:53], v[166:169]
	v_mfma_f32_16x16x32_f16 v[162:165], v[14:17], v[50:53], v[162:165]
	ds_read_b128 v[2:5], v151 offset:5056
	ds_read_b128 v[50:53], v151 offset:5664
	s_waitcnt lgkmcnt(1)
	v_mfma_f32_16x16x32_f16 v[218:221], v[26:29], v[2:5], v[218:221]
	v_mfma_f32_16x16x32_f16 v[138:141], v[14:17], v[2:5], v[138:141]
	s_waitcnt lgkmcnt(0)
	v_mfma_f32_16x16x32_f16 v[170:173], v[26:29], v[50:53], v[170:173]
	v_mfma_f32_16x16x32_f16 v[126:129], v[14:17], v[50:53], v[126:129]
	v_add_u32_e32 v2, 0x10e100, v150
	v_min_u32_e32 v2, v2, v154
	v_cndmask_b32_e64 v2, 0, v2, s[0:1]
	global_load_dwordx4 v[66:69], v2, s[8:9] nt
	s_waitcnt vmcnt(21)
	v_cvt_pk_f16_f32 v3, v108, v109
	v_cvt_pk_f16_f32 v2, v106, v107
	ds_write_b16 v234, v2 offset:7296
	ds_write_b16_d16_hi v235, v2 offset:7296
	ds_write_b16 v236, v3 offset:7296
	ds_write_b16_d16_hi v237, v3 offset:7296
	ds_read_b128 v[2:5], v151 offset:6272
	ds_read_b128 v[50:53], v151 offset:6880
	ds_read_b128 v[106:109], v151 offset:7488
	s_mov_b32 s3, 0xb0000
	s_waitcnt lgkmcnt(0)
	v_mfma_f32_16x16x32_f16 v[116:119], v[26:29], v[2:5], v[118:121]
	s_barrier
	v_sub_u32_e32 v245, v234, v243
	v_add_u32_e32 v246, 0xfffffdc0, v245
	v_min_u32_e32 v245, v245, v246
	v_add_u32_e32 v234, v242, v245
	v_sub_u32_e32 v245, v235, v243
	v_add_u32_e32 v246, 0xfffffdc0, v245
	v_min_u32_e32 v245, v245, v246
	v_add_u32_e32 v235, v242, v245
	v_sub_u32_e32 v245, v236, v243
	v_add_u32_e32 v246, 0xfffffdc0, v245
	v_min_u32_e32 v245, v245, v246
	v_add_u32_e32 v236, v242, v245
	v_sub_u32_e32 v245, v237, v243
	v_add_u32_e32 v246, 0xfffffdc0, v245
	v_min_u32_e32 v245, v245, v246
	v_add_u32_e32 v237, v242, v245
	v_sub_u32_e32 v245, v238, v243
	v_add_u32_e32 v246, 0xfffffdc0, v245
	v_min_u32_e32 v245, v245, v246
	v_add_u32_e32 v238, v242, v245
	v_sub_u32_e32 v245, v239, v243
	v_add_u32_e32 v246, 0xfffffdc0, v245
	v_min_u32_e32 v245, v245, v246
	v_add_u32_e32 v239, v242, v245
	v_sub_u32_e32 v245, v240, v243
	v_add_u32_e32 v246, 0xfffffdc0, v245
	v_min_u32_e32 v245, v245, v246
	v_add_u32_e32 v240, v242, v245
	v_sub_u32_e32 v245, v241, v243
	v_add_u32_e32 v246, 0xfffffdc0, v245
	v_min_u32_e32 v245, v245, v246
	v_add_u32_e32 v241, v242, v245
	v_mfma_f32_16x16x32_f16 v[174:177], v[14:17], v[2:5], v[174:177]
	v_add_co_u32_e32 v2, vcc, s3, v152
	s_nop 1
	v_addc_co_u32_e32 v3, vcc, 0, v153, vcc
	v_mfma_f32_16x16x32_f16 v[186:189], v[26:29], v[50:53], v[186:189]
	v_mfma_f32_16x16x32_f16 v[214:217], v[26:29], v[106:109], v[214:217]
	v_add_co_u32_e32 v26, vcc, s2, v152
	s_nop 1
	v_addc_co_u32_e32 v27, vcc, 0, v153, vcc
	v_mfma_f32_16x16x32_f16 v[194:197], v[14:17], v[50:53], v[194:197]
	global_load_dwordx4 v[50:53], v[2:3], off sc1
	global_load_dwordx4 v[54:57], v[2:3], off offset:256 sc1
	s_nop 0
	global_load_dwordx4 v[2:5], v[26:27], off sc1
	s_nop 0
	global_load_dwordx4 v[26:29], v[26:27], off offset:256 sc1
	v_mfma_f32_16x16x32_f16 v[14:17], v[14:17], v[106:109], v[102:105]
	v_mov_b32_e32 v114, 0
	s_nop 1
	ds_read_b128 v[102:105], v151 offset:256
	v_mov_b32_e32 v115, 0
	v_add_u32_e32 v106, 0x1800, v150
	s_waitcnt vmcnt(24) lgkmcnt(0)
	v_mfma_f32_16x16x32_f16 v[130:133], v[34:37], v[102:105], v[130:133]
	s_waitcnt vmcnt(23)
	v_mfma_f32_16x16x32_f16 v[202:205], v[46:49], v[102:105], v[202:205]
	v_min_u32_e32 v102, v106, v114
	global_load_dwordx4 v[102:105], v102, s[8:9] nt
	s_waitcnt vmcnt(21)
	v_cvt_pk_f16_f32 v107, v112, v113
	v_cvt_pk_f16_f32 v106, v110, v111
	ds_write_b16 v234, v106 offset:0
	ds_write_b16_d16_hi v235, v106 offset:0
	ds_write_b16 v236, v107 offset:0
	ds_write_b16_d16_hi v237, v107 offset:0
	ds_read_b128 v[106:109], v151 offset:864
	ds_read_b128 v[110:113], v151 offset:1472
	s_waitcnt lgkmcnt(1)
	v_mfma_f32_16x16x32_f16 v[142:145], v[34:37], v[106:109], v[142:145]
	v_mfma_f32_16x16x32_f16 v[158:161], v[46:49], v[106:109], v[158:161]
	s_waitcnt lgkmcnt(0)
	v_mfma_f32_16x16x32_f16 v[222:225], v[34:37], v[110:113], v[222:225]
	v_mfma_f32_16x16x32_f16 v[110:113], v[46:49], v[110:113], v[178:181]
	ds_read_b128 v[106:109], v151 offset:2080
	s_nop 1
	ds_read_b128 v[178:181], v151 offset:2688
	s_waitcnt lgkmcnt(1)
	v_mfma_f32_16x16x32_f16 v[182:185], v[34:37], v[106:109], v[182:185]
	v_mfma_f32_16x16x32_f16 v[198:201], v[46:49], v[106:109], v[198:201]
	s_waitcnt lgkmcnt(0)
	v_mfma_f32_16x16x32_f16 v[134:137], v[34:37], v[178:181], v[134:137]
	v_mfma_f32_16x16x32_f16 v[146:149], v[46:49], v[178:181], v[146:149]
	v_add_u32_e32 v106, 0x17e40, v244
	v_min_u32_e32 v106, v106, v114
	global_load_dwordx4 v[106:109], v106, s[8:9] nt
	s_waitcnt vmcnt(21)
	v_cvt_pk_f16_f32 v61, v60, v61
	v_cvt_pk_f16_f32 v60, v58, v59
	ds_write_b16 v238, v60 offset:608
	ds_write_b16_d16_hi v239, v60 offset:608
	ds_write_b16 v240, v61 offset:608
	ds_write_b16_d16_hi v241, v61 offset:608
	ds_read_b128 v[58:61], v151 offset:3296
	ds_read_b128 v[178:181], v151 offset:5120
	s_waitcnt lgkmcnt(1)
	v_mfma_f32_16x16x32_f16 v[206:209], v[34:37], v[58:61], v[206:209]
	v_mfma_f32_16x16x32_f16 v[120:123], v[46:49], v[58:61], v[122:125]
	ds_read_b128 v[58:61], v151 offset:3904
	ds_read_b128 v[226:229], v151 offset:4512
	s_waitcnt lgkmcnt(1)
	v_mfma_f32_16x16x32_f16 v[210:213], v[34:37], v[58:61], v[210:213]
	v_mfma_f32_16x16x32_f16 v[190:193], v[46:49], v[58:61], v[190:193]
	s_waitcnt lgkmcnt(0)
	v_mfma_f32_16x16x32_f16 v[166:169], v[34:37], v[226:229], v[166:169]
	v_mfma_f32_16x16x32_f16 v[162:165], v[46:49], v[226:229], v[162:165]
	v_mfma_f32_16x16x32_f16 v[218:221], v[34:37], v[178:181], v[218:221]
	v_mfma_f32_16x16x32_f16 v[138:141], v[46:49], v[178:181], v[138:141]
	v_add_u32_e32 v58, 0x2e480, v150
	v_min_u32_e32 v58, v58, v114
	global_load_dwordx4 v[58:61], v58, s[8:9] nt
	s_waitcnt vmcnt(21)
	v_cvt_pk_f16_f32 v73, v72, v73
	v_cvt_pk_f16_f32 v72, v70, v71
	ds_write_b16 v234, v72 offset:1216
	ds_write_b16_d16_hi v235, v72 offset:1216
	ds_write_b16 v236, v73 offset:1216
	ds_write_b16_d16_hi v237, v73 offset:1216
	ds_read_b128 v[70:73], v151 offset:5728
	ds_read_b128 v[178:181], v151 offset:6336
	s_waitcnt lgkmcnt(1)
	v_mfma_f32_16x16x32_f16 v[170:173], v[34:37], v[70:73], v[170:173]
	v_mfma_f32_16x16x32_f16 v[124:127], v[46:49], v[70:73], v[126:129]
	s_waitcnt lgkmcnt(0)
	v_mfma_f32_16x16x32_f16 v[116:119], v[34:37], v[178:181], v[116:119]
	v_mfma_f32_16x16x32_f16 v[174:177], v[46:49], v[178:181], v[174:177]
	ds_read_b128 v[70:73], v151 offset:6944
	ds_read_b128 v[178:181], v151 offset:7552
	s_waitcnt lgkmcnt(1)
	v_mfma_f32_16x16x32_f16 v[186:189], v[34:37], v[70:73], v[186:189]
	v_mfma_f32_16x16x32_f16 v[194:197], v[46:49], v[70:73], v[194:197]
	s_waitcnt lgkmcnt(0)
	v_mfma_f32_16x16x32_f16 v[214:217], v[34:37], v[178:181], v[214:217]
	v_mfma_f32_16x16x32_f16 v[178:181], v[46:49], v[178:181], v[14:17]
	s_nop 2
	v_add_u32_e32 v14, 0x44ac0, v244
	v_min_u32_e32 v14, v14, v114
	global_load_dwordx4 v[34:37], v14, s[8:9] nt
	s_waitcnt vmcnt(21)
	v_cvt_pk_f16_f32 v15, v44, v45
	v_cvt_pk_f16_f32 v14, v42, v43
	ds_write_b16 v238, v14 offset:1824
	ds_write_b16_d16_hi v239, v14 offset:1824
	ds_write_b16 v240, v15 offset:1824
	ds_write_b16_d16_hi v241, v15 offset:1824
	ds_read_b128 v[14:17], v151 offset:320
	ds_read_b128 v[42:45], v151 offset:928
	s_waitcnt lgkmcnt(1)
	v_mfma_f32_16x16x32_f16 v[128:131], v[10:13], v[14:17], v[130:133]
	v_mfma_f32_16x16x32_f16 v[202:205], v[6:9], v[14:17], v[202:205]
	s_waitcnt lgkmcnt(0)
	v_mfma_f32_16x16x32_f16 v[142:145], v[10:13], v[42:45], v[142:145]
	v_mfma_f32_16x16x32_f16 v[158:161], v[6:9], v[42:45], v[158:161]
	ds_read_b128 v[14:17], v151 offset:1536
	ds_read_b128 v[42:45], v151 offset:2144
	s_waitcnt lgkmcnt(1)
	v_mfma_f32_16x16x32_f16 v[222:225], v[10:13], v[14:17], v[222:225]
	v_mfma_f32_16x16x32_f16 v[110:113], v[6:9], v[14:17], v[110:113]
	s_waitcnt lgkmcnt(0)
	v_mfma_f32_16x16x32_f16 v[182:185], v[10:13], v[42:45], v[182:185]
	v_mfma_f32_16x16x32_f16 v[198:201], v[6:9], v[42:45], v[198:201]
	v_add_u32_e32 v14, 0x5b100, v150
	v_min_u32_e32 v14, v14, v114
	global_load_dwordx4 v[70:73], v14, s[8:9] nt
	s_waitcnt vmcnt(21)
	v_cvt_pk_f16_f32 v15, v76, v77
	v_cvt_pk_f16_f32 v14, v74, v75
	ds_write_b16 v234, v14 offset:2432
	ds_write_b16_d16_hi v235, v14 offset:2432
	ds_write_b16 v236, v15 offset:2432
	ds_write_b16_d16_hi v237, v15 offset:2432
	ds_read_b128 v[14:17], v151 offset:2752
	ds_read_b128 v[42:45], v151 offset:3360
	s_waitcnt lgkmcnt(1)
	v_mfma_f32_16x16x32_f16 v[132:135], v[10:13], v[14:17], v[134:137]
	v_mfma_f32_16x16x32_f16 v[146:149], v[6:9], v[14:17], v[146:149]
	s_waitcnt lgkmcnt(0)
	v_mfma_f32_16x16x32_f16 v[206:209], v[10:13], v[42:45], v[206:209]
	v_mfma_f32_16x16x32_f16 v[120:123], v[6:9], v[42:45], v[120:123]
	ds_read_b128 v[14:17], v151 offset:3968
	ds_read_b128 v[42:45], v151 offset:4576
	s_waitcnt lgkmcnt(1)
	v_mfma_f32_16x16x32_f16 v[210:213], v[10:13], v[14:17], v[210:213]
	v_mfma_f32_16x16x32_f16 v[190:193], v[6:9], v[14:17], v[190:193]
	s_waitcnt lgkmcnt(0)
	v_mfma_f32_16x16x32_f16 v[166:169], v[10:13], v[42:45], v[166:169]
	v_mfma_f32_16x16x32_f16 v[162:165], v[6:9], v[42:45], v[162:165]
	v_add_u32_e32 v14, 0x71740, v244
	v_min_u32_e32 v14, v14, v114
	global_load_dwordx4 v[74:77], v14, s[8:9] nt
	s_waitcnt vmcnt(21)
	v_cvt_pk_f16_f32 v15, v80, v81
	v_cvt_pk_f16_f32 v14, v78, v79
	ds_write_b16 v238, v14 offset:3040
	ds_write_b16_d16_hi v239, v14 offset:3040
	ds_write_b16 v240, v15 offset:3040
	ds_write_b16_d16_hi v241, v15 offset:3040
	ds_read_b128 v[14:17], v151 offset:5184
	ds_read_b128 v[42:45], v151 offset:5792
	s_waitcnt lgkmcnt(1)
	v_mfma_f32_16x16x32_f16 v[218:221], v[10:13], v[14:17], v[218:221]
	v_mfma_f32_16x16x32_f16 v[136:139], v[6:9], v[14:17], v[138:141]
	s_waitcnt lgkmcnt(0)
	v_mfma_f32_16x16x32_f16 v[170:173], v[10:13], v[42:45], v[170:173]
	v_mfma_f32_16x16x32_f16 v[124:127], v[6:9], v[42:45], v[124:127]
	ds_read_b128 v[14:17], v151 offset:6400
	ds_read_b128 v[42:45], v151 offset:7008
	s_waitcnt lgkmcnt(1)
	v_mfma_f32_16x16x32_f16 v[116:119], v[10:13], v[14:17], v[116:119]
	v_mfma_f32_16x16x32_f16 v[174:177], v[6:9], v[14:17], v[174:177]
	s_waitcnt lgkmcnt(0)
	v_mfma_f32_16x16x32_f16 v[186:189], v[10:13], v[42:45], v[186:189]
	v_mfma_f32_16x16x32_f16 v[194:197], v[6:9], v[42:45], v[194:197]
	v_add_u32_e32 v14, 0x87d80, v150
	v_min_u32_e32 v14, v14, v114
	global_load_dwordx4 v[78:81], v14, s[8:9] nt
	s_waitcnt vmcnt(21)
	v_cvt_pk_f16_f32 v15, v84, v85
	v_cvt_pk_f16_f32 v14, v82, v83
	ds_write_b16 v234, v14 offset:3648
	ds_write_b16_d16_hi v235, v14 offset:3648
	ds_write_b16 v236, v15 offset:3648
	ds_write_b16_d16_hi v237, v15 offset:3648
	ds_read_b128 v[82:85], v151 offset:7616
	s_mov_b32 s2, 0xb8000
	v_add_co_u32_e32 v14, vcc, s2, v152
	s_mov_b32 s2, 0xbc000
	s_nop 0
	v_addc_co_u32_e32 v15, vcc, 0, v153, vcc
	v_add_co_u32_e32 v42, vcc, s2, v152
	s_waitcnt lgkmcnt(0)
	v_mfma_f32_16x16x32_f16 v[214:217], v[10:13], v[82:85], v[214:217]
	v_addc_co_u32_e32 v43, vcc, 0, v153, vcc
	global_load_dwordx4 v[10:13], v[14:15], off sc1
	s_nop 0
	global_load_dwordx4 v[14:17], v[14:15], off offset:256 sc1
	s_nop 0
	global_load_dwordx4 v[46:49], v[42:43], off sc1
	s_nop 0
	global_load_dwordx4 v[42:45], v[42:43], off offset:256 sc1
	v_mfma_f32_16x16x32_f16 v[178:181], v[6:9], v[82:85], v[178:181]
	ds_read_b128 v[6:9], v151 offset:384
	ds_read_b128 v[82:85], v151 offset:992
	s_waitcnt vmcnt(24) lgkmcnt(1)
	v_mfma_f32_16x16x32_f16 v[128:131], v[30:33], v[6:9], v[128:131]
	s_waitcnt vmcnt(23)
	v_mfma_f32_16x16x32_f16 v[202:205], v[38:41], v[6:9], v[202:205]
	ds_read_b128 v[6:9], v151 offset:1600
	s_waitcnt lgkmcnt(1)
	v_mfma_f32_16x16x32_f16 v[140:143], v[30:33], v[82:85], v[142:145]
	v_mfma_f32_16x16x32_f16 v[158:161], v[38:41], v[82:85], v[158:161]
	s_waitcnt lgkmcnt(0)
	v_mfma_f32_16x16x32_f16 v[222:225], v[30:33], v[6:9], v[222:225]
	v_mfma_f32_16x16x32_f16 v[110:113], v[38:41], v[6:9], v[110:113]
	v_add_u32_e32 v6, 0x9e3c0, v244
	v_min_u32_e32 v6, v6, v114
	global_load_dwordx4 v[6:9], v6, s[8:9] nt
	s_waitcnt vmcnt(21)
	v_cvt_pk_f16_f32 v83, v88, v89
	v_cvt_pk_f16_f32 v82, v86, v87
	ds_write_b16 v238, v82 offset:4256
	ds_write_b16_d16_hi v239, v82 offset:4256
	ds_write_b16 v240, v83 offset:4256
	ds_write_b16_d16_hi v241, v83 offset:4256
	ds_read_b128 v[82:85], v151 offset:2208
	ds_read_b128 v[86:89], v151 offset:2816
	s_waitcnt lgkmcnt(1)
	v_mfma_f32_16x16x32_f16 v[182:185], v[30:33], v[82:85], v[182:185]
	v_mfma_f32_16x16x32_f16 v[198:201], v[38:41], v[82:85], v[198:201]
	s_waitcnt lgkmcnt(0)
	v_mfma_f32_16x16x32_f16 v[132:135], v[30:33], v[86:89], v[132:135]
	v_mfma_f32_16x16x32_f16 v[144:147], v[38:41], v[86:89], v[146:149]
	ds_read_b128 v[82:85], v151 offset:3424
	ds_read_b128 v[86:89], v151 offset:4032
	s_waitcnt lgkmcnt(1)
	v_mfma_f32_16x16x32_f16 v[206:209], v[30:33], v[82:85], v[206:209]
	v_mfma_f32_16x16x32_f16 v[120:123], v[38:41], v[82:85], v[120:123]
	s_waitcnt lgkmcnt(0)
	v_mfma_f32_16x16x32_f16 v[210:213], v[30:33], v[86:89], v[210:213]
	v_mfma_f32_16x16x32_f16 v[190:193], v[38:41], v[86:89], v[190:193]
	v_add_u32_e32 v82, 0xb4a00, v150
	v_min_u32_e32 v82, v82, v114
	global_load_dwordx4 v[82:85], v82, s[8:9] nt
	s_waitcnt vmcnt(21)
	v_cvt_pk_f16_f32 v87, v92, v93
	v_cvt_pk_f16_f32 v86, v90, v91
	ds_write_b16 v234, v86 offset:4864
	ds_write_b16_d16_hi v235, v86 offset:4864
	ds_write_b16 v236, v87 offset:4864
	ds_write_b16_d16_hi v237, v87 offset:4864
	ds_read_b128 v[86:89], v151 offset:4640
	ds_read_b128 v[90:93], v151 offset:6464
	s_waitcnt lgkmcnt(1)
	v_mfma_f32_16x16x32_f16 v[166:169], v[30:33], v[86:89], v[166:169]
	v_mfma_f32_16x16x32_f16 v[162:165], v[38:41], v[86:89], v[162:165]
	ds_read_b128 v[86:89], v151 offset:5248
	ds_read_b128 v[226:229], v151 offset:5856
	s_waitcnt lgkmcnt(1)
	v_mfma_f32_16x16x32_f16 v[218:221], v[30:33], v[86:89], v[218:221]
	v_mfma_f32_16x16x32_f16 v[136:139], v[38:41], v[86:89], v[136:139]
	s_waitcnt lgkmcnt(0)
	v_mfma_f32_16x16x32_f16 v[170:173], v[30:33], v[226:229], v[170:173]
	v_mfma_f32_16x16x32_f16 v[124:127], v[38:41], v[226:229], v[124:127]
	v_mfma_f32_16x16x32_f16 v[116:119], v[30:33], v[90:93], v[116:119]
	v_mfma_f32_16x16x32_f16 v[90:93], v[38:41], v[90:93], v[174:177]
	v_add_u32_e32 v86, 0xcb040, v244
	v_min_u32_e32 v86, v86, v114
	global_load_dwordx4 v[86:89], v86, s[8:9] nt
	s_waitcnt vmcnt(21)
	v_cvt_pk_f16_f32 v97, v96, v97
	v_cvt_pk_f16_f32 v96, v94, v95
	ds_write_b16 v238, v96 offset:5472
	ds_write_b16_d16_hi v239, v96 offset:5472
	ds_write_b16 v240, v97 offset:5472
	ds_write_b16_d16_hi v241, v97 offset:5472
	ds_read_b128 v[94:97], v151 offset:7072
	ds_read_b128 v[174:177], v151 offset:7680
	s_waitcnt lgkmcnt(1)
	v_mfma_f32_16x16x32_f16 v[186:189], v[30:33], v[94:97], v[186:189]
	v_mfma_f32_16x16x32_f16 v[94:97], v[38:41], v[94:97], v[194:197]
	s_waitcnt lgkmcnt(0)
	v_mfma_f32_16x16x32_f16 v[194:197], v[30:33], v[174:177], v[214:217]
	v_mfma_f32_16x16x32_f16 v[174:177], v[38:41], v[174:177], v[178:181]
	ds_read_b128 v[30:33], v151 offset:448
	ds_read_b128 v[38:41], v151 offset:1056
	s_waitcnt lgkmcnt(1)
	v_mfma_f32_16x16x32_f16 v[128:131], v[22:25], v[30:33], v[128:131]
	v_mfma_f32_16x16x32_f16 v[178:181], v[18:21], v[30:33], v[202:205]
	s_waitcnt lgkmcnt(0)
	v_mfma_f32_16x16x32_f16 v[140:143], v[22:25], v[38:41], v[140:143]
	v_mfma_f32_16x16x32_f16 v[158:161], v[18:21], v[38:41], v[158:161]
	v_add_u32_e32 v30, 0xe1680, v150
	v_min_u32_e32 v30, v30, v114
	global_load_dwordx4 v[30:33], v30, s[8:9] nt
	s_waitcnt vmcnt(21)
	v_cvt_pk_f16_f32 v39, v100, v101
	v_cvt_pk_f16_f32 v38, v98, v99
	ds_write_b16 v234, v38 offset:6080
	ds_write_b16_d16_hi v235, v38 offset:6080
	ds_write_b16 v236, v39 offset:6080
	ds_write_b16_d16_hi v237, v39 offset:6080
	ds_read_b128 v[38:41], v151 offset:1664
	ds_read_b128 v[98:101], v151 offset:2272
	s_waitcnt lgkmcnt(1)
	v_mfma_f32_16x16x32_f16 v[202:205], v[22:25], v[38:41], v[222:225]
	v_mfma_f32_16x16x32_f16 v[214:217], v[18:21], v[38:41], v[110:113]
	ds_read_b128 v[38:41], v151 offset:2880
	s_nop 1
	ds_read_b128 v[110:113], v151 offset:3488
	s_waitcnt lgkmcnt(2)
	v_mfma_f32_16x16x32_f16 v[182:185], v[22:25], v[98:101], v[182:185]
	v_mfma_f32_16x16x32_f16 v[98:101], v[18:21], v[98:101], v[198:201]
	s_waitcnt lgkmcnt(1)
	v_mfma_f32_16x16x32_f16 v[132:135], v[22:25], v[38:41], v[132:135]
	v_mfma_f32_16x16x32_f16 v[144:147], v[18:21], v[38:41], v[144:147]
	s_waitcnt lgkmcnt(0)
	v_mfma_f32_16x16x32_f16 v[198:201], v[22:25], v[110:113], v[206:209]
	v_mfma_f32_16x16x32_f16 v[120:123], v[18:21], v[110:113], v[120:123]
	v_add_u32_e32 v38, 0xf7cc0, v244
	v_min_u32_e32 v38, v38, v114
	global_load_dwordx4 v[38:41], v38, s[8:9] nt
	s_waitcnt vmcnt(21)
	v_cvt_pk_f16_f32 v65, v64, v65
	v_cvt_pk_f16_f32 v64, v62, v63
	ds_write_b16 v238, v64 offset:6688
	ds_write_b16_d16_hi v239, v64 offset:6688
	ds_write_b16 v240, v65 offset:6688
	ds_write_b16_d16_hi v241, v65 offset:6688
	ds_read_b128 v[62:65], v151 offset:4096
	ds_read_b128 v[110:113], v151 offset:4704
	s_waitcnt lgkmcnt(1)
	v_mfma_f32_16x16x32_f16 v[206:209], v[22:25], v[62:65], v[210:213]
	v_mfma_f32_16x16x32_f16 v[62:65], v[18:21], v[62:65], v[190:193]
	s_waitcnt lgkmcnt(0)
	v_mfma_f32_16x16x32_f16 v[166:169], v[22:25], v[110:113], v[166:169]
	v_mfma_f32_16x16x32_f16 v[162:165], v[18:21], v[110:113], v[162:165]
	ds_read_b128 v[110:113], v151 offset:5312
	ds_read_b128 v[190:193], v151 offset:5920
	s_waitcnt lgkmcnt(1)
	v_mfma_f32_16x16x32_f16 v[210:213], v[22:25], v[110:113], v[218:221]
	v_mfma_f32_16x16x32_f16 v[136:139], v[18:21], v[110:113], v[136:139]
	s_waitcnt lgkmcnt(0)
	v_mfma_f32_16x16x32_f16 v[170:173], v[22:25], v[190:193], v[170:173]
	v_mfma_f32_16x16x32_f16 v[124:127], v[18:21], v[190:193], v[124:127]
	v_add_u32_e32 v110, 0x10e300, v150
	v_min_u32_e32 v110, v110, v114
	v_cndmask_b32_e64 v110, 0, v110, s[0:1]
	global_load_dwordx4 v[110:113], v110, s[8:9] nt
	s_waitcnt vmcnt(21)
	v_cvt_pk_f16_f32 v69, v68, v69
	v_cvt_pk_f16_f32 v68, v66, v67
	ds_write_b16 v234, v68 offset:7296
	ds_write_b16_d16_hi v235, v68 offset:7296
	ds_write_b16 v236, v69 offset:7296
	ds_write_b16_d16_hi v237, v69 offset:7296
	ds_read_b128 v[66:69], v151 offset:6528
	ds_read_b128 v[152:155], v151 offset:7136
	s_waitcnt lgkmcnt(1)
	v_mfma_f32_16x16x32_f16 v[116:119], v[22:25], v[66:69], v[116:119]
	v_mfma_f32_16x16x32_f16 v[66:69], v[18:21], v[66:69], v[90:93]
	s_waitcnt lgkmcnt(0)
	v_mfma_f32_16x16x32_f16 v[90:93], v[22:25], v[152:155], v[186:189]
	v_mfma_f32_16x16x32_f16 v[94:97], v[18:21], v[152:155], v[94:97]
	ds_read_b128 v[152:155], v151 offset:7744
	s_waitcnt lgkmcnt(0)
	s_barrier
	v_sub_u32_e32 v245, v234, v243
	v_add_u32_e32 v246, 0xfffffdc0, v245
	v_min_u32_e32 v245, v245, v246
	v_add_u32_e32 v234, v242, v245
	v_sub_u32_e32 v245, v235, v243
	v_add_u32_e32 v246, 0xfffffdc0, v245
	v_min_u32_e32 v245, v245, v246
	v_add_u32_e32 v235, v242, v245
	v_sub_u32_e32 v245, v236, v243
	v_add_u32_e32 v246, 0xfffffdc0, v245
	v_min_u32_e32 v245, v245, v246
	v_add_u32_e32 v236, v242, v245
	v_sub_u32_e32 v245, v237, v243
	v_add_u32_e32 v246, 0xfffffdc0, v245
	v_min_u32_e32 v245, v245, v246
	v_add_u32_e32 v237, v242, v245
	v_sub_u32_e32 v245, v238, v243
	v_add_u32_e32 v246, 0xfffffdc0, v245
	v_min_u32_e32 v245, v245, v246
	v_add_u32_e32 v238, v242, v245
	v_sub_u32_e32 v245, v239, v243
	v_add_u32_e32 v246, 0xfffffdc0, v245
	v_min_u32_e32 v245, v245, v246
	v_add_u32_e32 v239, v242, v245
	v_sub_u32_e32 v245, v240, v243
	v_add_u32_e32 v246, 0xfffffdc0, v245
	v_min_u32_e32 v245, v245, v246
	v_add_u32_e32 v240, v242, v245
	v_sub_u32_e32 v245, v241, v243
	v_add_u32_e32 v246, 0xfffffdc0, v245
	v_min_u32_e32 v245, v245, v246
	v_add_u32_e32 v241, v242, v245
	v_mfma_f32_16x16x32_f16 v[22:25], v[22:25], v[152:155], v[194:197]
	v_mfma_f32_16x16x32_f16 v[18:21], v[18:21], v[152:155], v[174:177]
	v_mov_b32_e32 v114, 0
	ds_read_b128 v[152:155], v151 offset:512
	s_waitcnt vmcnt(20) lgkmcnt(0)
	v_mfma_f32_16x16x32_f16 v[128:131], v[50:53], v[152:155], v[128:131]
	s_waitcnt vmcnt(19)
	v_mfma_f32_16x16x32_f16 v[152:155], v[54:57], v[152:155], v[178:181]
	s_waitcnt vmcnt(16)
	v_cvt_pk_f16_f32 v105, v104, v105
	v_cvt_pk_f16_f32 v104, v102, v103
	ds_write_b16 v234, v104 offset:0
	ds_write_b16_d16_hi v235, v104 offset:0
	ds_write_b16 v236, v105 offset:0
	ds_write_b16_d16_hi v237, v105 offset:0
	ds_read_b128 v[102:105], v151 offset:1120
	ds_read_b128 v[174:177], v151 offset:1728
	ds_read_b128 v[178:181], v151 offset:2336
	ds_read_b128 v[186:189], v151 offset:2944
	s_waitcnt lgkmcnt(3)
	v_mfma_f32_16x16x32_f16 v[140:143], v[50:53], v[102:105], v[140:143]
	v_mfma_f32_16x16x32_f16 v[102:105], v[54:57], v[102:105], v[158:161]
	s_waitcnt lgkmcnt(2)
	v_mfma_f32_16x16x32_f16 v[158:161], v[50:53], v[174:177], v[202:205]
	v_mfma_f32_16x16x32_f16 v[174:177], v[54:57], v[174:177], v[214:217]
	s_waitcnt lgkmcnt(1)
	v_mfma_f32_16x16x32_f16 v[182:185], v[50:53], v[178:181], v[182:185]
	v_mfma_f32_16x16x32_f16 v[98:101], v[54:57], v[178:181], v[98:101]
	s_waitcnt lgkmcnt(0)
	v_mfma_f32_16x16x32_f16 v[132:135], v[50:53], v[186:189], v[132:135]
	v_mfma_f32_16x16x32_f16 v[144:147], v[54:57], v[186:189], v[144:147]
	s_waitcnt vmcnt(15)
	v_cvt_pk_f16_f32 v109, v108, v109
	v_cvt_pk_f16_f32 v108, v106, v107
	ds_write_b16 v238, v108 offset:608
	ds_write_b16_d16_hi v239, v108 offset:608
	ds_write_b16 v240, v109 offset:608
	ds_write_b16_d16_hi v241, v109 offset:608
	ds_read_b128 v[106:109], v151 offset:3552
	ds_read_b128 v[178:181], v151 offset:5376
	s_waitcnt lgkmcnt(1)
	v_mfma_f32_16x16x32_f16 v[186:189], v[50:53], v[106:109], v[198:201]
	v_mfma_f32_16x16x32_f16 v[106:109], v[54:57], v[106:109], v[120:123]
	s_nop 2
	ds_read_b128 v[120:123], v151 offset:4160
	ds_read_b128 v[190:193], v151 offset:4768
	s_waitcnt lgkmcnt(1)
	v_mfma_f32_16x16x32_f16 v[194:197], v[50:53], v[120:123], v[206:209]
	v_mfma_f32_16x16x32_f16 v[62:65], v[54:57], v[120:123], v[62:65]
	s_waitcnt lgkmcnt(0)
	v_mfma_f32_16x16x32_f16 v[120:123], v[50:53], v[190:193], v[166:169]
	v_mfma_f32_16x16x32_f16 v[162:165], v[54:57], v[190:193], v[162:165]
	v_mfma_f32_16x16x32_f16 v[166:169], v[50:53], v[178:181], v[210:213]
	v_mfma_f32_16x16x32_f16 v[136:139], v[54:57], v[178:181], v[136:139]
	s_waitcnt vmcnt(14)
	v_cvt_pk_f16_f32 v61, v60, v61
	v_cvt_pk_f16_f32 v60, v58, v59
	ds_write_b16 v234, v60 offset:1216
	ds_write_b16_d16_hi v235, v60 offset:1216
	ds_write_b16 v236, v61 offset:1216
	ds_write_b16_d16_hi v237, v61 offset:1216
	ds_read_b128 v[58:61], v151 offset:5984
	ds_read_b128 v[178:181], v151 offset:6592
	s_waitcnt lgkmcnt(1)
	v_mfma_f32_16x16x32_f16 v[170:173], v[50:53], v[58:61], v[170:173]
	v_mfma_f32_16x16x32_f16 v[58:61], v[54:57], v[58:61], v[124:127]
	s_waitcnt lgkmcnt(0)
	v_mfma_f32_16x16x32_f16 v[116:119], v[50:53], v[178:181], v[116:119]
	v_mfma_f32_16x16x32_f16 v[66:69], v[54:57], v[178:181], v[66:69]
	ds_read_b128 v[124:127], v151 offset:7200
	ds_read_b128 v[178:181], v151 offset:7808
	s_waitcnt lgkmcnt(1)
	v_mfma_f32_16x16x32_f16 v[90:93], v[50:53], v[124:127], v[90:93]
	v_mfma_f32_16x16x32_f16 v[94:97], v[54:57], v[124:127], v[94:97]
	s_waitcnt lgkmcnt(0)
	v_mfma_f32_16x16x32_f16 v[22:25], v[50:53], v[178:181], v[22:25]
	v_mfma_f32_16x16x32_f16 v[18:21], v[54:57], v[178:181], v[18:21]
	s_waitcnt vmcnt(13)
	v_cvt_pk_f16_f32 v37, v36, v37
	v_cvt_pk_f16_f32 v36, v34, v35
	ds_write_b16 v238, v36 offset:1824
	ds_write_b16_d16_hi v239, v36 offset:1824
	ds_write_b16 v240, v37 offset:1824
	ds_write_b16_d16_hi v241, v37 offset:1824
	ds_read_b128 v[34:37], v151 offset:0
	ds_read_b128 v[50:53], v151 offset:608
	s_waitcnt lgkmcnt(1)
	v_mfma_f32_16x16x32_f16 v[54:57], v[2:5], v[34:37], v[128:131]
	s_waitcnt lgkmcnt(0)
	v_mfma_f32_16x16x32_f16 v[124:127], v[2:5], v[50:53], v[140:143]
	v_mfma_f32_16x16x32_f16 v[50:53], v[26:29], v[50:53], v[102:105]
	s_nop 2
	ds_read_b128 v[102:105], v151 offset:1216
	ds_read_b128 v[128:131], v151 offset:1824
	v_mfma_f32_16x16x32_f16 v[34:37], v[26:29], v[34:37], v[152:155]
	s_waitcnt lgkmcnt(1)
	v_mfma_f32_16x16x32_f16 v[140:143], v[2:5], v[102:105], v[158:161]
	v_mfma_f32_16x16x32_f16 v[102:105], v[26:29], v[102:105], v[174:177]
	s_waitcnt lgkmcnt(0)
	v_mfma_f32_16x16x32_f16 v[152:155], v[2:5], v[128:131], v[182:185]
	v_mfma_f32_16x16x32_f16 v[98:101], v[26:29], v[128:131], v[98:101]
	s_waitcnt vmcnt(12)
	v_cvt_pk_f16_f32 v73, v72, v73
	v_cvt_pk_f16_f32 v72, v70, v71
	ds_write_b16 v234, v72 offset:2432
	ds_write_b16_d16_hi v235, v72 offset:2432
	ds_write_b16 v236, v73 offset:2432
	ds_write_b16_d16_hi v237, v73 offset:2432
	ds_read_b128 v[70:73], v151 offset:2432
	ds_read_b128 v[128:131], v151 offset:3040
	s_waitcnt lgkmcnt(1)
	v_mfma_f32_16x16x32_f16 v[132:135], v[2:5], v[70:73], v[132:135]
	v_mfma_f32_16x16x32_f16 v[70:73], v[26:29], v[70:73], v[144:147]
	s_waitcnt lgkmcnt(0)
	v_mfma_f32_16x16x32_f16 v[144:147], v[2:5], v[128:131], v[186:189]
	v_mfma_f32_16x16x32_f16 v[106:109], v[26:29], v[128:131], v[106:109]
	ds_read_b128 v[128:131], v151 offset:3648
	ds_read_b128 v[158:161], v151 offset:4256
	s_waitcnt lgkmcnt(1)
	v_mfma_f32_16x16x32_f16 v[174:177], v[2:5], v[128:131], v[194:197]
	v_mfma_f32_16x16x32_f16 v[62:65], v[26:29], v[128:131], v[62:65]
	s_waitcnt lgkmcnt(0)
	v_mfma_f32_16x16x32_f16 v[120:123], v[2:5], v[158:161], v[120:123]
	v_mfma_f32_16x16x32_f16 v[128:131], v[26:29], v[158:161], v[162:165]
	s_waitcnt vmcnt(11)
	v_cvt_pk_f16_f32 v77, v76, v77
	v_cvt_pk_f16_f32 v76, v74, v75
	ds_write_b16 v238, v76 offset:3040
	ds_write_b16_d16_hi v239, v76 offset:3040
	ds_write_b16 v240, v77 offset:3040
	ds_write_b16_d16_hi v241, v77 offset:3040
	ds_read_b128 v[74:77], v151 offset:4864
	ds_read_b128 v[158:161], v151 offset:5472
	s_waitcnt lgkmcnt(1)
	v_mfma_f32_16x16x32_f16 v[162:165], v[2:5], v[74:77], v[166:169]
	v_mfma_f32_16x16x32_f16 v[74:77], v[26:29], v[74:77], v[136:139]
	s_waitcnt lgkmcnt(0)
	v_mfma_f32_16x16x32_f16 v[136:139], v[2:5], v[158:161], v[170:173]
	v_mfma_f32_16x16x32_f16 v[58:61], v[26:29], v[158:161], v[58:61]
	ds_read_b128 v[158:161], v151 offset:6080
	ds_read_b128 v[166:169], v151 offset:6688
	s_waitcnt lgkmcnt(1)
	v_mfma_f32_16x16x32_f16 v[116:119], v[2:5], v[158:161], v[116:119]
	v_mfma_f32_16x16x32_f16 v[66:69], v[26:29], v[158:161], v[66:69]
	s_waitcnt lgkmcnt(0)
	v_mfma_f32_16x16x32_f16 v[90:93], v[2:5], v[166:169], v[90:93]
	v_mfma_f32_16x16x32_f16 v[94:97], v[26:29], v[166:169], v[94:97]
	s_waitcnt vmcnt(10)
	v_cvt_pk_f16_f32 v81, v80, v81
	v_cvt_pk_f16_f32 v80, v78, v79
	ds_write_b16 v234, v80 offset:3648
	ds_write_b16_d16_hi v235, v80 offset:3648
	ds_write_b16 v236, v81 offset:3648
	ds_write_b16_d16_hi v237, v81 offset:3648
	ds_read_b128 v[78:81], v151 offset:7296
	s_waitcnt lgkmcnt(0)
	v_mfma_f32_16x16x32_f16 v[2:5], v[2:5], v[78:81], v[22:25]
	v_mfma_f32_16x16x32_f16 v[18:21], v[26:29], v[78:81], v[18:21]
	s_nop 1
	ds_read_b128 v[22:25], v151 offset:64
	ds_read_b128 v[26:29], v151 offset:672
	s_waitcnt vmcnt(9) lgkmcnt(1)
	v_mfma_f32_16x16x32_f16 v[54:57], v[10:13], v[22:25], v[54:57]
	s_waitcnt vmcnt(8)
	v_mfma_f32_16x16x32_f16 v[22:25], v[14:17], v[22:25], v[34:37]
	s_waitcnt lgkmcnt(0)
	v_mfma_f32_16x16x32_f16 v[34:37], v[10:13], v[26:29], v[124:127]
	v_mfma_f32_16x16x32_f16 v[26:29], v[14:17], v[26:29], v[50:53]
	s_nop 2
	ds_read_b128 v[50:53], v151 offset:1280
	s_waitcnt lgkmcnt(0)
	v_mfma_f32_16x16x32_f16 v[78:81], v[10:13], v[50:53], v[140:143]
	v_mfma_f32_16x16x32_f16 v[50:53], v[14:17], v[50:53], v[102:105]
	s_waitcnt vmcnt(5)
	v_cvt_pk_f16_f32 v9, v8, v9
	v_cvt_pk_f16_f32 v8, v6, v7
	ds_write_b16 v238, v8 offset:4256
	ds_write_b16_d16_hi v239, v8 offset:4256
	ds_write_b16 v240, v9 offset:4256
	ds_write_b16_d16_hi v241, v9 offset:4256
	ds_read_b128 v[6:9], v151 offset:1888
	ds_read_b128 v[102:105], v151 offset:2496
	s_waitcnt lgkmcnt(1)
	v_mfma_f32_16x16x32_f16 v[124:127], v[10:13], v[6:9], v[152:155]
	v_mfma_f32_16x16x32_f16 v[6:9], v[14:17], v[6:9], v[98:101]
	s_waitcnt lgkmcnt(0)
	v_mfma_f32_16x16x32_f16 v[132:135], v[10:13], v[102:105], v[132:135]
	v_mfma_f32_16x16x32_f16 v[70:73], v[14:17], v[102:105], v[70:73]
	ds_read_b128 v[98:101], v151 offset:3104
	ds_read_b128 v[102:105], v151 offset:3712
	s_waitcnt lgkmcnt(1)
	v_mfma_f32_16x16x32_f16 v[140:143], v[10:13], v[98:101], v[144:147]
	v_mfma_f32_16x16x32_f16 v[144:147], v[14:17], v[98:101], v[106:109]
	s_waitcnt lgkmcnt(0)
	v_mfma_f32_16x16x32_f16 v[152:155], v[10:13], v[102:105], v[174:177]
	v_mfma_f32_16x16x32_f16 v[158:161], v[14:17], v[102:105], v[62:65]
	s_waitcnt vmcnt(4)
	s_nop 1
	v_cvt_pk_f16_f32 v63, v84, v85
	v_cvt_pk_f16_f32 v62, v82, v83
	ds_write_b16 v234, v62 offset:4864
	ds_write_b16_d16_hi v235, v62 offset:4864
	ds_write_b16 v236, v63 offset:4864
	ds_write_b16_d16_hi v237, v63 offset:4864
	ds_read_b128 v[62:65], v151 offset:4320
	ds_read_b128 v[82:85], v151 offset:6144
	s_waitcnt lgkmcnt(1)
	v_mfma_f32_16x16x32_f16 v[120:123], v[10:13], v[62:65], v[120:123]
	v_mfma_f32_16x16x32_f16 v[128:131], v[14:17], v[62:65], v[128:131]
	ds_read_b128 v[62:65], v151 offset:4928
	ds_read_b128 v[98:101], v151 offset:5536
	s_waitcnt lgkmcnt(1)
	v_mfma_f32_16x16x32_f16 v[162:165], v[10:13], v[62:65], v[162:165]
	v_mfma_f32_16x16x32_f16 v[166:169], v[14:17], v[62:65], v[74:77]
	s_waitcnt lgkmcnt(0)
	v_mfma_f32_16x16x32_f16 v[136:139], v[10:13], v[98:101], v[136:139]
	v_mfma_f32_16x16x32_f16 v[170:173], v[14:17], v[98:101], v[58:61]
	v_mfma_f32_16x16x32_f16 v[116:119], v[10:13], v[82:85], v[116:119]
	v_mfma_f32_16x16x32_f16 v[174:177], v[14:17], v[82:85], v[66:69]
	s_waitcnt vmcnt(3)
	v_cvt_pk_f16_f32 v59, v88, v89
	v_cvt_pk_f16_f32 v58, v86, v87
	ds_write_b16 v238, v58 offset:5472
	ds_write_b16_d16_hi v239, v58 offset:5472
	ds_write_b16 v240, v59 offset:5472
	ds_write_b16_d16_hi v241, v59 offset:5472
	ds_read_b128 v[58:61], v151 offset:6752
	ds_read_b128 v[62:65], v151 offset:7360
	s_waitcnt lgkmcnt(1)
	v_mfma_f32_16x16x32_f16 v[178:181], v[10:13], v[58:61], v[90:93]
	v_mfma_f32_16x16x32_f16 v[182:185], v[14:17], v[58:61], v[94:97]
	s_waitcnt lgkmcnt(0)
	v_mfma_f32_16x16x32_f16 v[2:5], v[10:13], v[62:65], v[2:5]
	v_mfma_f32_16x16x32_f16 v[186:189], v[14:17], v[62:65], v[18:21]
	ds_read_b128 v[10:13], v151 offset:128
	ds_read_b128 v[14:17], v151 offset:736
	s_waitcnt lgkmcnt(1)
	v_mfma_f32_16x16x32_f16 v[148:151], v[46:49], v[10:13], v[54:57]
	v_mfma_f32_16x16x32_f16 v[106:109], v[42:45], v[10:13], v[22:25]
	s_waitcnt lgkmcnt(0)
	v_mfma_f32_16x16x32_f16 v[102:105], v[46:49], v[14:17], v[34:37]
	v_mfma_f32_16x16x32_f16 v[94:97], v[42:45], v[14:17], v[26:29]
	s_waitcnt vmcnt(2)
	v_cvt_pk_f16_f32 v11, v32, v33
	v_cvt_pk_f16_f32 v10, v30, v31
	ds_write_b16 v234, v10 offset:6080
	ds_write_b16_d16_hi v235, v10 offset:6080
	ds_write_b16 v236, v11 offset:6080
	ds_write_b16_d16_hi v237, v11 offset:6080
	ds_read_b128 v[10:13], v151 offset:1344
	ds_read_b128 v[14:17], v151 offset:1952
	s_waitcnt lgkmcnt(1)
	v_mfma_f32_16x16x32_f16 v[98:101], v[46:49], v[10:13], v[78:81]
	v_mfma_f32_16x16x32_f16 v[90:93], v[42:45], v[10:13], v[50:53]
	s_waitcnt lgkmcnt(0)
	v_mfma_f32_16x16x32_f16 v[82:85], v[42:45], v[14:17], v[6:9]
	s_nop 2
	ds_read_b128 v[6:9], v151 offset:2560
	ds_read_b128 v[10:13], v151 offset:3168
	v_mfma_f32_16x16x32_f16 v[86:89], v[46:49], v[14:17], v[124:127]
	s_waitcnt lgkmcnt(1)
	v_mfma_f32_16x16x32_f16 v[78:81], v[46:49], v[6:9], v[132:135]
	v_mfma_f32_16x16x32_f16 v[74:77], v[42:45], v[6:9], v[70:73]
	s_waitcnt lgkmcnt(0)
	v_mfma_f32_16x16x32_f16 v[70:73], v[46:49], v[10:13], v[140:143]
	v_mfma_f32_16x16x32_f16 v[62:65], v[42:45], v[10:13], v[144:147]
	s_waitcnt vmcnt(1)
	v_cvt_pk_f16_f32 v7, v40, v41
	v_cvt_pk_f16_f32 v6, v38, v39
	ds_write_b16 v238, v6 offset:6688
	ds_write_b16_d16_hi v239, v6 offset:6688
	ds_write_b16 v240, v7 offset:6688
	ds_write_b16_d16_hi v241, v7 offset:6688
	ds_read_b128 v[6:9], v151 offset:3776
	ds_read_b128 v[10:13], v151 offset:4384
	s_waitcnt lgkmcnt(1)
	v_mfma_f32_16x16x32_f16 v[66:69], v[46:49], v[6:9], v[152:155]
	v_mfma_f32_16x16x32_f16 v[58:61], v[42:45], v[6:9], v[158:161]
	s_waitcnt lgkmcnt(0)
	v_mfma_f32_16x16x32_f16 v[54:57], v[46:49], v[10:13], v[120:123]
	v_mfma_f32_16x16x32_f16 v[50:53], v[42:45], v[10:13], v[128:131]
	ds_read_b128 v[6:9], v151 offset:4992
	ds_read_b128 v[10:13], v151 offset:5600
	s_waitcnt lgkmcnt(1)
	v_mfma_f32_16x16x32_f16 v[38:41], v[46:49], v[6:9], v[162:165]
	v_mfma_f32_16x16x32_f16 v[34:37], v[42:45], v[6:9], v[166:169]
	s_waitcnt lgkmcnt(0)
	v_mfma_f32_16x16x32_f16 v[30:33], v[46:49], v[10:13], v[136:139]
	v_mfma_f32_16x16x32_f16 v[18:21], v[42:45], v[10:13], v[170:173]
	s_waitcnt vmcnt(0)
	v_cvt_pk_f16_f32 v7, v112, v113
	v_cvt_pk_f16_f32 v6, v110, v111
	ds_write_b16 v234, v6 offset:7296
	ds_write_b16_d16_hi v235, v6 offset:7296
	ds_write_b16 v236, v7 offset:7296
	ds_write_b16_d16_hi v237, v7 offset:7296
	ds_read_b128 v[6:9], v151 offset:6208
	ds_read_b128 v[10:13], v151 offset:6816
	ds_read_b128 v[110:113], v151 offset:7424
	s_waitcnt lgkmcnt(0)
	s_barrier
	v_mfma_f32_16x16x32_f16 v[22:25], v[46:49], v[6:9], v[116:119]
	s_barrier
	v_mfma_f32_16x16x32_f16 v[26:29], v[42:45], v[6:9], v[174:177]
	s_movk_i32 s0, 0xffe0
	v_lshrrev_b32_e32 v6, 2, v0
	v_and_b32_e32 v1, 15, v0
	v_ashrrev_i32_e32 v114, 1, v0
	v_and_b32_e32 v116, 12, v6
	v_mfma_f32_16x16x32_f16 v[14:17], v[46:49], v[10:13], v[178:181]
	v_and_or_b32 v120, v114, s0, v116
	v_lshlrev_b32_e32 v114, 3, v1
	v_lshlrev_b32_e32 v129, 1, v120
	v_mfma_f32_16x16x32_f16 v[6:9], v[46:49], v[110:113], v[2:5]
	v_mov_b32_e32 v46, 0x1f480
	v_lshl_add_u32 v128, v120, 2, v46
	v_or_b32_e32 v46, 0x1ee00, v114
	v_or_b32_e32 v47, 0x1ee80, v114
	v_or_b32_e32 v48, 0x1ef00, v114
	v_or_b32_e32 v49, 0x1ef80, v114
	v_mfma_f32_16x16x32_f16 v[10:13], v[42:45], v[10:13], v[182:185]
	s_movk_i32 s4, 0x210
	s_movk_i32 s0, 0x1880
	v_cmp_gt_i32_e32 vcc, s0, v0
	v_mfma_f32_16x16x32_f16 v[2:5], v[42:45], v[110:113], v[186:189]
	ds_read_b128 v[42:45], v128
	ds_read_b64 v[124:125], v46
	ds_read_b64 v[126:127], v47
	ds_read_b64 v[118:119], v48
	ds_read_b64 v[116:117], v49
	ds_read_b128 v[46:49], v128
	ds_read_b128 v[120:123], v128 offset:64
	s_waitcnt lgkmcnt(4)
	v_pk_fma_f32 v[104:105], v[126:127], v[44:45], v[104:105] op_sel_hi:[0,1,1]
	v_pk_fma_f32 v[102:103], v[126:127], v[42:43], v[102:103] op_sel_hi:[0,1,1]
	s_waitcnt lgkmcnt(0)
	v_pk_fma_f32 v[108:109], v[124:125], v[122:123], v[108:109] op_sel_hi:[0,1,1]
	v_pk_fma_f32 v[106:107], v[124:125], v[120:121], v[106:107] op_sel_hi:[0,1,1]
	v_pk_mul_f32 v[108:109], v[124:125], v[108:109] op_sel:[1,0]
	v_pk_mul_f32 v[106:107], v[124:125], v[106:107] op_sel:[1,0]
	v_cvt_pk_f16_f32 v109, v108, v109
	v_cvt_pk_f16_f32 v108, v106, v107
	v_or_b32_e32 v106, 32, v129
	v_mad_u32_u24 v107, v1, s4, v106
	ds_write_b64 v107, v[108:109]
	v_mov_b32_e32 v107, 0x2100
	v_pk_fma_f32 v[96:97], v[126:127], v[122:123], v[96:97] op_sel_hi:[0,1,1]
	v_pk_fma_f32 v[94:95], v[126:127], v[120:121], v[94:95] op_sel_hi:[0,1,1]
	v_mad_u32_u24 v107, v1, s4, v107
	v_pk_mul_f32 v[96:97], v[126:127], v[96:97] op_sel:[1,0]
	v_pk_mul_f32 v[94:95], v[126:127], v[94:95] op_sel:[1,0]
	v_pk_mul_f32 v[104:105], v[126:127], v[104:105] op_sel:[1,0]
	v_pk_mul_f32 v[102:103], v[126:127], v[102:103] op_sel:[1,0]
	v_cvt_pk_f16_f32 v97, v96, v97
	v_cvt_pk_f16_f32 v96, v94, v95
	v_add_u32_e32 v94, v107, v106
	v_cvt_pk_f16_f32 v105, v104, v105
	v_cvt_pk_f16_f32 v104, v102, v103
	v_add_u32_e32 v102, v107, v129
	ds_write_b64 v94, v[96:97]
	v_mov_b32_e32 v94, 0x4200
	v_pk_fma_f32 v[92:93], v[118:119], v[122:123], v[92:93] op_sel_hi:[0,1,1]
	v_pk_fma_f32 v[90:91], v[118:119], v[120:121], v[90:91] op_sel_hi:[0,1,1]
	ds_write_b64 v102, v[104:105]
	v_mad_u32_u24 v102, v1, s4, v94
	v_pk_mul_f32 v[92:93], v[118:119], v[92:93] op_sel:[1,0]
	v_pk_mul_f32 v[90:91], v[118:119], v[90:91] op_sel:[1,0]
	v_cvt_pk_f16_f32 v93, v92, v93
	v_cvt_pk_f16_f32 v92, v90, v91
	v_add_u32_e32 v90, v102, v106
	ds_write_b64 v90, v[92:93]
	v_mov_b32_e32 v90, 0x6300
	v_pk_fma_f32 v[84:85], v[116:117], v[122:123], v[84:85] op_sel_hi:[0,1,1]
	v_pk_fma_f32 v[82:83], v[116:117], v[120:121], v[82:83] op_sel_hi:[0,1,1]
	v_pk_fma_f32 v[110:111], v[124:125], v[44:45], v[150:151] op_sel_hi:[0,1,1]
	v_pk_fma_f32 v[112:113], v[124:125], v[42:43], v[148:149] op_sel_hi:[0,1,1]
	v_mad_u32_u24 v90, v1, s4, v90
	v_pk_mul_f32 v[84:85], v[116:117], v[84:85] op_sel:[1,0]
	v_pk_mul_f32 v[82:83], v[116:117], v[82:83] op_sel:[1,0]
	v_pk_mul_f32 v[110:111], v[124:125], v[110:111] op_sel:[1,0]
	v_pk_mul_f32 v[112:113], v[124:125], v[112:113] op_sel:[1,0]
	v_cvt_pk_f16_f32 v85, v84, v85
	v_cvt_pk_f16_f32 v84, v82, v83
	v_add_u32_e32 v82, v90, v106
	v_cvt_pk_f16_f32 v111, v110, v111
	v_cvt_pk_f16_f32 v110, v112, v113
	v_mad_u32_u24 v112, v1, s4, v129
	ds_write_b64 v82, v[84:85]
	v_or_b32_e32 v82, 0x1f000, v114
	ds_write_b64 v112, v[110:111]
	ds_read_b128 v[110:113], v128
	ds_read_b64 v[82:83], v82
	v_pk_fma_f32 v[94:95], v[118:119], v[44:45], v[100:101] op_sel_hi:[0,1,1]
	v_pk_fma_f32 v[96:97], v[118:119], v[42:43], v[98:99] op_sel_hi:[0,1,1]
	v_pk_fma_f32 v[88:89], v[116:117], v[44:45], v[88:89] op_sel_hi:[0,1,1]
	v_pk_fma_f32 v[86:87], v[116:117], v[42:43], v[86:87] op_sel_hi:[0,1,1]
	v_pk_mul_f32 v[94:95], v[118:119], v[94:95] op_sel:[1,0]
	v_pk_mul_f32 v[96:97], v[118:119], v[96:97] op_sel:[1,0]
	v_pk_mul_f32 v[88:89], v[116:117], v[88:89] op_sel:[1,0]
	v_pk_mul_f32 v[86:87], v[116:117], v[86:87] op_sel:[1,0]
	v_mov_b32_e32 v84, 0x8400
	s_waitcnt lgkmcnt(0)
	v_pk_fma_f32 v[44:45], v[82:83], v[44:45], v[80:81] op_sel_hi:[0,1,1]
	v_pk_fma_f32 v[42:43], v[82:83], v[42:43], v[78:79] op_sel_hi:[0,1,1]
	v_cvt_pk_f16_f32 v95, v94, v95
	v_cvt_pk_f16_f32 v94, v96, v97
	v_add_u32_e32 v96, v102, v129
	v_cvt_pk_f16_f32 v89, v88, v89
	v_cvt_pk_f16_f32 v88, v86, v87
	v_add_u32_e32 v86, v90, v129
	v_mad_u32_u24 v90, v1, s4, v84
	v_pk_mul_f32 v[44:45], v[82:83], v[44:45] op_sel:[1,0]
	v_pk_mul_f32 v[42:43], v[82:83], v[42:43] op_sel:[1,0]
	ds_write_b64 v96, v[94:95]
	ds_write_b64 v86, v[88:89]
	v_or_b32_e32 v84, 0x1f080, v114
	v_or_b32_e32 v86, 0x1f100, v114
	v_or_b32_e32 v88, 0x1f180, v114
	v_cvt_pk_f16_f32 v45, v44, v45
	v_cvt_pk_f16_f32 v44, v42, v43
	v_add_u32_e32 v42, v90, v129
	ds_read_b64 v[84:85], v84
	ds_read_b64 v[86:87], v86
	ds_read_b64 v[88:89], v88
	ds_write_b64 v42, v[44:45]
	v_pk_fma_f32 v[42:43], v[82:83], v[122:123], v[76:77] op_sel_hi:[0,1,1]
	v_pk_fma_f32 v[44:45], v[82:83], v[120:121], v[74:75] op_sel_hi:[0,1,1]
	v_pk_mul_f32 v[42:43], v[82:83], v[42:43] op_sel:[1,0]
	v_pk_mul_f32 v[44:45], v[82:83], v[44:45] op_sel:[1,0]
	v_cvt_pk_f16_f32 v43, v42, v43
	v_cvt_pk_f16_f32 v42, v44, v45
	v_add_u32_e32 v44, v90, v106
	ds_write_b64 v44, v[42:43]
	v_mov_b32_e32 v42, 0xa500
	v_mad_u32_u24 v74, v1, s4, v42
	s_waitcnt lgkmcnt(4)
	v_pk_fma_f32 v[42:43], v[84:85], v[48:49], v[72:73] op_sel_hi:[0,1,1]
	v_pk_fma_f32 v[44:45], v[84:85], v[46:47], v[70:71] op_sel_hi:[0,1,1]
	v_pk_mul_f32 v[42:43], v[84:85], v[42:43] op_sel:[1,0]
	v_pk_mul_f32 v[70:71], v[84:85], v[44:45] op_sel:[1,0]
	v_cvt_pk_f16_f32 v73, v42, v43
	ds_read_b128 v[42:45], v128 offset:64
	v_cvt_pk_f16_f32 v72, v70, v71
	v_add_u32_e32 v70, v74, v129
	ds_write_b64 v70, v[72:73]
	ds_read_b128 v[70:73], v128 offset:64
	s_waitcnt lgkmcnt(2)
	v_pk_fma_f32 v[64:65], v[84:85], v[44:45], v[64:65] op_sel_hi:[0,1,1]
	v_pk_fma_f32 v[62:63], v[84:85], v[42:43], v[62:63] op_sel_hi:[0,1,1]
	v_pk_mul_f32 v[64:65], v[84:85], v[64:65] op_sel:[1,0]
	v_pk_mul_f32 v[62:63], v[84:85], v[62:63] op_sel:[1,0]
	v_cvt_pk_f16_f32 v65, v64, v65
	v_cvt_pk_f16_f32 v64, v62, v63
	v_add_u32_e32 v62, v74, v106
	ds_write_b64 v62, v[64:65]
	v_mov_b32_e32 v62, 0xc600
	v_pk_fma_f32 v[60:61], v[86:87], v[44:45], v[60:61] op_sel_hi:[0,1,1]
	v_pk_fma_f32 v[58:59], v[86:87], v[42:43], v[58:59] op_sel_hi:[0,1,1]
	v_mad_u32_u24 v74, v1, s4, v62
	v_pk_mul_f32 v[60:61], v[86:87], v[60:61] op_sel:[1,0]
	v_pk_mul_f32 v[58:59], v[86:87], v[58:59] op_sel:[1,0]
	v_cvt_pk_f16_f32 v61, v60, v61
	v_cvt_pk_f16_f32 v60, v58, v59
	v_add_u32_e32 v58, v74, v106
	ds_write_b64 v58, v[60:61]
	v_mov_b32_e32 v58, 0xe700
	v_pk_fma_f32 v[52:53], v[88:89], v[44:45], v[52:53] op_sel_hi:[0,1,1]
	v_pk_fma_f32 v[50:51], v[88:89], v[42:43], v[50:51] op_sel_hi:[0,1,1]
	v_mad_u32_u24 v58, v1, s4, v58
	v_pk_mul_f32 v[52:53], v[88:89], v[52:53] op_sel:[1,0]
	v_pk_mul_f32 v[50:51], v[88:89], v[50:51] op_sel:[1,0]
	v_cvt_pk_f16_f32 v53, v52, v53
	v_cvt_pk_f16_f32 v52, v50, v51
	v_add_u32_e32 v50, v58, v106
	ds_write_b64 v50, v[52:53]
	v_or_b32_e32 v50, 0x1f200, v114
	ds_read_b64 v[50:51], v50
	v_pk_fma_f32 v[62:63], v[86:87], v[48:49], v[68:69] op_sel_hi:[0,1,1]
	v_pk_fma_f32 v[64:65], v[86:87], v[46:47], v[66:67] op_sel_hi:[0,1,1]
	v_pk_fma_f32 v[56:57], v[88:89], v[48:49], v[56:57] op_sel_hi:[0,1,1]
	v_pk_fma_f32 v[54:55], v[88:89], v[46:47], v[54:55] op_sel_hi:[0,1,1]
	v_pk_mul_f32 v[62:63], v[86:87], v[62:63] op_sel:[1,0]
	v_pk_mul_f32 v[64:65], v[86:87], v[64:65] op_sel:[1,0]
	v_pk_mul_f32 v[56:57], v[88:89], v[56:57] op_sel:[1,0]
	v_pk_mul_f32 v[54:55], v[88:89], v[54:55] op_sel:[1,0]
	v_cvt_pk_f16_f32 v63, v62, v63
	v_cvt_pk_f16_f32 v62, v64, v65
	v_add_u32_e32 v64, v74, v129
	v_cvt_pk_f16_f32 v57, v56, v57
	v_cvt_pk_f16_f32 v56, v54, v55
	v_add_u32_e32 v54, v58, v129
	v_mov_b32_e32 v52, 0x10800
	ds_write_b64 v64, v[62:63]
	ds_write_b64 v54, v[56:57]
	v_mad_u32_u24 v58, v1, s4, v52
	v_or_b32_e32 v52, 0x1f280, v114
	v_or_b32_e32 v54, 0x1f300, v114
	v_or_b32_e32 v56, 0x1f380, v114
	ds_read_b64 v[52:53], v52
	ds_read_b64 v[54:55], v54
	ds_read_b64 v[56:57], v56
	s_waitcnt lgkmcnt(5)
	v_pk_fma_f32 v[36:37], v[50:51], v[44:45], v[36:37] op_sel_hi:[0,1,1]
	v_pk_fma_f32 v[34:35], v[50:51], v[42:43], v[34:35] op_sel_hi:[0,1,1]
	v_pk_mul_f32 v[36:37], v[50:51], v[36:37] op_sel:[1,0]
	v_pk_mul_f32 v[34:35], v[50:51], v[34:35] op_sel:[1,0]
	v_cvt_pk_f16_f32 v37, v36, v37
	v_cvt_pk_f16_f32 v36, v34, v35
	v_add_u32_e32 v34, v58, v106
	v_pk_fma_f32 v[40:41], v[50:51], v[48:49], v[40:41] op_sel_hi:[0,1,1]
	v_pk_fma_f32 v[38:39], v[50:51], v[46:47], v[38:39] op_sel_hi:[0,1,1]
	ds_write_b64 v34, v[36:37]
	v_mov_b32_e32 v34, 0x12900
	s_waitcnt lgkmcnt(3)
	v_pk_fma_f32 v[20:21], v[52:53], v[44:45], v[20:21] op_sel_hi:[0,1,1]
	v_pk_fma_f32 v[18:19], v[52:53], v[42:43], v[18:19] op_sel_hi:[0,1,1]
	v_pk_mul_f32 v[40:41], v[50:51], v[40:41] op_sel:[1,0]
	v_pk_mul_f32 v[38:39], v[50:51], v[38:39] op_sel:[1,0]
	v_mad_u32_u24 v34, v1, s4, v34
	v_pk_fma_f32 v[32:33], v[52:53], v[48:49], v[32:33] op_sel_hi:[0,1,1]
	v_pk_fma_f32 v[30:31], v[52:53], v[46:47], v[30:31] op_sel_hi:[0,1,1]
	v_pk_mul_f32 v[20:21], v[52:53], v[20:21] op_sel:[1,0]
	v_pk_mul_f32 v[18:19], v[52:53], v[18:19] op_sel:[1,0]
	v_cvt_pk_f16_f32 v41, v40, v41
	v_cvt_pk_f16_f32 v40, v38, v39
	v_add_u32_e32 v38, v58, v129
	v_pk_mul_f32 v[32:33], v[52:53], v[32:33] op_sel:[1,0]
	v_pk_mul_f32 v[30:31], v[52:53], v[30:31] op_sel:[1,0]
	v_cvt_pk_f16_f32 v21, v20, v21
	v_cvt_pk_f16_f32 v20, v18, v19
	v_add_u32_e32 v18, v34, v106
	ds_write_b64 v38, v[40:41]
	v_cvt_pk_f16_f32 v33, v32, v33
	v_cvt_pk_f16_f32 v32, v30, v31
	v_add_u32_e32 v30, v34, v129
	ds_write_b64 v18, v[20:21]
	v_mov_b32_e32 v18, 0x14a00
	ds_write_b64 v30, v[32:33]
	v_mad_u32_u24 v30, v1, s4, v18
	s_waitcnt lgkmcnt(5)
	v_pk_fma_f32 v[18:19], v[54:55], v[112:113], v[24:25] op_sel_hi:[0,1,1]
	v_pk_fma_f32 v[20:21], v[54:55], v[110:111], v[22:23] op_sel_hi:[0,1,1]
	v_pk_mul_f32 v[18:19], v[54:55], v[18:19] op_sel:[1,0]
	v_pk_mul_f32 v[20:21], v[54:55], v[20:21] op_sel:[1,0]
	v_cvt_pk_f16_f32 v19, v18, v19
	v_cvt_pk_f16_f32 v18, v20, v21
	v_add_u32_e32 v20, v30, v129
	s_waitcnt lgkmcnt(4)
	v_pk_fma_f32 v[12:13], v[56:57], v[72:73], v[12:13] op_sel_hi:[0,1,1]
	v_pk_fma_f32 v[10:11], v[56:57], v[70:71], v[10:11] op_sel_hi:[0,1,1]
	ds_write_b64 v20, v[18:19]
	v_pk_fma_f32 v[18:19], v[54:55], v[72:73], v[28:29] op_sel_hi:[0,1,1]
	v_pk_fma_f32 v[20:21], v[54:55], v[70:71], v[26:27] op_sel_hi:[0,1,1]
	v_pk_mul_f32 v[12:13], v[56:57], v[12:13] op_sel:[1,0]
	v_pk_mul_f32 v[10:11], v[56:57], v[10:11] op_sel:[1,0]
	v_pk_mul_f32 v[18:19], v[54:55], v[18:19] op_sel:[1,0]
	v_pk_mul_f32 v[20:21], v[54:55], v[20:21] op_sel:[1,0]
	v_cvt_pk_f16_f32 v13, v12, v13
	v_cvt_pk_f16_f32 v12, v10, v11
	v_or_b32_e32 v10, 0x1f400, v114
	v_cvt_pk_f16_f32 v19, v18, v19
	v_cvt_pk_f16_f32 v18, v20, v21
	v_add_u32_e32 v20, v30, v106
	ds_read_b64 v[10:11], v10
	ds_write_b64 v20, v[18:19]
	v_mov_b32_e32 v18, 0x16b00
	v_pk_fma_f32 v[16:17], v[56:57], v[112:113], v[16:17] op_sel_hi:[0,1,1]
	v_pk_fma_f32 v[14:15], v[56:57], v[110:111], v[14:15] op_sel_hi:[0,1,1]
	v_mad_u32_u24 v18, v1, s4, v18
	v_pk_mul_f32 v[16:17], v[56:57], v[16:17] op_sel:[1,0]
	v_pk_mul_f32 v[14:15], v[56:57], v[14:15] op_sel:[1,0]
	v_cvt_pk_f16_f32 v17, v16, v17
	v_cvt_pk_f16_f32 v16, v14, v15
	v_add_u32_e32 v14, v18, v129
	ds_write_b64 v14, v[16:17]
	v_add_u32_e32 v14, v18, v106
	ds_write_b64 v14, v[12:13]
	v_mov_b32_e32 v12, 0x18c00
	s_waitcnt lgkmcnt(3)
	v_pk_fma_f32 v[8:9], v[10:11], v[112:113], v[8:9] op_sel_hi:[0,1,1]
	v_pk_fma_f32 v[6:7], v[10:11], v[110:111], v[6:7] op_sel_hi:[0,1,1]
	v_pk_fma_f32 v[4:5], v[10:11], v[72:73], v[4:5] op_sel_hi:[0,1,1]
	v_pk_fma_f32 v[2:3], v[10:11], v[70:71], v[2:3] op_sel_hi:[0,1,1]
	v_mad_u32_u24 v1, v1, s4, v12
	v_pk_mul_f32 v[8:9], v[10:11], v[8:9] op_sel:[1,0]
	v_pk_mul_f32 v[6:7], v[10:11], v[6:7] op_sel:[1,0]
	v_pk_mul_f32 v[4:5], v[10:11], v[4:5] op_sel:[1,0]
	v_pk_mul_f32 v[2:3], v[10:11], v[2:3] op_sel:[1,0]
	v_cvt_pk_f16_f32 v9, v8, v9
	v_cvt_pk_f16_f32 v8, v6, v7
	v_add_u32_e32 v6, v1, v129
	v_cvt_pk_f16_f32 v5, v4, v5
	v_cvt_pk_f16_f32 v4, v2, v3
	v_add_u32_e32 v1, v1, v106
	ds_write_b64 v6, v[8:9]
	ds_write_b64 v1, v[4:5]
	s_waitcnt lgkmcnt(0)
	s_barrier
	s_and_saveexec_b64 s[0:1], vcc
	s_cbranch_execz .LBB2_12
	v_lshlrev_b32_e32 v1, 4, v0
	v_and_b32_e32 v114, 0x70, v1
	v_lshl_add_u64 v[2:3], s[6:7], 0, v[114:115]
	s_mov_b64 s[0:1], 0
	s_mov_b32 s5, 0x5397829d
	s_movk_i32 s6, 0xf9e0
	s_mov_b32 s7, 0xc350
	s_movk_i32 s8, 0x167f
	s_branch .LBB2_10

.LBB2_10:
	v_mul_hi_i32 v1, v0, s5
	v_lshrrev_b32_e32 v4, 31, v1
	v_ashrrev_i32_e32 v1, 9, v1
	v_add_u32_e32 v1, v1, v4
	v_mad_i32_i24 v4, v1, s6, v0
	v_ashrrev_i32_e32 v5, 3, v4
	v_add_u32_e32 v4, s14, v5
	v_cmp_gt_i32_e32 vcc, s7, v4
	s_and_saveexec_b64 s[2:3], vcc
	s_cbranch_execz .LBB2_9
	v_mul_lo_u32 v5, v5, s4
	v_lshlrev_b32_e32 v6, 7, v1
	v_add3_u32 v5, v5, v6, v114
	ds_read_b128 v[6:9], v5
	v_mul_hi_i32_i24_e32 v11, 0xc351, v1
	v_mul_i32_i24_e32 v10, 0xc351, v1
	v_ashrrev_i32_e32 v5, 31, v4
	v_lshl_add_u64 v[4:5], v[10:11], 0, v[4:5]
	v_lshlrev_b64 v[4:5], 7, v[4:5]
	v_lshl_add_u64 v[4:5], v[2:3], 0, v[4:5]
	s_waitcnt lgkmcnt(0)
	global_store_dwordx4 v[4:5], v[6:9], off sc1
	s_branch .LBB2_9
